# v85 + sc1 on the 128 u-code gather loads of the P12 dot-product loop (no L1 reuse: each 128 B row piece is used once)
# baseline (speedup 1.0000x reference)
; #define P12_ISSUE(c_, i_, h_, CW_, SC_) do { _Pragma("unroll") for (int bb = 0; bb < 8; ++bb) { const unsigned ro = (unsigned)(c_) * 16384u + (unsigned)EL[(i_) * 128 + ((h_) * 8 + bb) * 8 + g8]; \
;         CW_[bb] = *(const v4u*)(U4 + (size_t)(ro * 128u + 16u * (unsigned)k8)); SC_[bb] = USS[(size_t)(ro * 8u + (unsigned)k8)]; } } while (0)
; #define P12_COMP(i_, h_, CW_, SC_) do { _Pragma("unroll") for (int bb = 0; bb < 8; ++bb) { int a0 = 0, a1 = 0; P12_U4(CW_[bb].x, xa.x, xa.y, a0); P12_U4(CW_[bb].y, xa.z, xa.w, a1); P12_U4(CW_[bb].z, xb.x, xb.y, a0); P12_U4(CW_[bb].w, xb.z, xb.w, a1); \
;         psum[(i_)][(h_) * 8 + bb] += __uint_as_float(SC_[bb] << 16) * (float)((a0 + a1) - xo); } } while (0)
; #define P12_BAR() asm volatile("" ::: "memory")
; __device__ __forceinline__ void p12_peer(Frame& F) {
;     ...
;     { v4u cwA[8], cwB[8]; unsigned scA[8], scB[8]; v4u xa, xb; int xo;
;       P12_ISSUE(0, 0, 0, cwA, scA);
; _Pragma("nounroll")
;       for (int c = 0; c < 16; ++c) { const int cn = c + 1 < 16 ? c + 1 : 15;
;           P12_XQ(c, 0); P12_ISSUE(c, 0, 1, cwB, scB); P12_BAR(); P12_COMP(0, 0, cwA, scA); P12_ISSUE(c, 1, 0, cwA, scA); P12_BAR(); P12_COMP(0, 1, cwB, scB);
;           P12_XQ(c, 1); P12_ISSUE(c, 1, 1, cwB, scB); P12_BAR(); P12_COMP(1, 0, cwA, scA); P12_ISSUE(c, 2, 0, cwA, scA); P12_BAR(); P12_COMP(1, 1, cwB, scB);
;           P12_XQ(c, 2); P12_ISSUE(c, 2, 1, cwB, scB); P12_BAR(); P12_COMP(2, 0, cwA, scA); P12_ISSUE(c, 3, 0, cwA, scA); P12_BAR(); P12_COMP(2, 1, cwB, scB);
;           P12_XQ(c, 3); P12_ISSUE(c, 3, 1, cwB, scB); P12_BAR(); P12_COMP(3, 0, cwA, scA); P12_ISSUE(cn, 0, 0, cwA, scA); P12_BAR(); P12_COMP(3, 1, cwB, scB);
.LBB0_3272:
	s_lshl_b32 s49, s44, 4
	s_sub_u32 s46, s18, s49
	s_subb_u32 s47, s19, 0
	ds_read_b128 v[36:39], v166
	ds_read_b128 v[32:35], v166 offset:16
	ds_read_u16 v44, v93 offset:16512
	ds_read_u16 v45, v93 offset:16528
	ds_read_u16 v46, v93 offset:16544
	ds_read_u16 v47, v93 offset:16560
	v_mov_b32_e32 v48, 0
	s_waitcnt lgkmcnt(3)
	v_add_u32_e32 v44, s44, v44
	v_lshl_or_b32 v49, v44, 7, v165
	global_load_dwordx4 v[88:91], v49, s[0:1] sc1
	v_lshl_or_b32 v49, v44, 5, v248
	s_waitcnt lgkmcnt(2)
	v_add_u32_e32 v44, s44, v45
	v_lshl_or_b32 v45, v44, 7, v165
	v_lshl_or_b32 v50, v44, 5, v248
	s_waitcnt lgkmcnt(1)
	v_add_u32_e32 v44, s44, v46
	global_load_dwordx4 v[84:87], v45, s[0:1] sc1
	v_lshl_or_b32 v45, v44, 7, v165
	v_lshl_or_b32 v51, v44, 5, v248
	s_waitcnt lgkmcnt(0)
	v_add_u32_e32 v44, s44, v47
	global_load_dwordx4 v[80:83], v45, s[0:1] sc1
	v_lshl_or_b32 v45, v44, 7, v165
	v_lshl_or_b32 v56, v44, 5, v248
	ds_read_u16 v44, v93 offset:16576
	global_load_dwordx4 v[76:79], v45, s[0:1] sc1
	v_dot4c_i32_i8_e32 v48, 0x1010101, v36
	v_dot4c_i32_i8_e32 v48, 0x1010101, v37
	v_dot4c_i32_i8_e32 v48, 0x1010101, v38
	s_waitcnt lgkmcnt(0)
	v_add_u32_e32 v44, s44, v44
	v_lshl_or_b32 v45, v44, 7, v165
	v_lshl_or_b32 v57, v44, 5, v248
	ds_read_u16 v44, v93 offset:16592
	global_load_dwordx4 v[68:71], v45, s[0:1] sc1
	v_dot4c_i32_i8_e32 v48, 0x1010101, v39
	v_dot4c_i32_i8_e32 v48, 0x1010101, v32
	v_dot4c_i32_i8_e32 v48, 0x1010101, v33
	s_waitcnt lgkmcnt(0)
	v_add_u32_e32 v44, s44, v44
	v_lshl_or_b32 v45, v44, 7, v165
	v_lshl_or_b32 v58, v44, 5, v248
	ds_read_u16 v44, v93 offset:16608
	global_load_dwordx4 v[60:63], v45, s[0:1] sc1
	v_dot4c_i32_i8_e32 v48, 0x1010101, v34
	v_dot4c_i32_i8_e32 v48, 0x1010101, v35
	s_add_i32 s45, s44, 0x4000
	s_waitcnt lgkmcnt(0)
	v_add_u32_e32 v44, s44, v44
	v_lshl_or_b32 v45, v44, 7, v165
	v_lshl_or_b32 v59, v44, 5, v248
	ds_read_u16 v44, v93 offset:16624
	global_load_dwordx4 v[52:55], v45, s[0:1] sc1
	v_lshlrev_b32_e32 v171, 3, v48
	s_waitcnt vmcnt(14)
	v_and_b32_e32 v48, 0xf0f0f0f, v28
	v_lshrrev_b32_e32 v28, 4, v28
	s_waitcnt lgkmcnt(0)
	v_add_u32_e32 v64, s44, v44
	v_lshl_or_b32 v44, v64, 7, v165
	global_load_dwordx4 v[44:47], v44, s[0:1] sc1
	v_lshl_or_b32 v64, v64, 5, v248
	global_load_dword v193, v50, s[46:47]
	global_load_dword v192, v49, s[46:47]
	global_load_dword v195, v56, s[46:47]
	global_load_dword v194, v51, s[46:47]
	global_load_dword v197, v58, s[46:47]
	global_load_dword v196, v57, s[46:47]
	global_load_dword v199, v64, s[46:47]
	global_load_dword v198, v59, s[46:47]
	v_mov_b32_e32 v49, 0
	v_dot4c_i32_i8_e32 v49, v48, v36
	v_and_b32_e32 v28, 0xf0f0f0f, v28
	v_dot4c_i32_i8_e32 v49, v28, v37
	v_and_b32_e32 v28, 0xf0f0f0f, v29
	v_mov_b32_e32 v48, 0
	v_dot4c_i32_i8_e32 v48, v28, v38
	v_lshrrev_b32_e32 v28, 4, v29
	v_and_b32_e32 v28, 0xf0f0f0f, v28
	v_dot4c_i32_i8_e32 v48, v28, v39
	v_and_b32_e32 v28, 0xf0f0f0f, v30
	v_dot4c_i32_i8_e32 v49, v28, v32
	v_lshrrev_b32_e32 v28, 4, v30
	v_and_b32_e32 v28, 0xf0f0f0f, v28
	v_dot4c_i32_i8_e32 v49, v28, v33
	v_and_b32_e32 v28, 0xf0f0f0f, v31
	v_dot4c_i32_i8_e32 v48, v28, v34
	v_lshrrev_b32_e32 v28, 4, v31
	v_and_b32_e32 v28, 0xf0f0f0f, v28
	v_dot4c_i32_i8_e32 v48, v28, v35
	s_waitcnt vmcnt(22)
	v_and_b32_e32 v28, 0xf0f0f0f, v24
	v_mov_b32_e32 v29, 0
	v_lshrrev_b32_e32 v24, 4, v24
	v_dot4c_i32_i8_e32 v29, v28, v36
	v_and_b32_e32 v24, 0xf0f0f0f, v24
	v_dot4c_i32_i8_e32 v29, v24, v37
	v_and_b32_e32 v24, 0xf0f0f0f, v25
	v_mov_b32_e32 v28, 0
	v_dot4c_i32_i8_e32 v28, v24, v38
	v_lshrrev_b32_e32 v24, 4, v25
	v_and_b32_e32 v24, 0xf0f0f0f, v24
	v_dot4c_i32_i8_e32 v28, v24, v39
	v_and_b32_e32 v24, 0xf0f0f0f, v26
	v_dot4c_i32_i8_e32 v29, v24, v32
	v_lshrrev_b32_e32 v24, 4, v26
	v_and_b32_e32 v24, 0xf0f0f0f, v24
	v_dot4c_i32_i8_e32 v29, v24, v33
	v_and_b32_e32 v24, 0xf0f0f0f, v27
	v_dot4c_i32_i8_e32 v28, v24, v34
	v_lshrrev_b32_e32 v24, 4, v27
	v_and_b32_e32 v24, 0xf0f0f0f, v24
	v_dot4c_i32_i8_e32 v28, v24, v35
	v_add_u32_e32 v26, v49, v48
	v_sub_u32_e32 v26, v26, v171
	v_and_b32_e32 v25, 0xffff0000, v43
	v_add_u32_e32 v27, v29, v28
	v_sub_u32_e32 v28, v27, v171
	v_cvt_f32_i32_e32 v27, v26
	v_cvt_f32_i32_e32 v26, v28
	v_lshlrev_b32_e32 v24, 16, v43
	s_cmp_eq_u32 s44, 0x3c000
	v_pk_fma_f32 v[158:159], v[24:25], v[26:27], v[158:159]
	s_waitcnt vmcnt(21)
	v_and_b32_e32 v24, 0xf0f0f0f, v20
	v_mov_b32_e32 v25, 0
	v_lshrrev_b32_e32 v20, 4, v20
	v_dot4c_i32_i8_e32 v25, v24, v36
	v_and_b32_e32 v20, 0xf0f0f0f, v20
	v_dot4c_i32_i8_e32 v25, v20, v37
	v_and_b32_e32 v20, 0xf0f0f0f, v21
	v_mov_b32_e32 v24, 0
	v_dot4c_i32_i8_e32 v24, v20, v38
	v_lshrrev_b32_e32 v20, 4, v21
	v_and_b32_e32 v20, 0xf0f0f0f, v20
	v_dot4c_i32_i8_e32 v24, v20, v39
	v_and_b32_e32 v20, 0xf0f0f0f, v22
	v_dot4c_i32_i8_e32 v25, v20, v32
	v_lshrrev_b32_e32 v20, 4, v22
	v_and_b32_e32 v20, 0xf0f0f0f, v20
	v_dot4c_i32_i8_e32 v25, v20, v33
	v_and_b32_e32 v20, 0xf0f0f0f, v23
	v_dot4c_i32_i8_e32 v24, v20, v34
	v_lshrrev_b32_e32 v20, 4, v23
	v_and_b32_e32 v20, 0xf0f0f0f, v20
	v_dot4c_i32_i8_e32 v24, v20, v35
	s_waitcnt vmcnt(20)
	v_and_b32_e32 v20, 0xf0f0f0f, v16
	v_mov_b32_e32 v21, 0
	v_lshrrev_b32_e32 v16, 4, v16
	v_dot4c_i32_i8_e32 v21, v20, v36
	v_and_b32_e32 v16, 0xf0f0f0f, v16
	v_dot4c_i32_i8_e32 v21, v16, v37
	v_and_b32_e32 v16, 0xf0f0f0f, v17
	v_mov_b32_e32 v20, 0
	v_dot4c_i32_i8_e32 v20, v16, v38
	v_lshrrev_b32_e32 v16, 4, v17
	v_and_b32_e32 v16, 0xf0f0f0f, v16
	v_dot4c_i32_i8_e32 v20, v16, v39
	v_and_b32_e32 v16, 0xf0f0f0f, v18
	v_dot4c_i32_i8_e32 v21, v16, v32
	v_lshrrev_b32_e32 v16, 4, v18
	v_and_b32_e32 v16, 0xf0f0f0f, v16
	v_dot4c_i32_i8_e32 v21, v16, v33
	v_and_b32_e32 v16, 0xf0f0f0f, v19
	v_dot4c_i32_i8_e32 v20, v16, v34
	v_lshrrev_b32_e32 v16, 4, v19
	v_and_b32_e32 v16, 0xf0f0f0f, v16
	v_dot4c_i32_i8_e32 v20, v16, v35
	v_add_u32_e32 v18, v25, v24
	v_sub_u32_e32 v18, v18, v171
	v_and_b32_e32 v17, 0xffff0000, v42
	v_add_u32_e32 v19, v21, v20
	v_sub_u32_e32 v20, v19, v171
	v_cvt_f32_i32_e32 v19, v18
	v_cvt_f32_i32_e32 v18, v20
	v_lshlrev_b32_e32 v16, 16, v42
	v_pk_fma_f32 v[156:157], v[16:17], v[18:19], v[156:157]
	s_waitcnt vmcnt(19)
; #define P12_ISSUE(c_, i_, h_, CW_, SC_) do { _Pragma("unroll") for (int bb = 0; bb < 8; ++bb) { const unsigned ro = (unsigned)(c_) * 16384u + (unsigned)EL[(i_) * 128 + ((h_) * 8 + bb) * 8 + g8]; \
;         CW_[bb] = *(const v4u*)(U4 + (size_t)(ro * 128u + 16u * (unsigned)k8)); SC_[bb] = USS[(size_t)(ro * 8u + (unsigned)k8)]; } } while (0)
; #define P12_COMP(i_, h_, CW_, SC_) do { _Pragma("unroll") for (int bb = 0; bb < 8; ++bb) { int a0 = 0, a1 = 0; P12_U4(CW_[bb].x, xa.x, xa.y, a0); P12_U4(CW_[bb].y, xa.z, xa.w, a1); P12_U4(CW_[bb].z, xb.x, xb.y, a0); P12_U4(CW_[bb].w, xb.z, xb.w, a1); \
;         psum[(i_)][(h_) * 8 + bb] += __uint_as_float(SC_[bb] << 16) * (float)((a0 + a1) - xo); } } while (0)
; #define P12_BAR() asm volatile("" ::: "memory")
; __device__ __forceinline__ void p12_peer(Frame& F) {
;     ...
;     { v4u cwA[8], cwB[8]; unsigned scA[8], scB[8]; v4u xa, xb; int xo;
;       P12_ISSUE(0, 0, 0, cwA, scA);
; _Pragma("nounroll")
;       for (int c = 0; c < 16; ++c) { const int cn = c + 1 < 16 ? c + 1 : 15;
;           P12_XQ(c, 0); P12_ISSUE(c, 0, 1, cwB, scB); P12_BAR(); P12_COMP(0, 0, cwA, scA); P12_ISSUE(c, 1, 0, cwA, scA); P12_BAR(); P12_COMP(0, 1, cwB, scB);
;           P12_XQ(c, 1); P12_ISSUE(c, 1, 1, cwB, scB); P12_BAR(); P12_COMP(1, 0, cwA, scA); P12_ISSUE(c, 2, 0, cwA, scA); P12_BAR(); P12_COMP(1, 1, cwB, scB);
;           P12_XQ(c, 2); P12_ISSUE(c, 2, 1, cwB, scB); P12_BAR(); P12_COMP(2, 0, cwA, scA); P12_ISSUE(c, 3, 0, cwA, scA); P12_BAR(); P12_COMP(2, 1, cwB, scB);
;           P12_XQ(c, 3); P12_ISSUE(c, 3, 1, cwB, scB); P12_BAR(); P12_COMP(3, 0, cwA, scA); P12_ISSUE(cn, 0, 0, cwA, scA); P12_BAR(); P12_COMP(3, 1, cwB, scB);
;       } }
	v_and_b32_e32 v16, 0xf0f0f0f, v12
	v_mov_b32_e32 v17, 0
	v_lshrrev_b32_e32 v12, 4, v12
	v_dot4c_i32_i8_e32 v17, v16, v36
	v_and_b32_e32 v12, 0xf0f0f0f, v12
	v_dot4c_i32_i8_e32 v17, v12, v37
	v_and_b32_e32 v12, 0xf0f0f0f, v13
	v_mov_b32_e32 v16, 0
	v_dot4c_i32_i8_e32 v16, v12, v38
	v_lshrrev_b32_e32 v12, 4, v13
	v_and_b32_e32 v12, 0xf0f0f0f, v12
	v_dot4c_i32_i8_e32 v16, v12, v39
	v_and_b32_e32 v12, 0xf0f0f0f, v14
	v_dot4c_i32_i8_e32 v17, v12, v32
	v_lshrrev_b32_e32 v12, 4, v14
	v_and_b32_e32 v12, 0xf0f0f0f, v12
	v_dot4c_i32_i8_e32 v17, v12, v33
	v_and_b32_e32 v12, 0xf0f0f0f, v15
	v_dot4c_i32_i8_e32 v16, v12, v34
	v_lshrrev_b32_e32 v12, 4, v15
	v_and_b32_e32 v12, 0xf0f0f0f, v12
	v_dot4c_i32_i8_e32 v16, v12, v35
	s_waitcnt vmcnt(18)
	v_and_b32_e32 v12, 0xf0f0f0f, v8
	v_mov_b32_e32 v13, 0
	v_lshrrev_b32_e32 v8, 4, v8
	v_dot4c_i32_i8_e32 v13, v12, v36
	v_and_b32_e32 v8, 0xf0f0f0f, v8
	v_dot4c_i32_i8_e32 v13, v8, v37
	v_and_b32_e32 v8, 0xf0f0f0f, v9
	v_mov_b32_e32 v12, 0
	v_dot4c_i32_i8_e32 v12, v8, v38
	v_lshrrev_b32_e32 v8, 4, v9
	v_and_b32_e32 v8, 0xf0f0f0f, v8
	v_dot4c_i32_i8_e32 v12, v8, v39
	v_and_b32_e32 v8, 0xf0f0f0f, v10
	v_dot4c_i32_i8_e32 v13, v8, v32
	v_lshrrev_b32_e32 v8, 4, v10
	v_and_b32_e32 v8, 0xf0f0f0f, v8
	v_dot4c_i32_i8_e32 v13, v8, v33
	v_and_b32_e32 v8, 0xf0f0f0f, v11
	v_dot4c_i32_i8_e32 v12, v8, v34
	v_lshrrev_b32_e32 v8, 4, v11
	v_and_b32_e32 v8, 0xf0f0f0f, v8
	v_dot4c_i32_i8_e32 v12, v8, v35
	v_add_u32_e32 v10, v17, v16
	v_sub_u32_e32 v10, v10, v171
	v_and_b32_e32 v9, 0xffff0000, v41
	v_add_u32_e32 v11, v13, v12
	v_sub_u32_e32 v12, v11, v171
	v_cvt_f32_i32_e32 v11, v10
	v_cvt_f32_i32_e32 v10, v12
	v_lshlrev_b32_e32 v8, 16, v41
	v_pk_fma_f32 v[154:155], v[8:9], v[10:11], v[154:155]
	s_waitcnt vmcnt(17)
	v_and_b32_e32 v8, 0xf0f0f0f, v4
	v_mov_b32_e32 v9, 0
	v_lshrrev_b32_e32 v4, 4, v4
	v_dot4c_i32_i8_e32 v9, v8, v36
	v_and_b32_e32 v4, 0xf0f0f0f, v4
	v_dot4c_i32_i8_e32 v9, v4, v37
	v_and_b32_e32 v4, 0xf0f0f0f, v5
	v_mov_b32_e32 v8, 0
	v_dot4c_i32_i8_e32 v8, v4, v38
	v_lshrrev_b32_e32 v4, 4, v5
	v_and_b32_e32 v4, 0xf0f0f0f, v4
	v_dot4c_i32_i8_e32 v8, v4, v39
	v_and_b32_e32 v4, 0xf0f0f0f, v6
	v_dot4c_i32_i8_e32 v9, v4, v32
	v_lshrrev_b32_e32 v4, 4, v6
	v_and_b32_e32 v4, 0xf0f0f0f, v4
	v_dot4c_i32_i8_e32 v9, v4, v33
	v_and_b32_e32 v4, 0xf0f0f0f, v7
	v_dot4c_i32_i8_e32 v8, v4, v34
	v_lshrrev_b32_e32 v4, 4, v7
	v_and_b32_e32 v4, 0xf0f0f0f, v4
	v_dot4c_i32_i8_e32 v8, v4, v35
	s_waitcnt vmcnt(16)
	v_and_b32_e32 v4, 0xf0f0f0f, v0
	v_mov_b32_e32 v5, 0
	v_lshrrev_b32_e32 v0, 4, v0
	v_dot4c_i32_i8_e32 v5, v4, v36
	v_and_b32_e32 v0, 0xf0f0f0f, v0
	v_dot4c_i32_i8_e32 v5, v0, v37
	v_and_b32_e32 v0, 0xf0f0f0f, v1
	v_mov_b32_e32 v4, 0
	v_dot4c_i32_i8_e32 v4, v0, v38
	v_lshrrev_b32_e32 v0, 4, v1
	v_and_b32_e32 v0, 0xf0f0f0f, v0
	v_dot4c_i32_i8_e32 v4, v0, v39
	v_and_b32_e32 v0, 0xf0f0f0f, v2
	v_dot4c_i32_i8_e32 v5, v0, v32
	v_lshrrev_b32_e32 v0, 4, v2
	v_and_b32_e32 v0, 0xf0f0f0f, v0
	v_dot4c_i32_i8_e32 v5, v0, v33
	v_and_b32_e32 v0, 0xf0f0f0f, v3
	v_dot4c_i32_i8_e32 v4, v0, v34
	v_lshrrev_b32_e32 v0, 4, v3
	v_and_b32_e32 v0, 0xf0f0f0f, v0
	v_dot4c_i32_i8_e32 v4, v0, v35
	v_add_u32_e32 v2, v9, v8
	v_sub_u32_e32 v2, v2, v171
	v_and_b32_e32 v1, 0xffff0000, v40
	v_add_u32_e32 v3, v5, v4
	v_sub_u32_e32 v4, v3, v171
	v_cvt_f32_i32_e32 v3, v2
	v_cvt_f32_i32_e32 v2, v4
	v_lshlrev_b32_e32 v0, 16, v40
	v_pk_fma_f32 v[152:153], v[0:1], v[2:3], v[152:153]
	ds_read_u16 v0, v93 offset:16640
	ds_read_u16 v1, v93 offset:16656
	ds_read_u16 v2, v93 offset:16672
	ds_read_u16 v3, v93 offset:16688
	s_waitcnt lgkmcnt(3)
	v_add_u32_e32 v0, s44, v0
	v_lshl_or_b32 v4, v0, 7, v165
	s_waitcnt lgkmcnt(2)
	v_add_u32_e32 v1, s44, v1
	global_load_dwordx4 v[72:75], v4, s[0:1] sc1
	v_lshl_or_b32 v4, v1, 7, v165
	s_waitcnt lgkmcnt(1)
	v_add_u32_e32 v2, s44, v2
	global_load_dwordx4 v[64:67], v4, s[0:1] sc1
	v_lshl_or_b32 v4, v2, 7, v165
	s_waitcnt lgkmcnt(0)
	v_add_u32_e32 v3, s44, v3
	global_load_dwordx4 v[56:59], v4, s[0:1] sc1
	v_lshl_or_b32 v4, v3, 7, v165
	global_load_dwordx4 v[48:51], v4, s[0:1] sc1
	ds_read_u16 v4, v93 offset:16704
	v_lshl_or_b32 v0, v0, 5, v248
	v_lshl_or_b32 v1, v1, 5, v248
	v_lshl_or_b32 v2, v2, 5, v248
	v_lshl_or_b32 v3, v3, 5, v248
	s_waitcnt lgkmcnt(0)
	v_add_u32_e32 v4, s44, v4
	v_lshl_or_b32 v5, v4, 7, v165
	global_load_dwordx4 v[40:43], v5, s[0:1] sc1
	ds_read_u16 v5, v93 offset:16720
	v_lshl_or_b32 v4, v4, 5, v248
	s_waitcnt lgkmcnt(0)
	v_add_u32_e32 v5, s44, v5
	v_lshl_or_b32 v6, v5, 7, v165
	global_load_dwordx4 v[24:27], v6, s[0:1] sc1
	ds_read_u16 v6, v93 offset:16736
	v_lshl_or_b32 v5, v5, 5, v248
	s_waitcnt lgkmcnt(0)
	v_add_u32_e32 v6, s44, v6
	v_lshl_or_b32 v7, v6, 7, v165
	global_load_dwordx4 v[12:15], v7, s[0:1] sc1
	ds_read_u16 v7, v93 offset:16752
	v_lshl_or_b32 v6, v6, 5, v248
	s_waitcnt lgkmcnt(0)
	v_add_u32_e32 v7, s44, v7
	v_lshl_or_b32 v8, v7, 7, v165
	global_load_dwordx4 v[8:11], v8, s[0:1] sc1
	v_lshl_or_b32 v7, v7, 5, v248
	global_load_dword v201, v1, s[46:47]
	global_load_dword v200, v0, s[46:47]
	global_load_dword v203, v3, s[46:47]
	global_load_dword v202, v2, s[46:47]
	global_load_dword v205, v5, s[46:47]
	global_load_dword v204, v4, s[46:47]
	global_load_dword v207, v7, s[46:47]
	global_load_dword v206, v6, s[46:47]
	s_waitcnt vmcnt(31)
	v_and_b32_e32 v0, 0xf0f0f0f, v88
	v_mov_b32_e32 v2, 0
	v_dot4c_i32_i8_e32 v2, v0, v36
	v_lshrrev_b32_e32 v0, 4, v88
	v_and_b32_e32 v0, 0xf0f0f0f, v0
	v_dot4c_i32_i8_e32 v2, v0, v37
	v_and_b32_e32 v0, 0xf0f0f0f, v89
	v_mov_b32_e32 v3, 0
	v_dot4c_i32_i8_e32 v3, v0, v38
	v_lshrrev_b32_e32 v0, 4, v89
	v_and_b32_e32 v0, 0xf0f0f0f, v0
	v_dot4c_i32_i8_e32 v3, v0, v39
	v_and_b32_e32 v0, 0xf0f0f0f, v90
	v_dot4c_i32_i8_e32 v2, v0, v32
	v_lshrrev_b32_e32 v0, 4, v90
	v_and_b32_e32 v0, 0xf0f0f0f, v0
	v_dot4c_i32_i8_e32 v2, v0, v33
	v_and_b32_e32 v0, 0xf0f0f0f, v91
	v_dot4c_i32_i8_e32 v3, v0, v34
	v_lshrrev_b32_e32 v0, 4, v91
	v_and_b32_e32 v0, 0xf0f0f0f, v0
	v_dot4c_i32_i8_e32 v3, v0, v35
	s_waitcnt vmcnt(30)
	v_and_b32_e32 v0, 0xf0f0f0f, v84
	v_mov_b32_e32 v4, 0
	v_dot4c_i32_i8_e32 v4, v0, v36
	v_lshrrev_b32_e32 v0, 4, v84
	v_and_b32_e32 v0, 0xf0f0f0f, v0
	v_dot4c_i32_i8_e32 v4, v0, v37
	v_and_b32_e32 v0, 0xf0f0f0f, v85
	v_mov_b32_e32 v5, 0
	v_dot4c_i32_i8_e32 v5, v0, v38
	v_lshrrev_b32_e32 v0, 4, v85
	v_and_b32_e32 v0, 0xf0f0f0f, v0
	v_dot4c_i32_i8_e32 v5, v0, v39
	v_and_b32_e32 v0, 0xf0f0f0f, v86
	v_dot4c_i32_i8_e32 v4, v0, v32
	v_lshrrev_b32_e32 v0, 4, v86
	v_and_b32_e32 v0, 0xf0f0f0f, v0
	v_dot4c_i32_i8_e32 v4, v0, v33
	v_and_b32_e32 v0, 0xf0f0f0f, v87
	v_dot4c_i32_i8_e32 v5, v0, v34
	v_lshrrev_b32_e32 v0, 4, v87
	v_and_b32_e32 v0, 0xf0f0f0f, v0
	v_dot4c_i32_i8_e32 v5, v0, v35
	v_add_u32_e32 v2, v2, v3
	v_sub_u32_e32 v2, v2, v171
	s_waitcnt vmcnt(22)
	v_lshlrev_b32_e32 v1, 16, v192
	v_sub_u32_e32 v3, v5, v171
	v_add_u32_e32 v4, v3, v4
	v_cvt_f32_i32_e32 v3, v2
	v_cvt_f32_i32_e32 v2, v4
	v_lshlrev_b32_e32 v0, 16, v193
	v_mov_b32_e32 v4, 0
	v_mov_b32_e32 v5, 0
	v_pk_fma_f32 v[150:151], v[0:1], v[2:3], v[150:151]
	v_and_b32_e32 v0, 0xf0f0f0f, v80
	v_mov_b32_e32 v2, 0
	v_dot4c_i32_i8_e32 v2, v0, v36
	v_lshrrev_b32_e32 v0, 4, v80
	v_and_b32_e32 v0, 0xf0f0f0f, v0
	v_dot4c_i32_i8_e32 v2, v0, v37
	v_and_b32_e32 v0, 0xf0f0f0f, v81
	v_mov_b32_e32 v3, 0
	v_dot4c_i32_i8_e32 v3, v0, v38
	v_lshrrev_b32_e32 v0, 4, v81
	v_and_b32_e32 v0, 0xf0f0f0f, v0
	v_dot4c_i32_i8_e32 v3, v0, v39
	v_and_b32_e32 v0, 0xf0f0f0f, v82
	v_dot4c_i32_i8_e32 v2, v0, v32
	v_lshrrev_b32_e32 v0, 4, v82
	v_and_b32_e32 v0, 0xf0f0f0f, v0
	v_dot4c_i32_i8_e32 v2, v0, v33
	v_and_b32_e32 v0, 0xf0f0f0f, v83
	v_dot4c_i32_i8_e32 v3, v0, v34
	v_lshrrev_b32_e32 v0, 4, v83
	v_and_b32_e32 v0, 0xf0f0f0f, v0
	v_dot4c_i32_i8_e32 v3, v0, v35
	v_and_b32_e32 v0, 0xf0f0f0f, v76
	v_dot4c_i32_i8_e32 v4, v0, v36
	v_lshrrev_b32_e32 v0, 4, v76
	v_and_b32_e32 v0, 0xf0f0f0f, v0
	v_dot4c_i32_i8_e32 v4, v0, v37
	v_and_b32_e32 v0, 0xf0f0f0f, v77
	v_dot4c_i32_i8_e32 v5, v0, v38
	v_lshrrev_b32_e32 v0, 4, v77
	v_and_b32_e32 v0, 0xf0f0f0f, v0
	v_dot4c_i32_i8_e32 v5, v0, v39
	v_and_b32_e32 v0, 0xf0f0f0f, v78
	v_dot4c_i32_i8_e32 v4, v0, v32
	v_lshrrev_b32_e32 v0, 4, v78
	v_and_b32_e32 v0, 0xf0f0f0f, v0
	v_dot4c_i32_i8_e32 v4, v0, v33
	v_and_b32_e32 v0, 0xf0f0f0f, v79
	v_dot4c_i32_i8_e32 v5, v0, v34
	v_lshrrev_b32_e32 v0, 4, v79
	v_and_b32_e32 v0, 0xf0f0f0f, v0
	v_dot4c_i32_i8_e32 v5, v0, v35
	v_sub_u32_e32 v3, v3, v171
	v_add_u32_e32 v2, v3, v2
	v_cvt_f32_i32_e32 v3, v2
	v_sub_u32_e32 v5, v5, v171
	v_add_u32_e32 v4, v5, v4
	v_cvt_f32_i32_e32 v2, v4
	s_waitcnt vmcnt(20)
	v_lshlrev_b32_e32 v1, 16, v194
	v_lshlrev_b32_e32 v0, 16, v195
	v_mov_b32_e32 v4, 0
	v_pk_fma_f32 v[148:149], v[0:1], v[2:3], v[148:149]
	v_and_b32_e32 v0, 0xf0f0f0f, v68
	v_mov_b32_e32 v2, 0
	v_dot4c_i32_i8_e32 v2, v0, v36
	v_lshrrev_b32_e32 v0, 4, v68
	v_and_b32_e32 v0, 0xf0f0f0f, v0
	v_dot4c_i32_i8_e32 v2, v0, v37
	v_and_b32_e32 v0, 0xf0f0f0f, v69
	v_mov_b32_e32 v3, 0
	v_dot4c_i32_i8_e32 v3, v0, v38
	v_lshrrev_b32_e32 v0, 4, v69
	v_and_b32_e32 v0, 0xf0f0f0f, v0
	v_dot4c_i32_i8_e32 v3, v0, v39
	v_and_b32_e32 v0, 0xf0f0f0f, v70
	v_dot4c_i32_i8_e32 v2, v0, v32
	v_lshrrev_b32_e32 v0, 4, v70
	v_and_b32_e32 v0, 0xf0f0f0f, v0
	v_dot4c_i32_i8_e32 v2, v0, v33
	v_and_b32_e32 v0, 0xf0f0f0f, v71
	v_dot4c_i32_i8_e32 v3, v0, v34
	v_lshrrev_b32_e32 v0, 4, v71
	v_and_b32_e32 v0, 0xf0f0f0f, v0
	v_dot4c_i32_i8_e32 v3, v0, v35
	v_and_b32_e32 v0, 0xf0f0f0f, v60
	v_dot4c_i32_i8_e32 v4, v0, v36
	v_lshrrev_b32_e32 v0, 4, v60
	v_and_b32_e32 v0, 0xf0f0f0f, v0
	v_dot4c_i32_i8_e32 v4, v0, v37
	v_and_b32_e32 v0, 0xf0f0f0f, v61
	v_mov_b32_e32 v5, 0
	v_dot4c_i32_i8_e32 v5, v0, v38
	v_lshrrev_b32_e32 v0, 4, v61
	v_and_b32_e32 v0, 0xf0f0f0f, v0
	v_dot4c_i32_i8_e32 v5, v0, v39
	v_and_b32_e32 v0, 0xf0f0f0f, v62
	v_dot4c_i32_i8_e32 v4, v0, v32
	v_lshrrev_b32_e32 v0, 4, v62
	v_and_b32_e32 v0, 0xf0f0f0f, v0
	v_dot4c_i32_i8_e32 v4, v0, v33
	v_and_b32_e32 v0, 0xf0f0f0f, v63
	v_dot4c_i32_i8_e32 v5, v0, v34
	v_lshrrev_b32_e32 v0, 4, v63
	v_and_b32_e32 v0, 0xf0f0f0f, v0
	v_dot4c_i32_i8_e32 v5, v0, v35
	v_sub_u32_e32 v3, v3, v171
	v_add_u32_e32 v2, v3, v2
	v_cvt_f32_i32_e32 v3, v2
	v_sub_u32_e32 v5, v5, v171
	v_add_u32_e32 v4, v5, v4
	v_cvt_f32_i32_e32 v2, v4
	s_waitcnt vmcnt(18)
	v_lshlrev_b32_e32 v1, 16, v196
	v_lshlrev_b32_e32 v0, 16, v197
	v_mov_b32_e32 v4, 0
	v_pk_fma_f32 v[146:147], v[0:1], v[2:3], v[146:147]
	v_and_b32_e32 v0, 0xf0f0f0f, v52
	v_mov_b32_e32 v2, 0
	v_dot4c_i32_i8_e32 v2, v0, v36
	v_lshrrev_b32_e32 v0, 4, v52
	v_and_b32_e32 v0, 0xf0f0f0f, v0
	v_dot4c_i32_i8_e32 v2, v0, v37
	v_and_b32_e32 v0, 0xf0f0f0f, v53
	v_mov_b32_e32 v3, 0
	v_dot4c_i32_i8_e32 v3, v0, v38
	v_lshrrev_b32_e32 v0, 4, v53
	v_and_b32_e32 v0, 0xf0f0f0f, v0
	v_dot4c_i32_i8_e32 v3, v0, v39
	v_and_b32_e32 v0, 0xf0f0f0f, v54
	v_dot4c_i32_i8_e32 v2, v0, v32
	v_lshrrev_b32_e32 v0, 4, v54
	v_and_b32_e32 v0, 0xf0f0f0f, v0
	v_dot4c_i32_i8_e32 v2, v0, v33
	v_and_b32_e32 v0, 0xf0f0f0f, v55
	v_dot4c_i32_i8_e32 v3, v0, v34
	v_lshrrev_b32_e32 v0, 4, v55
	v_and_b32_e32 v0, 0xf0f0f0f, v0
	v_dot4c_i32_i8_e32 v3, v0, v35
	v_and_b32_e32 v0, 0xf0f0f0f, v44
	v_dot4c_i32_i8_e32 v4, v0, v36
	v_lshrrev_b32_e32 v0, 4, v44
	v_and_b32_e32 v0, 0xf0f0f0f, v0
	v_dot4c_i32_i8_e32 v4, v0, v37
	v_and_b32_e32 v0, 0xf0f0f0f, v45
	v_mov_b32_e32 v5, 0
	v_dot4c_i32_i8_e32 v5, v0, v38
	v_lshrrev_b32_e32 v0, 4, v45
	v_and_b32_e32 v0, 0xf0f0f0f, v0
	v_dot4c_i32_i8_e32 v5, v0, v39
	v_and_b32_e32 v0, 0xf0f0f0f, v46
	v_dot4c_i32_i8_e32 v4, v0, v32
	v_lshrrev_b32_e32 v0, 4, v46
	v_and_b32_e32 v0, 0xf0f0f0f, v0
	v_dot4c_i32_i8_e32 v4, v0, v33
	v_and_b32_e32 v0, 0xf0f0f0f, v47
	v_dot4c_i32_i8_e32 v5, v0, v34
	v_lshrrev_b32_e32 v0, 4, v47
	v_and_b32_e32 v0, 0xf0f0f0f, v0
	v_dot4c_i32_i8_e32 v5, v0, v35
	v_sub_u32_e32 v3, v3, v171
	v_add_u32_e32 v2, v3, v2
	v_cvt_f32_i32_e32 v3, v2
	v_sub_u32_e32 v5, v5, v171
	v_add_u32_e32 v4, v5, v4
	v_cvt_f32_i32_e32 v2, v4
	s_waitcnt vmcnt(16)
	v_lshlrev_b32_e32 v1, 16, v198
	v_lshlrev_b32_e32 v0, 16, v199
	v_pk_fma_f32 v[144:145], v[0:1], v[2:3], v[144:145]
	ds_read_b128 v[4:7], v166 offset:4096
	ds_read_b128 v[0:3], v166 offset:4112
	ds_read_u16 v16, v93 offset:16768
	ds_read_u16 v17, v93 offset:16784
	ds_read_u16 v18, v93 offset:16800
	ds_read_u16 v19, v93 offset:16816
	v_mov_b32_e32 v44, 0
	s_waitcnt lgkmcnt(3)
	v_add_u32_e32 v16, s44, v16
	v_lshl_or_b32 v20, v16, 7, v165
	v_lshl_or_b32 v45, v16, 5, v248
	s_waitcnt lgkmcnt(2)
	v_add_u32_e32 v16, s44, v17
	v_lshl_or_b32 v17, v16, 7, v165
	v_lshl_or_b32 v46, v16, 5, v248
	s_waitcnt lgkmcnt(1)
	v_add_u32_e32 v16, s44, v18
	global_load_dwordx4 v[80:83], v20, s[0:1] sc1
	global_load_dwordx4 v[68:71], v17, s[0:1] sc1
	v_lshl_or_b32 v17, v16, 7, v165
	v_lshl_or_b32 v47, v16, 5, v248
	s_waitcnt lgkmcnt(0)
	v_add_u32_e32 v16, s44, v19
	global_load_dwordx4 v[52:55], v17, s[0:1] sc1
	v_lshl_or_b32 v17, v16, 7, v165
	v_lshl_or_b32 v60, v16, 5, v248
	ds_read_u16 v16, v93 offset:16832
	global_load_dwordx4 v[36:39], v17, s[0:1] sc1
	v_dot4c_i32_i8_e32 v44, 0x1010101, v4
	v_dot4c_i32_i8_e32 v44, 0x1010101, v5
	v_dot4c_i32_i8_e32 v44, 0x1010101, v6
	s_waitcnt lgkmcnt(0)
	v_add_u32_e32 v16, s44, v16
	v_lshl_or_b32 v17, v16, 7, v165
	v_lshl_or_b32 v61, v16, 5, v248
	ds_read_u16 v16, v93 offset:16848
	global_load_dwordx4 v[32:35], v17, s[0:1] sc1
	v_dot4c_i32_i8_e32 v44, 0x1010101, v7
	v_dot4c_i32_i8_e32 v44, 0x1010101, v0
	v_dot4c_i32_i8_e32 v44, 0x1010101, v1
	s_waitcnt lgkmcnt(0)
	v_add_u32_e32 v16, s44, v16
	v_lshl_or_b32 v17, v16, 7, v165
	v_lshl_or_b32 v62, v16, 5, v248
	ds_read_u16 v16, v93 offset:16864
	global_load_dwordx4 v[28:31], v17, s[0:1] sc1
	v_dot4c_i32_i8_e32 v44, 0x1010101, v2
	v_dot4c_i32_i8_e32 v44, 0x1010101, v3
	s_waitcnt lgkmcnt(0)
	v_add_u32_e32 v16, s44, v16
	v_lshl_or_b32 v17, v16, 7, v165
	v_lshl_or_b32 v63, v16, 5, v248
	ds_read_u16 v16, v93 offset:16880
	global_load_dwordx4 v[20:23], v17, s[0:1] sc1
	v_lshlrev_b32_e32 v84, 3, v44
	s_waitcnt vmcnt(22)
	v_and_b32_e32 v44, 0xf0f0f0f, v72
	s_waitcnt lgkmcnt(0)
	v_add_u32_e32 v76, s44, v16
	v_lshl_or_b32 v16, v76, 7, v165
	global_load_dwordx4 v[16:19], v16, s[0:1] sc1
	v_lshl_or_b32 v76, v76, 5, v248
	global_load_dword v209, v46, s[46:47]
	global_load_dword v208, v45, s[46:47]
	global_load_dword v211, v60, s[46:47]
	global_load_dword v210, v47, s[46:47]
	global_load_dword v213, v62, s[46:47]
	global_load_dword v212, v61, s[46:47]
	global_load_dword v215, v76, s[46:47]
	global_load_dword v214, v63, s[46:47]
	v_mov_b32_e32 v46, 0
	v_dot4c_i32_i8_e32 v46, v44, v4
	v_lshrrev_b32_e32 v44, 4, v72
	v_and_b32_e32 v44, 0xf0f0f0f, v44
	v_dot4c_i32_i8_e32 v46, v44, v5
	v_and_b32_e32 v44, 0xf0f0f0f, v73
	v_mov_b32_e32 v47, 0
	v_dot4c_i32_i8_e32 v47, v44, v6
	v_lshrrev_b32_e32 v44, 4, v73
	v_and_b32_e32 v44, 0xf0f0f0f, v44
	v_dot4c_i32_i8_e32 v47, v44, v7
	v_and_b32_e32 v44, 0xf0f0f0f, v74
	v_dot4c_i32_i8_e32 v46, v44, v0
	v_lshrrev_b32_e32 v44, 4, v74
	v_and_b32_e32 v44, 0xf0f0f0f, v44
	v_dot4c_i32_i8_e32 v46, v44, v1
	v_and_b32_e32 v44, 0xf0f0f0f, v75
	v_dot4c_i32_i8_e32 v47, v44, v2
	v_lshrrev_b32_e32 v44, 4, v75
	v_and_b32_e32 v44, 0xf0f0f0f, v44
	v_dot4c_i32_i8_e32 v47, v44, v3
	s_waitcnt vmcnt(30)
	v_and_b32_e32 v44, 0xf0f0f0f, v64
	v_mov_b32_e32 v60, 0
	v_dot4c_i32_i8_e32 v60, v44, v4
	v_lshrrev_b32_e32 v44, 4, v64
	v_and_b32_e32 v44, 0xf0f0f0f, v44
	v_dot4c_i32_i8_e32 v60, v44, v5
	v_and_b32_e32 v44, 0xf0f0f0f, v65
	v_mov_b32_e32 v61, 0
	v_dot4c_i32_i8_e32 v61, v44, v6
	v_lshrrev_b32_e32 v44, 4, v65
	v_and_b32_e32 v44, 0xf0f0f0f, v44
	v_dot4c_i32_i8_e32 v61, v44, v7
	v_and_b32_e32 v44, 0xf0f0f0f, v66
	v_dot4c_i32_i8_e32 v60, v44, v0
	v_lshrrev_b32_e32 v44, 4, v66
	v_and_b32_e32 v44, 0xf0f0f0f, v44
	v_dot4c_i32_i8_e32 v60, v44, v1
	v_and_b32_e32 v44, 0xf0f0f0f, v67
	v_dot4c_i32_i8_e32 v61, v44, v2
	v_lshrrev_b32_e32 v44, 4, v67
	v_and_b32_e32 v44, 0xf0f0f0f, v44
	v_dot4c_i32_i8_e32 v61, v44, v3
	v_add_u32_e32 v46, v46, v47
	v_sub_u32_e32 v46, v46, v84
	s_waitcnt vmcnt(22)
	v_lshlrev_b32_e32 v45, 16, v200
	v_add_u32_e32 v47, v60, v61
	v_sub_u32_e32 v60, v47, v84
	v_cvt_f32_i32_e32 v47, v46
	v_cvt_f32_i32_e32 v46, v60
	v_lshlrev_b32_e32 v44, 16, v201
	v_pk_fma_f32 v[142:143], v[44:45], v[46:47], v[142:143]
	v_and_b32_e32 v44, 0xf0f0f0f, v56
	v_mov_b32_e32 v46, 0
	v_dot4c_i32_i8_e32 v46, v44, v4
	v_lshrrev_b32_e32 v44, 4, v56
	v_and_b32_e32 v44, 0xf0f0f0f, v44
	v_dot4c_i32_i8_e32 v46, v44, v5
	v_and_b32_e32 v44, 0xf0f0f0f, v57
	v_mov_b32_e32 v47, 0
	v_dot4c_i32_i8_e32 v47, v44, v6
	v_lshrrev_b32_e32 v44, 4, v57
	v_and_b32_e32 v44, 0xf0f0f0f, v44
	v_dot4c_i32_i8_e32 v47, v44, v7
	v_and_b32_e32 v44, 0xf0f0f0f, v58
	v_dot4c_i32_i8_e32 v46, v44, v0
	v_lshrrev_b32_e32 v44, 4, v58
	v_and_b32_e32 v44, 0xf0f0f0f, v44
	v_dot4c_i32_i8_e32 v46, v44, v1
	v_and_b32_e32 v44, 0xf0f0f0f, v59
	v_dot4c_i32_i8_e32 v47, v44, v2
	v_lshrrev_b32_e32 v44, 4, v59
	v_and_b32_e32 v44, 0xf0f0f0f, v44
	v_dot4c_i32_i8_e32 v47, v44, v3
	v_and_b32_e32 v44, 0xf0f0f0f, v48
	v_mov_b32_e32 v56, 0
	v_dot4c_i32_i8_e32 v56, v44, v4
	v_lshrrev_b32_e32 v44, 4, v48
	v_and_b32_e32 v44, 0xf0f0f0f, v44
	v_dot4c_i32_i8_e32 v56, v44, v5
	v_and_b32_e32 v44, 0xf0f0f0f, v49
	v_mov_b32_e32 v48, 0
	v_dot4c_i32_i8_e32 v48, v44, v6
	v_lshrrev_b32_e32 v44, 4, v49
	v_and_b32_e32 v44, 0xf0f0f0f, v44
	v_dot4c_i32_i8_e32 v48, v44, v7
	v_and_b32_e32 v44, 0xf0f0f0f, v50
	v_dot4c_i32_i8_e32 v56, v44, v0
	v_lshrrev_b32_e32 v44, 4, v50
	v_and_b32_e32 v44, 0xf0f0f0f, v44
	v_dot4c_i32_i8_e32 v56, v44, v1
	v_and_b32_e32 v44, 0xf0f0f0f, v51
	v_dot4c_i32_i8_e32 v48, v44, v2
	v_lshrrev_b32_e32 v44, 4, v51
	v_and_b32_e32 v44, 0xf0f0f0f, v44
	v_dot4c_i32_i8_e32 v48, v44, v3
	v_add_u32_e32 v46, v46, v47
	v_sub_u32_e32 v46, v46, v84
	s_waitcnt vmcnt(20)
	v_lshlrev_b32_e32 v45, 16, v202
	v_add_u32_e32 v47, v56, v48
	v_sub_u32_e32 v48, v47, v84
	v_cvt_f32_i32_e32 v47, v46
	v_cvt_f32_i32_e32 v46, v48
	v_lshlrev_b32_e32 v44, 16, v203
	v_pk_fma_f32 v[140:141], v[44:45], v[46:47], v[140:141]
	v_and_b32_e32 v44, 0xf0f0f0f, v40
	v_mov_b32_e32 v45, 0
	v_lshrrev_b32_e32 v40, 4, v40
	v_dot4c_i32_i8_e32 v45, v44, v4
	v_and_b32_e32 v40, 0xf0f0f0f, v40
	v_dot4c_i32_i8_e32 v45, v40, v5
	v_and_b32_e32 v40, 0xf0f0f0f, v41
	v_mov_b32_e32 v44, 0
	v_dot4c_i32_i8_e32 v44, v40, v6
	v_lshrrev_b32_e32 v40, 4, v41
	v_and_b32_e32 v40, 0xf0f0f0f, v40
	v_dot4c_i32_i8_e32 v44, v40, v7
	v_and_b32_e32 v40, 0xf0f0f0f, v42
	v_dot4c_i32_i8_e32 v45, v40, v0
	v_lshrrev_b32_e32 v40, 4, v42
	v_and_b32_e32 v40, 0xf0f0f0f, v40
	v_dot4c_i32_i8_e32 v45, v40, v1
	v_and_b32_e32 v40, 0xf0f0f0f, v43
	v_dot4c_i32_i8_e32 v44, v40, v2
	v_lshrrev_b32_e32 v40, 4, v43
	v_and_b32_e32 v40, 0xf0f0f0f, v40
	v_dot4c_i32_i8_e32 v44, v40, v3
	v_and_b32_e32 v40, 0xf0f0f0f, v24
	v_mov_b32_e32 v41, 0
	v_lshrrev_b32_e32 v24, 4, v24
	v_dot4c_i32_i8_e32 v41, v40, v4
	v_and_b32_e32 v24, 0xf0f0f0f, v24
	v_dot4c_i32_i8_e32 v41, v24, v5
	v_and_b32_e32 v24, 0xf0f0f0f, v25
	v_mov_b32_e32 v40, 0
	v_dot4c_i32_i8_e32 v40, v24, v6
	v_lshrrev_b32_e32 v24, 4, v25
	v_and_b32_e32 v24, 0xf0f0f0f, v24
	v_dot4c_i32_i8_e32 v40, v24, v7
	v_and_b32_e32 v24, 0xf0f0f0f, v26
	v_dot4c_i32_i8_e32 v41, v24, v0
	v_lshrrev_b32_e32 v24, 4, v26
	v_and_b32_e32 v24, 0xf0f0f0f, v24
	v_dot4c_i32_i8_e32 v41, v24, v1
	v_and_b32_e32 v24, 0xf0f0f0f, v27
	v_dot4c_i32_i8_e32 v40, v24, v2
	v_lshrrev_b32_e32 v24, 4, v27
	v_and_b32_e32 v24, 0xf0f0f0f, v24
	v_dot4c_i32_i8_e32 v40, v24, v3
	v_add_u32_e32 v26, v45, v44
	v_sub_u32_e32 v26, v26, v84
	s_waitcnt vmcnt(18)
	v_lshlrev_b32_e32 v25, 16, v204
	v_add_u32_e32 v27, v41, v40
	v_sub_u32_e32 v40, v27, v84
	v_cvt_f32_i32_e32 v27, v26
	v_cvt_f32_i32_e32 v26, v40
	v_lshlrev_b32_e32 v24, 16, v205
	v_pk_fma_f32 v[138:139], v[24:25], v[26:27], v[138:139]
	v_and_b32_e32 v24, 0xf0f0f0f, v12
	v_mov_b32_e32 v25, 0
	v_lshrrev_b32_e32 v12, 4, v12
	v_dot4c_i32_i8_e32 v25, v24, v4
	v_and_b32_e32 v12, 0xf0f0f0f, v12
	v_dot4c_i32_i8_e32 v25, v12, v5
	v_and_b32_e32 v12, 0xf0f0f0f, v13
	v_mov_b32_e32 v24, 0
	v_dot4c_i32_i8_e32 v24, v12, v6
	v_lshrrev_b32_e32 v12, 4, v13
	v_and_b32_e32 v12, 0xf0f0f0f, v12
	v_dot4c_i32_i8_e32 v24, v12, v7
	v_and_b32_e32 v12, 0xf0f0f0f, v14
	v_dot4c_i32_i8_e32 v25, v12, v0
	v_lshrrev_b32_e32 v12, 4, v14
	v_and_b32_e32 v12, 0xf0f0f0f, v12
	v_dot4c_i32_i8_e32 v25, v12, v1
	v_and_b32_e32 v12, 0xf0f0f0f, v15
	v_dot4c_i32_i8_e32 v24, v12, v2
	v_lshrrev_b32_e32 v12, 4, v15
	v_and_b32_e32 v12, 0xf0f0f0f, v12
	v_dot4c_i32_i8_e32 v24, v12, v3
	v_and_b32_e32 v12, 0xf0f0f0f, v8
	v_mov_b32_e32 v13, 0
	v_lshrrev_b32_e32 v8, 4, v8
	v_dot4c_i32_i8_e32 v13, v12, v4
	v_and_b32_e32 v8, 0xf0f0f0f, v8
	v_dot4c_i32_i8_e32 v13, v8, v5
	v_and_b32_e32 v8, 0xf0f0f0f, v9
	v_mov_b32_e32 v12, 0
	v_dot4c_i32_i8_e32 v12, v8, v6
	v_lshrrev_b32_e32 v8, 4, v9
	v_and_b32_e32 v8, 0xf0f0f0f, v8
	v_dot4c_i32_i8_e32 v12, v8, v7
	v_and_b32_e32 v8, 0xf0f0f0f, v10
	v_dot4c_i32_i8_e32 v13, v8, v0
	v_lshrrev_b32_e32 v8, 4, v10
	v_and_b32_e32 v8, 0xf0f0f0f, v8
	v_dot4c_i32_i8_e32 v13, v8, v1
	v_and_b32_e32 v8, 0xf0f0f0f, v11
	v_dot4c_i32_i8_e32 v12, v8, v2
	v_lshrrev_b32_e32 v8, 4, v11
	v_and_b32_e32 v8, 0xf0f0f0f, v8
	v_dot4c_i32_i8_e32 v12, v8, v3
	v_add_u32_e32 v10, v25, v24
	v_sub_u32_e32 v10, v10, v84
	s_waitcnt vmcnt(16)
	v_lshlrev_b32_e32 v9, 16, v206
	v_add_u32_e32 v11, v13, v12
	v_sub_u32_e32 v12, v11, v84
	v_cvt_f32_i32_e32 v11, v10
	v_cvt_f32_i32_e32 v10, v12
	v_lshlrev_b32_e32 v8, 16, v207
	v_pk_fma_f32 v[136:137], v[8:9], v[10:11], v[136:137]
	ds_read_u16 v8, v93 offset:16896
	ds_read_u16 v9, v93 offset:16912
	ds_read_u16 v10, v93 offset:16928
	ds_read_u16 v11, v93 offset:16944
	s_waitcnt lgkmcnt(3)
	v_add_u32_e32 v8, s44, v8
	v_lshl_or_b32 v12, v8, 7, v165
	v_lshl_or_b32 v40, v8, 5, v248
	s_waitcnt lgkmcnt(2)
	v_add_u32_e32 v8, s44, v9
	v_lshl_or_b32 v9, v8, 7, v165
	v_lshl_or_b32 v41, v8, 5, v248
	s_waitcnt lgkmcnt(1)
	v_add_u32_e32 v8, s44, v10
	global_load_dwordx4 v[76:79], v12, s[0:1] sc1
	global_load_dwordx4 v[72:75], v9, s[0:1] sc1
	v_lshl_or_b32 v9, v8, 7, v165
	v_lshl_or_b32 v42, v8, 5, v248
	s_waitcnt lgkmcnt(0)
	v_add_u32_e32 v8, s44, v11
	global_load_dwordx4 v[60:63], v9, s[0:1] sc1
	v_lshl_or_b32 v9, v8, 7, v165
	v_lshl_or_b32 v43, v8, 5, v248
	ds_read_u16 v8, v93 offset:16960
	global_load_dwordx4 v[56:59], v9, s[0:1] sc1
	s_waitcnt lgkmcnt(0)
	v_add_u32_e32 v8, s44, v8
	v_lshl_or_b32 v9, v8, 7, v165
	v_lshl_or_b32 v48, v8, 5, v248
	ds_read_u16 v8, v93 offset:16976
	global_load_dwordx4 v[44:47], v9, s[0:1] sc1
	s_waitcnt lgkmcnt(0)
	v_add_u32_e32 v8, s44, v8
	v_lshl_or_b32 v9, v8, 7, v165
	v_lshl_or_b32 v49, v8, 5, v248
	ds_read_u16 v8, v93 offset:16992
	global_load_dwordx4 v[24:27], v9, s[0:1] sc1
	s_waitcnt lgkmcnt(0)
	v_add_u32_e32 v8, s44, v8
	v_lshl_or_b32 v9, v8, 7, v165
	v_lshl_or_b32 v50, v8, 5, v248
	ds_read_u16 v8, v93 offset:17008
	global_load_dwordx4 v[12:15], v9, s[0:1] sc1
	s_waitcnt lgkmcnt(0)
	v_add_u32_e32 v51, s44, v8
	v_lshl_or_b32 v8, v51, 7, v165
	global_load_dwordx4 v[8:11], v8, s[0:1] sc1
	v_lshl_or_b32 v51, v51, 5, v248
	global_load_dword v217, v41, s[46:47]
	global_load_dword v216, v40, s[46:47]
	global_load_dword v219, v43, s[46:47]
	global_load_dword v218, v42, s[46:47]
	global_load_dword v221, v49, s[46:47]
	global_load_dword v220, v48, s[46:47]
	global_load_dword v223, v51, s[46:47]
	global_load_dword v222, v50, s[46:47]
	s_waitcnt vmcnt(31)
	v_and_b32_e32 v40, 0xf0f0f0f, v80
	v_mov_b32_e32 v42, 0
	v_dot4c_i32_i8_e32 v42, v40, v4
	v_lshrrev_b32_e32 v40, 4, v80
	v_and_b32_e32 v40, 0xf0f0f0f, v40
	v_dot4c_i32_i8_e32 v42, v40, v5
	v_and_b32_e32 v40, 0xf0f0f0f, v81
	v_mov_b32_e32 v43, 0
	v_dot4c_i32_i8_e32 v43, v40, v6
	v_lshrrev_b32_e32 v40, 4, v81
	v_and_b32_e32 v40, 0xf0f0f0f, v40
	v_dot4c_i32_i8_e32 v43, v40, v7
	v_and_b32_e32 v40, 0xf0f0f0f, v82
	v_dot4c_i32_i8_e32 v42, v40, v0
	v_lshrrev_b32_e32 v40, 4, v82
	v_and_b32_e32 v40, 0xf0f0f0f, v40
	v_dot4c_i32_i8_e32 v42, v40, v1
	v_and_b32_e32 v40, 0xf0f0f0f, v83
	v_dot4c_i32_i8_e32 v43, v40, v2
	v_lshrrev_b32_e32 v40, 4, v83
	v_and_b32_e32 v40, 0xf0f0f0f, v40
	v_dot4c_i32_i8_e32 v43, v40, v3
	s_waitcnt vmcnt(30)
	v_and_b32_e32 v40, 0xf0f0f0f, v68
	v_mov_b32_e32 v48, 0
	v_dot4c_i32_i8_e32 v48, v40, v4
	v_lshrrev_b32_e32 v40, 4, v68
	v_and_b32_e32 v40, 0xf0f0f0f, v40
	v_dot4c_i32_i8_e32 v48, v40, v5
	v_and_b32_e32 v40, 0xf0f0f0f, v69
	v_mov_b32_e32 v49, 0
	v_dot4c_i32_i8_e32 v49, v40, v6
	v_lshrrev_b32_e32 v40, 4, v69
	v_and_b32_e32 v40, 0xf0f0f0f, v40
	v_dot4c_i32_i8_e32 v49, v40, v7
	v_and_b32_e32 v40, 0xf0f0f0f, v70
	v_dot4c_i32_i8_e32 v48, v40, v0
	v_lshrrev_b32_e32 v40, 4, v70
	v_and_b32_e32 v40, 0xf0f0f0f, v40
	v_dot4c_i32_i8_e32 v48, v40, v1
	v_and_b32_e32 v40, 0xf0f0f0f, v71
	v_dot4c_i32_i8_e32 v49, v40, v2
	v_lshrrev_b32_e32 v40, 4, v71
	v_and_b32_e32 v40, 0xf0f0f0f, v40
	v_dot4c_i32_i8_e32 v49, v40, v3
	v_add_u32_e32 v42, v42, v43
	v_sub_u32_e32 v42, v42, v84
	s_waitcnt vmcnt(22)
	v_lshlrev_b32_e32 v41, 16, v208
	v_sub_u32_e32 v43, v49, v84
	v_add_u32_e32 v48, v43, v48
	v_cvt_f32_i32_e32 v43, v42
	v_cvt_f32_i32_e32 v42, v48
	v_lshlrev_b32_e32 v40, 16, v209
	v_pk_fma_f32 v[134:135], v[40:41], v[42:43], v[134:135]
	v_and_b32_e32 v40, 0xf0f0f0f, v52
	v_mov_b32_e32 v41, 0
	v_dot4c_i32_i8_e32 v41, v40, v4
	v_lshrrev_b32_e32 v40, 4, v52
	v_and_b32_e32 v40, 0xf0f0f0f, v40
	v_dot4c_i32_i8_e32 v41, v40, v5
	v_and_b32_e32 v40, 0xf0f0f0f, v53
	v_mov_b32_e32 v42, 0
	v_dot4c_i32_i8_e32 v42, v40, v6
	v_lshrrev_b32_e32 v40, 4, v53
	v_and_b32_e32 v40, 0xf0f0f0f, v40
	v_dot4c_i32_i8_e32 v42, v40, v7
	v_and_b32_e32 v40, 0xf0f0f0f, v54
	v_dot4c_i32_i8_e32 v41, v40, v0
	v_lshrrev_b32_e32 v40, 4, v54
	v_and_b32_e32 v40, 0xf0f0f0f, v40
	v_dot4c_i32_i8_e32 v41, v40, v1
	v_and_b32_e32 v40, 0xf0f0f0f, v55
	v_dot4c_i32_i8_e32 v42, v40, v2
	v_lshrrev_b32_e32 v40, 4, v55
	v_and_b32_e32 v40, 0xf0f0f0f, v40
	v_dot4c_i32_i8_e32 v42, v40, v3
	v_and_b32_e32 v40, 0xf0f0f0f, v36
	v_mov_b32_e32 v43, 0
	v_lshrrev_b32_e32 v36, 4, v36
	v_dot4c_i32_i8_e32 v43, v40, v4
	v_and_b32_e32 v36, 0xf0f0f0f, v36
	v_dot4c_i32_i8_e32 v43, v36, v5
	v_and_b32_e32 v36, 0xf0f0f0f, v37
	v_mov_b32_e32 v40, 0
	v_dot4c_i32_i8_e32 v40, v36, v6
	v_lshrrev_b32_e32 v36, 4, v37
	v_and_b32_e32 v36, 0xf0f0f0f, v36
	v_dot4c_i32_i8_e32 v40, v36, v7
	v_and_b32_e32 v36, 0xf0f0f0f, v38
	v_dot4c_i32_i8_e32 v43, v36, v0
	v_lshrrev_b32_e32 v36, 4, v38
	v_and_b32_e32 v36, 0xf0f0f0f, v36
	v_dot4c_i32_i8_e32 v43, v36, v1
	v_and_b32_e32 v36, 0xf0f0f0f, v39
	v_dot4c_i32_i8_e32 v40, v36, v2
	v_lshrrev_b32_e32 v36, 4, v39
	v_and_b32_e32 v36, 0xf0f0f0f, v36
	v_dot4c_i32_i8_e32 v40, v36, v3
	v_sub_u32_e32 v38, v42, v84
	v_add_u32_e32 v38, v38, v41
	s_waitcnt vmcnt(20)
	v_lshlrev_b32_e32 v37, 16, v210
	v_sub_u32_e32 v39, v40, v84
	v_add_u32_e32 v40, v39, v43
	v_cvt_f32_i32_e32 v39, v38
	v_cvt_f32_i32_e32 v38, v40
	v_lshlrev_b32_e32 v36, 16, v211
	v_pk_fma_f32 v[132:133], v[36:37], v[38:39], v[132:133]
	v_and_b32_e32 v36, 0xf0f0f0f, v32
	v_mov_b32_e32 v37, 0
	v_lshrrev_b32_e32 v32, 4, v32
	v_dot4c_i32_i8_e32 v37, v36, v4
	v_and_b32_e32 v32, 0xf0f0f0f, v32
	v_dot4c_i32_i8_e32 v37, v32, v5
	v_and_b32_e32 v32, 0xf0f0f0f, v33
	v_mov_b32_e32 v36, 0
	v_dot4c_i32_i8_e32 v36, v32, v6
	v_lshrrev_b32_e32 v32, 4, v33
	v_and_b32_e32 v32, 0xf0f0f0f, v32
	v_dot4c_i32_i8_e32 v36, v32, v7
	v_and_b32_e32 v32, 0xf0f0f0f, v34
	v_dot4c_i32_i8_e32 v37, v32, v0
	v_lshrrev_b32_e32 v32, 4, v34
	v_and_b32_e32 v32, 0xf0f0f0f, v32
	v_dot4c_i32_i8_e32 v37, v32, v1
	v_and_b32_e32 v32, 0xf0f0f0f, v35
	v_dot4c_i32_i8_e32 v36, v32, v2
	v_lshrrev_b32_e32 v32, 4, v35
	v_and_b32_e32 v32, 0xf0f0f0f, v32
	v_dot4c_i32_i8_e32 v36, v32, v3
	v_and_b32_e32 v32, 0xf0f0f0f, v28
	v_mov_b32_e32 v33, 0
	v_lshrrev_b32_e32 v28, 4, v28
	v_dot4c_i32_i8_e32 v33, v32, v4
	v_and_b32_e32 v28, 0xf0f0f0f, v28
	v_dot4c_i32_i8_e32 v33, v28, v5
	v_and_b32_e32 v28, 0xf0f0f0f, v29
	v_mov_b32_e32 v32, 0
	v_dot4c_i32_i8_e32 v32, v28, v6
	v_lshrrev_b32_e32 v28, 4, v29
	v_and_b32_e32 v28, 0xf0f0f0f, v28
	v_dot4c_i32_i8_e32 v32, v28, v7
	v_and_b32_e32 v28, 0xf0f0f0f, v30
	v_dot4c_i32_i8_e32 v33, v28, v0
	v_lshrrev_b32_e32 v28, 4, v30
	v_and_b32_e32 v28, 0xf0f0f0f, v28
	v_dot4c_i32_i8_e32 v33, v28, v1
	v_and_b32_e32 v28, 0xf0f0f0f, v31
	v_dot4c_i32_i8_e32 v32, v28, v2
	v_lshrrev_b32_e32 v28, 4, v31
	v_and_b32_e32 v28, 0xf0f0f0f, v28
	v_dot4c_i32_i8_e32 v32, v28, v3
	v_sub_u32_e32 v30, v36, v84
	v_add_u32_e32 v30, v30, v37
	s_waitcnt vmcnt(18)
	v_lshlrev_b32_e32 v29, 16, v212
	v_sub_u32_e32 v31, v32, v84
	v_add_u32_e32 v32, v31, v33
	v_cvt_f32_i32_e32 v31, v30
	v_cvt_f32_i32_e32 v30, v32
	v_lshlrev_b32_e32 v28, 16, v213
	v_pk_fma_f32 v[130:131], v[28:29], v[30:31], v[130:131]
	v_and_b32_e32 v28, 0xf0f0f0f, v20
	v_mov_b32_e32 v29, 0
	v_lshrrev_b32_e32 v20, 4, v20
	v_dot4c_i32_i8_e32 v29, v28, v4
	v_and_b32_e32 v20, 0xf0f0f0f, v20
	v_dot4c_i32_i8_e32 v29, v20, v5
	v_and_b32_e32 v20, 0xf0f0f0f, v21
	v_mov_b32_e32 v28, 0
	v_dot4c_i32_i8_e32 v28, v20, v6
	v_lshrrev_b32_e32 v20, 4, v21
	v_and_b32_e32 v20, 0xf0f0f0f, v20
	v_dot4c_i32_i8_e32 v28, v20, v7
	v_and_b32_e32 v20, 0xf0f0f0f, v22
	v_dot4c_i32_i8_e32 v29, v20, v0
	v_lshrrev_b32_e32 v20, 4, v22
	v_and_b32_e32 v20, 0xf0f0f0f, v20
	v_dot4c_i32_i8_e32 v29, v20, v1
	v_and_b32_e32 v20, 0xf0f0f0f, v23
	v_dot4c_i32_i8_e32 v28, v20, v2
	v_lshrrev_b32_e32 v20, 4, v23
	v_and_b32_e32 v20, 0xf0f0f0f, v20
	v_dot4c_i32_i8_e32 v28, v20, v3
	v_and_b32_e32 v20, 0xf0f0f0f, v16
	v_mov_b32_e32 v21, 0
	v_dot4c_i32_i8_e32 v21, v20, v4
	v_lshrrev_b32_e32 v4, 4, v16
	v_and_b32_e32 v4, 0xf0f0f0f, v4
	v_dot4c_i32_i8_e32 v21, v4, v5
	v_and_b32_e32 v4, 0xf0f0f0f, v17
	v_mov_b32_e32 v5, 0
	v_dot4c_i32_i8_e32 v5, v4, v6
	v_lshrrev_b32_e32 v4, 4, v17
	v_and_b32_e32 v4, 0xf0f0f0f, v4
	v_dot4c_i32_i8_e32 v5, v4, v7
	v_and_b32_e32 v4, 0xf0f0f0f, v18
	v_dot4c_i32_i8_e32 v21, v4, v0
	v_lshrrev_b32_e32 v0, 4, v18
	v_and_b32_e32 v0, 0xf0f0f0f, v0
	v_dot4c_i32_i8_e32 v21, v0, v1
	v_and_b32_e32 v0, 0xf0f0f0f, v19
	v_dot4c_i32_i8_e32 v5, v0, v2
	v_lshrrev_b32_e32 v0, 4, v19
	v_and_b32_e32 v0, 0xf0f0f0f, v0
	v_dot4c_i32_i8_e32 v5, v0, v3
	v_sub_u32_e32 v2, v28, v84
	v_add_u32_e32 v2, v2, v29
	s_waitcnt vmcnt(16)
	v_lshlrev_b32_e32 v1, 16, v214
	v_sub_u32_e32 v3, v5, v84
	v_add_u32_e32 v4, v3, v21
	v_cvt_f32_i32_e32 v3, v2
	v_cvt_f32_i32_e32 v2, v4
	v_lshlrev_b32_e32 v0, 16, v215
	ds_read_b128 v[32:35], v166 offset:8192
	ds_read_b128 v[28:31], v166 offset:8208
	v_pk_fma_f32 v[128:129], v[0:1], v[2:3], v[128:129]
	ds_read_u16 v1, v93 offset:17024
	ds_read_u16 v2, v93 offset:17040
	ds_read_u16 v3, v93 offset:17056
	ds_read_u16 v4, v93 offset:17072
	v_mov_b32_e32 v0, 0
	s_waitcnt lgkmcnt(3)
	v_add_u32_e32 v1, s44, v1
	v_lshl_or_b32 v5, v1, 7, v165
	s_waitcnt lgkmcnt(2)
	v_add_u32_e32 v2, s44, v2
	global_load_dwordx4 v[84:87], v5, s[0:1] sc1
	v_lshl_or_b32 v5, v2, 7, v165
	s_waitcnt lgkmcnt(1)
	v_add_u32_e32 v3, s44, v3
	global_load_dwordx4 v[80:83], v5, s[0:1] sc1
	v_lshl_or_b32 v5, v3, 7, v165
	s_waitcnt lgkmcnt(0)
	v_add_u32_e32 v4, s44, v4
	global_load_dwordx4 v[68:71], v5, s[0:1] sc1
	v_lshl_or_b32 v5, v4, 7, v165
	global_load_dwordx4 v[64:67], v5, s[0:1] sc1
	ds_read_u16 v5, v93 offset:17088
	v_dot4c_i32_i8_e32 v0, 0x1010101, v32
	v_dot4c_i32_i8_e32 v0, 0x1010101, v33
	v_dot4c_i32_i8_e32 v0, 0x1010101, v34
	v_dot4c_i32_i8_e32 v0, 0x1010101, v35
	s_waitcnt lgkmcnt(0)
	v_add_u32_e32 v5, s44, v5
	v_lshl_or_b32 v6, v5, 7, v165
	global_load_dwordx4 v[52:55], v6, s[0:1] sc1
	ds_read_u16 v6, v93 offset:17104
	v_dot4c_i32_i8_e32 v0, 0x1010101, v28
	v_dot4c_i32_i8_e32 v0, 0x1010101, v29
	v_dot4c_i32_i8_e32 v0, 0x1010101, v30
	v_dot4c_i32_i8_e32 v0, 0x1010101, v31
	s_waitcnt lgkmcnt(0)
	v_add_u32_e32 v6, s44, v6
	v_lshl_or_b32 v7, v6, 7, v165
	global_load_dwordx4 v[48:51], v7, s[0:1] sc1
	ds_read_u16 v7, v93 offset:17120
	v_lshl_or_b32 v2, v2, 5, v248
	v_lshl_or_b32 v1, v1, 5, v248
	v_lshl_or_b32 v3, v3, 5, v248
	v_lshl_or_b32 v4, v4, 5, v248
	s_waitcnt lgkmcnt(0)
	v_add_u32_e32 v7, s44, v7
	v_lshl_or_b32 v16, v7, 7, v165
	global_load_dwordx4 v[40:43], v16, s[0:1] sc1
	ds_read_u16 v16, v93 offset:17136
	v_lshl_or_b32 v5, v5, 5, v248
	v_lshl_or_b32 v6, v6, 5, v248
	v_lshl_or_b32 v7, v7, 5, v248
	v_lshlrev_b32_e32 v169, 3, v0
	s_waitcnt lgkmcnt(0)
	v_add_u32_e32 v16, s44, v16
	v_lshl_or_b32 v17, v16, 7, v165
	global_load_dwordx4 v[36:39], v17, s[0:1] sc1
	v_lshl_or_b32 v16, v16, 5, v248
	global_load_dword v225, v2, s[46:47]
	global_load_dword v224, v1, s[46:47]
	global_load_dword v227, v4, s[46:47]
	global_load_dword v226, v3, s[46:47]
	global_load_dword v229, v6, s[46:47]
	global_load_dword v228, v5, s[46:47]
	global_load_dword v231, v16, s[46:47]
	global_load_dword v230, v7, s[46:47]
	s_waitcnt vmcnt(31)
	v_and_b32_e32 v0, 0xf0f0f0f, v76
	v_mov_b32_e32 v2, 0
	v_dot4c_i32_i8_e32 v2, v0, v32
	v_lshrrev_b32_e32 v0, 4, v76
	v_and_b32_e32 v0, 0xf0f0f0f, v0
	v_dot4c_i32_i8_e32 v2, v0, v33
	v_and_b32_e32 v0, 0xf0f0f0f, v77
	v_mov_b32_e32 v3, 0
	v_dot4c_i32_i8_e32 v3, v0, v34
	v_lshrrev_b32_e32 v0, 4, v77
	v_and_b32_e32 v0, 0xf0f0f0f, v0
	v_dot4c_i32_i8_e32 v3, v0, v35
	v_and_b32_e32 v0, 0xf0f0f0f, v78
	v_dot4c_i32_i8_e32 v2, v0, v28
	v_lshrrev_b32_e32 v0, 4, v78
	v_and_b32_e32 v0, 0xf0f0f0f, v0
	v_dot4c_i32_i8_e32 v2, v0, v29
	v_and_b32_e32 v0, 0xf0f0f0f, v79
	v_dot4c_i32_i8_e32 v3, v0, v30
	v_lshrrev_b32_e32 v0, 4, v79
	v_and_b32_e32 v0, 0xf0f0f0f, v0
	v_dot4c_i32_i8_e32 v3, v0, v31
	s_waitcnt vmcnt(30)
	v_and_b32_e32 v0, 0xf0f0f0f, v72
	v_mov_b32_e32 v4, 0
	v_dot4c_i32_i8_e32 v4, v0, v32
	v_lshrrev_b32_e32 v0, 4, v72
	v_and_b32_e32 v0, 0xf0f0f0f, v0
	v_dot4c_i32_i8_e32 v4, v0, v33
	v_and_b32_e32 v0, 0xf0f0f0f, v73
	v_mov_b32_e32 v5, 0
	v_dot4c_i32_i8_e32 v5, v0, v34
	v_lshrrev_b32_e32 v0, 4, v73
	v_and_b32_e32 v0, 0xf0f0f0f, v0
	v_dot4c_i32_i8_e32 v5, v0, v35
	v_and_b32_e32 v0, 0xf0f0f0f, v74
	v_dot4c_i32_i8_e32 v4, v0, v28
	v_lshrrev_b32_e32 v0, 4, v74
	v_and_b32_e32 v0, 0xf0f0f0f, v0
	v_dot4c_i32_i8_e32 v4, v0, v29
	v_and_b32_e32 v0, 0xf0f0f0f, v75
	v_dot4c_i32_i8_e32 v5, v0, v30
	v_lshrrev_b32_e32 v0, 4, v75
	v_and_b32_e32 v0, 0xf0f0f0f, v0
	v_dot4c_i32_i8_e32 v5, v0, v31
	v_add_u32_e32 v2, v2, v3
	v_sub_u32_e32 v2, v2, v169
	s_waitcnt vmcnt(22)
	v_lshlrev_b32_e32 v1, 16, v216
	v_add_u32_e32 v3, v4, v5
	v_sub_u32_e32 v4, v3, v169
	v_cvt_f32_i32_e32 v3, v2
	v_cvt_f32_i32_e32 v2, v4
	v_lshlrev_b32_e32 v0, 16, v217
	v_mov_b32_e32 v4, 0
	v_mov_b32_e32 v5, 0
	v_pk_fma_f32 v[126:127], v[0:1], v[2:3], v[126:127]
	v_and_b32_e32 v0, 0xf0f0f0f, v60
	v_mov_b32_e32 v2, 0
	v_dot4c_i32_i8_e32 v2, v0, v32
	v_lshrrev_b32_e32 v0, 4, v60
	v_and_b32_e32 v0, 0xf0f0f0f, v0
	v_dot4c_i32_i8_e32 v2, v0, v33
	v_and_b32_e32 v0, 0xf0f0f0f, v61
	v_mov_b32_e32 v3, 0
	v_dot4c_i32_i8_e32 v3, v0, v34
	v_lshrrev_b32_e32 v0, 4, v61
	v_and_b32_e32 v0, 0xf0f0f0f, v0
	v_dot4c_i32_i8_e32 v3, v0, v35
	v_and_b32_e32 v0, 0xf0f0f0f, v62
	v_dot4c_i32_i8_e32 v2, v0, v28
	v_lshrrev_b32_e32 v0, 4, v62
	v_and_b32_e32 v0, 0xf0f0f0f, v0
	v_dot4c_i32_i8_e32 v2, v0, v29
	v_and_b32_e32 v0, 0xf0f0f0f, v63
	v_dot4c_i32_i8_e32 v3, v0, v30
	v_lshrrev_b32_e32 v0, 4, v63
	v_and_b32_e32 v0, 0xf0f0f0f, v0
	v_dot4c_i32_i8_e32 v3, v0, v31
	v_and_b32_e32 v0, 0xf0f0f0f, v56
	v_dot4c_i32_i8_e32 v4, v0, v32
	v_lshrrev_b32_e32 v0, 4, v56
	v_and_b32_e32 v0, 0xf0f0f0f, v0
	v_dot4c_i32_i8_e32 v4, v0, v33
	v_and_b32_e32 v0, 0xf0f0f0f, v57
	v_dot4c_i32_i8_e32 v5, v0, v34
	v_lshrrev_b32_e32 v0, 4, v57
	v_and_b32_e32 v0, 0xf0f0f0f, v0
	v_dot4c_i32_i8_e32 v5, v0, v35
	v_and_b32_e32 v0, 0xf0f0f0f, v58
	v_dot4c_i32_i8_e32 v4, v0, v28
	v_lshrrev_b32_e32 v0, 4, v58
	v_and_b32_e32 v0, 0xf0f0f0f, v0
	v_dot4c_i32_i8_e32 v4, v0, v29
	v_and_b32_e32 v0, 0xf0f0f0f, v59
	v_dot4c_i32_i8_e32 v5, v0, v30
	v_lshrrev_b32_e32 v0, 4, v59
	v_and_b32_e32 v0, 0xf0f0f0f, v0
	v_dot4c_i32_i8_e32 v5, v0, v31
	v_add_u32_e32 v2, v2, v3
	v_sub_u32_e32 v2, v2, v169
	s_waitcnt vmcnt(20)
	v_lshlrev_b32_e32 v1, 16, v218
	v_add_u32_e32 v3, v4, v5
	v_sub_u32_e32 v4, v3, v169
	v_cvt_f32_i32_e32 v3, v2
	v_cvt_f32_i32_e32 v2, v4
	v_lshlrev_b32_e32 v0, 16, v219
	v_mov_b32_e32 v4, 0
	v_mov_b32_e32 v5, 0
	v_pk_fma_f32 v[124:125], v[0:1], v[2:3], v[124:125]
	v_and_b32_e32 v0, 0xf0f0f0f, v44
	v_mov_b32_e32 v2, 0
	v_dot4c_i32_i8_e32 v2, v0, v32
	v_lshrrev_b32_e32 v0, 4, v44
	v_and_b32_e32 v0, 0xf0f0f0f, v0
	v_dot4c_i32_i8_e32 v2, v0, v33
	v_and_b32_e32 v0, 0xf0f0f0f, v45
	v_mov_b32_e32 v3, 0
	v_dot4c_i32_i8_e32 v3, v0, v34
	v_lshrrev_b32_e32 v0, 4, v45
	v_and_b32_e32 v0, 0xf0f0f0f, v0
	v_dot4c_i32_i8_e32 v3, v0, v35
	v_and_b32_e32 v0, 0xf0f0f0f, v46
	v_dot4c_i32_i8_e32 v2, v0, v28
	v_lshrrev_b32_e32 v0, 4, v46
	v_and_b32_e32 v0, 0xf0f0f0f, v0
	v_dot4c_i32_i8_e32 v2, v0, v29
	v_and_b32_e32 v0, 0xf0f0f0f, v47
	v_dot4c_i32_i8_e32 v3, v0, v30
	v_lshrrev_b32_e32 v0, 4, v47
	v_and_b32_e32 v0, 0xf0f0f0f, v0
	v_dot4c_i32_i8_e32 v3, v0, v31
	v_and_b32_e32 v0, 0xf0f0f0f, v24
	v_dot4c_i32_i8_e32 v4, v0, v32
	v_lshrrev_b32_e32 v0, 4, v24
	v_and_b32_e32 v0, 0xf0f0f0f, v0
	v_dot4c_i32_i8_e32 v4, v0, v33
	v_and_b32_e32 v0, 0xf0f0f0f, v25
	v_dot4c_i32_i8_e32 v5, v0, v34
	v_lshrrev_b32_e32 v0, 4, v25
	v_and_b32_e32 v0, 0xf0f0f0f, v0
	v_dot4c_i32_i8_e32 v5, v0, v35
	v_and_b32_e32 v0, 0xf0f0f0f, v26
	v_dot4c_i32_i8_e32 v4, v0, v28
	v_lshrrev_b32_e32 v0, 4, v26
	v_and_b32_e32 v0, 0xf0f0f0f, v0
	v_dot4c_i32_i8_e32 v4, v0, v29
	v_and_b32_e32 v0, 0xf0f0f0f, v27
	v_dot4c_i32_i8_e32 v5, v0, v30
	v_lshrrev_b32_e32 v0, 4, v27
	v_and_b32_e32 v0, 0xf0f0f0f, v0
	v_dot4c_i32_i8_e32 v5, v0, v31
	v_add_u32_e32 v2, v2, v3
	v_sub_u32_e32 v2, v2, v169
	s_waitcnt vmcnt(18)
	v_lshlrev_b32_e32 v1, 16, v220
	v_add_u32_e32 v3, v4, v5
	v_sub_u32_e32 v4, v3, v169
	v_cvt_f32_i32_e32 v3, v2
	v_cvt_f32_i32_e32 v2, v4
	v_lshlrev_b32_e32 v0, 16, v221
	v_mov_b32_e32 v4, 0
	v_mov_b32_e32 v5, 0
	v_pk_fma_f32 v[122:123], v[0:1], v[2:3], v[122:123]
	v_and_b32_e32 v0, 0xf0f0f0f, v12
	v_mov_b32_e32 v2, 0
	v_dot4c_i32_i8_e32 v2, v0, v32
	v_lshrrev_b32_e32 v0, 4, v12
	v_and_b32_e32 v0, 0xf0f0f0f, v0
	v_dot4c_i32_i8_e32 v2, v0, v33
	v_and_b32_e32 v0, 0xf0f0f0f, v13
	v_mov_b32_e32 v3, 0
	v_dot4c_i32_i8_e32 v3, v0, v34
	v_lshrrev_b32_e32 v0, 4, v13
	v_and_b32_e32 v0, 0xf0f0f0f, v0
	v_dot4c_i32_i8_e32 v3, v0, v35
	v_and_b32_e32 v0, 0xf0f0f0f, v14
	v_dot4c_i32_i8_e32 v2, v0, v28
	v_lshrrev_b32_e32 v0, 4, v14
	v_and_b32_e32 v0, 0xf0f0f0f, v0
	v_dot4c_i32_i8_e32 v2, v0, v29
	v_and_b32_e32 v0, 0xf0f0f0f, v15
	v_dot4c_i32_i8_e32 v3, v0, v30
	v_lshrrev_b32_e32 v0, 4, v15
	v_and_b32_e32 v0, 0xf0f0f0f, v0
	v_dot4c_i32_i8_e32 v3, v0, v31
	v_and_b32_e32 v0, 0xf0f0f0f, v8
	v_dot4c_i32_i8_e32 v4, v0, v32
	v_lshrrev_b32_e32 v0, 4, v8
	v_and_b32_e32 v0, 0xf0f0f0f, v0
	v_dot4c_i32_i8_e32 v4, v0, v33
	v_and_b32_e32 v0, 0xf0f0f0f, v9
	v_dot4c_i32_i8_e32 v5, v0, v34
	v_lshrrev_b32_e32 v0, 4, v9
	v_and_b32_e32 v0, 0xf0f0f0f, v0
	v_dot4c_i32_i8_e32 v5, v0, v35
	v_and_b32_e32 v0, 0xf0f0f0f, v10
	v_dot4c_i32_i8_e32 v4, v0, v28
	v_lshrrev_b32_e32 v0, 4, v10
	v_and_b32_e32 v0, 0xf0f0f0f, v0
	v_dot4c_i32_i8_e32 v4, v0, v29
	v_and_b32_e32 v0, 0xf0f0f0f, v11
	v_dot4c_i32_i8_e32 v5, v0, v30
	v_lshrrev_b32_e32 v0, 4, v11
	v_and_b32_e32 v0, 0xf0f0f0f, v0
	v_dot4c_i32_i8_e32 v5, v0, v31
	v_add_u32_e32 v2, v2, v3
	v_sub_u32_e32 v2, v2, v169
	s_waitcnt vmcnt(16)
	v_lshlrev_b32_e32 v1, 16, v222
	v_add_u32_e32 v3, v4, v5
	v_sub_u32_e32 v4, v3, v169
	v_cvt_f32_i32_e32 v3, v2
	v_cvt_f32_i32_e32 v2, v4
	v_lshlrev_b32_e32 v0, 16, v223
	v_pk_fma_f32 v[120:121], v[0:1], v[2:3], v[120:121]
	ds_read_u16 v0, v93 offset:17152
	ds_read_u16 v1, v93 offset:17168
	ds_read_u16 v2, v93 offset:17184
	ds_read_u16 v3, v93 offset:17200
	s_waitcnt lgkmcnt(3)
	v_add_u32_e32 v0, s44, v0
	v_lshl_or_b32 v4, v0, 7, v165
	v_lshl_or_b32 v44, v0, 5, v248
	s_waitcnt lgkmcnt(2)
	v_add_u32_e32 v0, s44, v1
	v_lshl_or_b32 v1, v0, 7, v165
	v_lshl_or_b32 v45, v0, 5, v248
	s_waitcnt lgkmcnt(1)
	v_add_u32_e32 v0, s44, v2
	global_load_dwordx4 v[72:75], v4, s[0:1] sc1
	global_load_dwordx4 v[24:27], v1, s[0:1] sc1
	v_lshl_or_b32 v1, v0, 7, v165
	v_lshl_or_b32 v46, v0, 5, v248
	s_waitcnt lgkmcnt(0)
	v_add_u32_e32 v0, s44, v3
	global_load_dwordx4 v[20:23], v1, s[0:1] sc1
	v_lshl_or_b32 v1, v0, 7, v165
	v_lshl_or_b32 v47, v0, 5, v248
	ds_read_u16 v0, v93 offset:17216
	global_load_dwordx4 v[16:19], v1, s[0:1] sc1
	s_waitcnt lgkmcnt(0)
	v_add_u32_e32 v0, s44, v0
	v_lshl_or_b32 v1, v0, 7, v165
	v_lshl_or_b32 v56, v0, 5, v248
	ds_read_u16 v0, v93 offset:17232
	global_load_dwordx4 v[12:15], v1, s[0:1] sc1
	s_waitcnt lgkmcnt(0)
	v_add_u32_e32 v0, s44, v0
	v_lshl_or_b32 v1, v0, 7, v165
	v_lshl_or_b32 v57, v0, 5, v248
	ds_read_u16 v0, v93 offset:17248
	global_load_dwordx4 v[8:11], v1, s[0:1] sc1
	s_waitcnt lgkmcnt(0)
	v_add_u32_e32 v0, s44, v0
	v_lshl_or_b32 v1, v0, 7, v165
	v_lshl_or_b32 v58, v0, 5, v248
	ds_read_u16 v0, v93 offset:17264
	global_load_dwordx4 v[4:7], v1, s[0:1] sc1
	s_waitcnt lgkmcnt(0)
	v_add_u32_e32 v59, s44, v0
	v_lshl_or_b32 v0, v59, 7, v165
	global_load_dwordx4 v[0:3], v0, s[0:1] sc1
	v_lshl_or_b32 v59, v59, 5, v248
	global_load_dword v233, v45, s[46:47]
	global_load_dword v232, v44, s[46:47]
	global_load_dword v235, v47, s[46:47]
	global_load_dword v234, v46, s[46:47]
	global_load_dword v236, v56, s[46:47]
	global_load_dword v237, v57, s[46:47]
	global_load_dword v238, v58, s[46:47]
	global_load_dword v239, v59, s[46:47]
	s_waitcnt vmcnt(31)
	v_and_b32_e32 v44, 0xf0f0f0f, v84
	v_mov_b32_e32 v46, 0
	v_dot4c_i32_i8_e32 v46, v44, v32
	v_lshrrev_b32_e32 v44, 4, v84
	v_and_b32_e32 v44, 0xf0f0f0f, v44
	v_dot4c_i32_i8_e32 v46, v44, v33
	v_and_b32_e32 v44, 0xf0f0f0f, v85
	v_mov_b32_e32 v47, 0
	v_dot4c_i32_i8_e32 v47, v44, v34
	v_lshrrev_b32_e32 v44, 4, v85
	v_and_b32_e32 v44, 0xf0f0f0f, v44
	v_dot4c_i32_i8_e32 v47, v44, v35
	v_and_b32_e32 v44, 0xf0f0f0f, v86
	v_dot4c_i32_i8_e32 v46, v44, v28
	v_lshrrev_b32_e32 v44, 4, v86
	v_and_b32_e32 v44, 0xf0f0f0f, v44
	v_dot4c_i32_i8_e32 v46, v44, v29
	v_and_b32_e32 v44, 0xf0f0f0f, v87
	v_dot4c_i32_i8_e32 v47, v44, v30
	v_lshrrev_b32_e32 v44, 4, v87
	v_and_b32_e32 v44, 0xf0f0f0f, v44
	v_dot4c_i32_i8_e32 v47, v44, v31
	s_waitcnt vmcnt(30)
	v_and_b32_e32 v44, 0xf0f0f0f, v80
	v_mov_b32_e32 v56, 0
	v_dot4c_i32_i8_e32 v56, v44, v32
	v_lshrrev_b32_e32 v44, 4, v80
	v_and_b32_e32 v44, 0xf0f0f0f, v44
	v_dot4c_i32_i8_e32 v56, v44, v33
	v_and_b32_e32 v44, 0xf0f0f0f, v81
	v_mov_b32_e32 v57, 0
	v_dot4c_i32_i8_e32 v57, v44, v34
	v_lshrrev_b32_e32 v44, 4, v81
	v_and_b32_e32 v44, 0xf0f0f0f, v44
	v_dot4c_i32_i8_e32 v57, v44, v35
	v_and_b32_e32 v44, 0xf0f0f0f, v82
	v_dot4c_i32_i8_e32 v56, v44, v28
	v_lshrrev_b32_e32 v44, 4, v82
	v_and_b32_e32 v44, 0xf0f0f0f, v44
	v_dot4c_i32_i8_e32 v56, v44, v29
	v_and_b32_e32 v44, 0xf0f0f0f, v83
	v_dot4c_i32_i8_e32 v57, v44, v30
	v_lshrrev_b32_e32 v44, 4, v83
	v_and_b32_e32 v44, 0xf0f0f0f, v44
	v_dot4c_i32_i8_e32 v57, v44, v31
	v_add_u32_e32 v46, v46, v47
	v_sub_u32_e32 v46, v46, v169
	s_waitcnt vmcnt(22)
	v_lshlrev_b32_e32 v45, 16, v224
	v_sub_u32_e32 v47, v57, v169
	v_add_u32_e32 v56, v47, v56
	v_cvt_f32_i32_e32 v47, v46
	v_cvt_f32_i32_e32 v46, v56
	v_lshlrev_b32_e32 v44, 16, v225
	v_mov_b32_e32 v56, 0
	v_mov_b32_e32 v57, 0
	v_pk_fma_f32 v[118:119], v[44:45], v[46:47], v[118:119]
	v_and_b32_e32 v44, 0xf0f0f0f, v68
	v_mov_b32_e32 v46, 0
	v_dot4c_i32_i8_e32 v46, v44, v32
	v_lshrrev_b32_e32 v44, 4, v68
	v_and_b32_e32 v44, 0xf0f0f0f, v44
	v_dot4c_i32_i8_e32 v46, v44, v33
	v_and_b32_e32 v44, 0xf0f0f0f, v69
	v_mov_b32_e32 v47, 0
	v_dot4c_i32_i8_e32 v47, v44, v34
	v_lshrrev_b32_e32 v44, 4, v69
	v_and_b32_e32 v44, 0xf0f0f0f, v44
	v_dot4c_i32_i8_e32 v47, v44, v35
	v_and_b32_e32 v44, 0xf0f0f0f, v70
	v_dot4c_i32_i8_e32 v46, v44, v28
	v_lshrrev_b32_e32 v44, 4, v70
	v_and_b32_e32 v44, 0xf0f0f0f, v44
	v_dot4c_i32_i8_e32 v46, v44, v29
	v_and_b32_e32 v44, 0xf0f0f0f, v71
	v_dot4c_i32_i8_e32 v47, v44, v30
	v_lshrrev_b32_e32 v44, 4, v71
	v_and_b32_e32 v44, 0xf0f0f0f, v44
	v_dot4c_i32_i8_e32 v47, v44, v31
	v_and_b32_e32 v44, 0xf0f0f0f, v64
	v_dot4c_i32_i8_e32 v56, v44, v32
	v_lshrrev_b32_e32 v44, 4, v64
	v_and_b32_e32 v44, 0xf0f0f0f, v44
	v_dot4c_i32_i8_e32 v56, v44, v33
	v_and_b32_e32 v44, 0xf0f0f0f, v65
	v_dot4c_i32_i8_e32 v57, v44, v34
	v_lshrrev_b32_e32 v44, 4, v65
	v_and_b32_e32 v44, 0xf0f0f0f, v44
	v_dot4c_i32_i8_e32 v57, v44, v35
	v_and_b32_e32 v44, 0xf0f0f0f, v66
	v_dot4c_i32_i8_e32 v56, v44, v28
	v_lshrrev_b32_e32 v44, 4, v66
	v_and_b32_e32 v44, 0xf0f0f0f, v44
	v_dot4c_i32_i8_e32 v56, v44, v29
	v_and_b32_e32 v44, 0xf0f0f0f, v67
	v_dot4c_i32_i8_e32 v57, v44, v30
	v_lshrrev_b32_e32 v44, 4, v67
	v_and_b32_e32 v44, 0xf0f0f0f, v44
	v_dot4c_i32_i8_e32 v57, v44, v31
	v_sub_u32_e32 v47, v47, v169
	v_add_u32_e32 v46, v47, v46
	v_cvt_f32_i32_e32 v47, v46
	v_sub_u32_e32 v57, v57, v169
	v_add_u32_e32 v56, v57, v56
	v_cvt_f32_i32_e32 v46, v56
	s_waitcnt vmcnt(20)
	v_lshlrev_b32_e32 v45, 16, v226
	v_lshlrev_b32_e32 v44, 16, v227
	v_pk_fma_f32 v[116:117], v[44:45], v[46:47], v[116:117]
	v_and_b32_e32 v44, 0xf0f0f0f, v52
	v_mov_b32_e32 v46, 0
	v_dot4c_i32_i8_e32 v46, v44, v32
	v_lshrrev_b32_e32 v44, 4, v52
	v_and_b32_e32 v44, 0xf0f0f0f, v44
	v_dot4c_i32_i8_e32 v46, v44, v33
	v_and_b32_e32 v44, 0xf0f0f0f, v53
	v_mov_b32_e32 v47, 0
	v_dot4c_i32_i8_e32 v47, v44, v34
	v_lshrrev_b32_e32 v44, 4, v53
	v_and_b32_e32 v44, 0xf0f0f0f, v44
	v_dot4c_i32_i8_e32 v47, v44, v35
	v_and_b32_e32 v44, 0xf0f0f0f, v54
	v_dot4c_i32_i8_e32 v46, v44, v28
	v_lshrrev_b32_e32 v44, 4, v54
	v_and_b32_e32 v44, 0xf0f0f0f, v44
	v_dot4c_i32_i8_e32 v46, v44, v29
	v_and_b32_e32 v44, 0xf0f0f0f, v55
	v_dot4c_i32_i8_e32 v47, v44, v30
	v_lshrrev_b32_e32 v44, 4, v55
	v_and_b32_e32 v44, 0xf0f0f0f, v44
	v_dot4c_i32_i8_e32 v47, v44, v31
	v_and_b32_e32 v44, 0xf0f0f0f, v48
	v_mov_b32_e32 v52, 0
	v_dot4c_i32_i8_e32 v52, v44, v32
	v_lshrrev_b32_e32 v44, 4, v48
	v_and_b32_e32 v44, 0xf0f0f0f, v44
	v_dot4c_i32_i8_e32 v52, v44, v33
	v_and_b32_e32 v44, 0xf0f0f0f, v49
	v_mov_b32_e32 v48, 0
	v_dot4c_i32_i8_e32 v48, v44, v34
	v_lshrrev_b32_e32 v44, 4, v49
	v_and_b32_e32 v44, 0xf0f0f0f, v44
	v_dot4c_i32_i8_e32 v48, v44, v35
	v_and_b32_e32 v44, 0xf0f0f0f, v50
	v_dot4c_i32_i8_e32 v52, v44, v28
	v_lshrrev_b32_e32 v44, 4, v50
	v_and_b32_e32 v44, 0xf0f0f0f, v44
	v_dot4c_i32_i8_e32 v52, v44, v29
	v_and_b32_e32 v44, 0xf0f0f0f, v51
	v_dot4c_i32_i8_e32 v48, v44, v30
	v_lshrrev_b32_e32 v44, 4, v51
	v_and_b32_e32 v44, 0xf0f0f0f, v44
	v_dot4c_i32_i8_e32 v48, v44, v31
	v_sub_u32_e32 v47, v47, v169
	v_add_u32_e32 v46, v47, v46
	v_cvt_f32_i32_e32 v47, v46
	v_sub_u32_e32 v48, v48, v169
	v_add_u32_e32 v48, v48, v52
	v_cvt_f32_i32_e32 v46, v48
	s_waitcnt vmcnt(18)
	v_lshlrev_b32_e32 v45, 16, v228
	v_lshlrev_b32_e32 v44, 16, v229
	v_pk_fma_f32 v[114:115], v[44:45], v[46:47], v[114:115]
	v_and_b32_e32 v44, 0xf0f0f0f, v40
	v_mov_b32_e32 v45, 0
	v_lshrrev_b32_e32 v40, 4, v40
	v_dot4c_i32_i8_e32 v45, v44, v32
	v_and_b32_e32 v40, 0xf0f0f0f, v40
	v_dot4c_i32_i8_e32 v45, v40, v33
	v_and_b32_e32 v40, 0xf0f0f0f, v41
	v_mov_b32_e32 v44, 0
	v_dot4c_i32_i8_e32 v44, v40, v34
	v_lshrrev_b32_e32 v40, 4, v41
	v_and_b32_e32 v40, 0xf0f0f0f, v40
	v_dot4c_i32_i8_e32 v44, v40, v35
	v_and_b32_e32 v40, 0xf0f0f0f, v42
	v_dot4c_i32_i8_e32 v45, v40, v28
	v_lshrrev_b32_e32 v40, 4, v42
	v_and_b32_e32 v40, 0xf0f0f0f, v40
	v_dot4c_i32_i8_e32 v45, v40, v29
	v_and_b32_e32 v40, 0xf0f0f0f, v43
	v_dot4c_i32_i8_e32 v44, v40, v30
	v_lshrrev_b32_e32 v40, 4, v43
	v_and_b32_e32 v40, 0xf0f0f0f, v40
	v_dot4c_i32_i8_e32 v44, v40, v31
	v_and_b32_e32 v40, 0xf0f0f0f, v36
	v_mov_b32_e32 v41, 0
	v_dot4c_i32_i8_e32 v41, v40, v32
	v_lshrrev_b32_e32 v32, 4, v36
	v_and_b32_e32 v32, 0xf0f0f0f, v32
	v_dot4c_i32_i8_e32 v41, v32, v33
	v_and_b32_e32 v32, 0xf0f0f0f, v37
	v_mov_b32_e32 v33, 0
	v_dot4c_i32_i8_e32 v33, v32, v34
	v_lshrrev_b32_e32 v32, 4, v37
	v_and_b32_e32 v32, 0xf0f0f0f, v32
	v_dot4c_i32_i8_e32 v33, v32, v35
	v_and_b32_e32 v32, 0xf0f0f0f, v38
	v_dot4c_i32_i8_e32 v41, v32, v28
	v_lshrrev_b32_e32 v28, 4, v38
	v_and_b32_e32 v28, 0xf0f0f0f, v28
	v_dot4c_i32_i8_e32 v41, v28, v29
	v_and_b32_e32 v28, 0xf0f0f0f, v39
	v_dot4c_i32_i8_e32 v33, v28, v30
	v_lshrrev_b32_e32 v28, 4, v39
	v_and_b32_e32 v28, 0xf0f0f0f, v28
	v_dot4c_i32_i8_e32 v33, v28, v31
	v_sub_u32_e32 v30, v44, v169
	v_add_u32_e32 v30, v30, v45
	s_waitcnt vmcnt(16)
	v_lshlrev_b32_e32 v29, 16, v230
	v_sub_u32_e32 v31, v33, v169
	v_add_u32_e32 v32, v31, v41
	v_cvt_f32_i32_e32 v31, v30
	v_cvt_f32_i32_e32 v30, v32
	v_lshlrev_b32_e32 v28, 16, v231
	ds_read_b128 v[36:39], v166 offset:12288
	ds_read_b128 v[32:35], v166 offset:12304
	v_add_u32_e32 v166, 0x100, v166
	v_pk_fma_f32 v[112:113], v[28:29], v[30:31], v[112:113]
	ds_read_u16 v29, v93 offset:17280
	ds_read_u16 v30, v93 offset:17296
	ds_read_u16 v31, v93 offset:17312
	ds_read_u16 v40, v93 offset:17328
	v_mov_b32_e32 v28, 0
	s_waitcnt lgkmcnt(3)
	v_add_u32_e32 v29, s44, v29
	v_lshl_or_b32 v41, v29, 7, v165
	s_waitcnt lgkmcnt(2)
	v_add_u32_e32 v30, s44, v30
	global_load_dwordx4 v[68:71], v41, s[0:1] sc1
	v_lshl_or_b32 v41, v30, 7, v165
	s_waitcnt lgkmcnt(1)
	v_add_u32_e32 v31, s44, v31
	global_load_dwordx4 v[64:67], v41, s[0:1] sc1
	v_lshl_or_b32 v41, v31, 7, v165
	s_waitcnt lgkmcnt(0)
	v_add_u32_e32 v40, s44, v40
	global_load_dwordx4 v[60:63], v41, s[0:1] sc1
	v_lshl_or_b32 v41, v40, 7, v165
	v_lshl_or_b32 v79, v40, 5, v248
	ds_read_u16 v40, v93 offset:17344
	global_load_dwordx4 v[56:59], v41, s[0:1] sc1
	v_dot4c_i32_i8_e32 v28, 0x1010101, v36
	v_dot4c_i32_i8_e32 v28, 0x1010101, v37
	v_dot4c_i32_i8_e32 v28, 0x1010101, v38
	s_waitcnt lgkmcnt(0)
	v_add_u32_e32 v40, s44, v40
	v_lshl_or_b32 v41, v40, 7, v165
	v_lshl_or_b32 v80, v40, 5, v248
	ds_read_u16 v40, v93 offset:17360
	global_load_dwordx4 v[52:55], v41, s[0:1] sc1
	v_dot4c_i32_i8_e32 v28, 0x1010101, v39
	v_dot4c_i32_i8_e32 v28, 0x1010101, v32
	v_dot4c_i32_i8_e32 v28, 0x1010101, v33
	s_waitcnt lgkmcnt(0)
	v_add_u32_e32 v40, s44, v40
	v_lshl_or_b32 v41, v40, 7, v165
	v_lshl_or_b32 v82, v40, 5, v248
	ds_read_u16 v40, v93 offset:17376
	global_load_dwordx4 v[48:51], v41, s[0:1] sc1
	v_dot4c_i32_i8_e32 v28, 0x1010101, v34
	v_dot4c_i32_i8_e32 v28, 0x1010101, v35
	v_lshl_or_b32 v29, v29, 5, v248
	s_waitcnt lgkmcnt(0)
	v_add_u32_e32 v40, s44, v40
	v_lshl_or_b32 v41, v40, 7, v165
	v_lshl_or_b32 v87, v40, 5, v248
	ds_read_u16 v40, v93 offset:17392
	v_lshl_or_b32 v30, v30, 5, v248
	v_lshl_or_b32 v31, v31, 5, v248
	global_load_dwordx4 v[44:47], v41, s[0:1] sc1
	s_waitcnt lgkmcnt(0)
; #define P12_ISSUE(c_, i_, h_, CW_, SC_) do { _Pragma("unroll") for (int bb = 0; bb < 8; ++bb) { const unsigned ro = (unsigned)(c_) * 16384u + (unsigned)EL[(i_) * 128 + ((h_) * 8 + bb) * 8 + g8]; \
;         CW_[bb] = *(const v4u*)(U4 + (size_t)(ro * 128u + 16u * (unsigned)k8)); SC_[bb] = USS[(size_t)(ro * 8u + (unsigned)k8)]; } } while (0)
; __device__ __forceinline__ void p12_peer(Frame& F) {
;     ...
;     { v4u cwA[8], cwB[8]; unsigned scA[8], scB[8]; v4u xa, xb; int xo;
;       P12_ISSUE(0, 0, 0, cwA, scA);
; _Pragma("nounroll")
;       for (int c = 0; c < 16; ++c) { const int cn = c + 1 < 16 ? c + 1 : 15;
	v_add_u32_e32 v78, s44, v40
	v_lshl_or_b32 v40, v78, 7, v165
	global_load_dwordx4 v[40:43], v40, s[0:1] sc1
	v_lshl_or_b32 v169, v78, 5, v248
	v_lshlrev_b32_e32 v78, 3, v28
	global_load_dword v240, v29, s[46:47]
	global_load_dword v241, v30, s[46:47]
	global_load_dword v242, v31, s[46:47]
	global_load_dword v243, v79, s[46:47]
	global_load_dword v244, v80, s[46:47]
	s_nop 0
	global_load_dword v245, v82, s[46:47]
	s_nop 0
	global_load_dword v246, v87, s[46:47]
	global_load_dword v247, v169, s[46:47]
	s_waitcnt vmcnt(31)
	v_and_b32_e32 v29, 0xf0f0f0f, v72
	v_mov_b32_e32 v28, 0
	v_dot4c_i32_i8_e32 v28, v29, v36
	v_lshrrev_b32_e32 v29, 4, v72
	v_and_b32_e32 v29, 0xf0f0f0f, v29
	v_dot4c_i32_i8_e32 v28, v29, v37
	v_and_b32_e32 v30, 0xf0f0f0f, v73
	v_mov_b32_e32 v29, 0
	v_dot4c_i32_i8_e32 v29, v30, v38
	v_lshrrev_b32_e32 v30, 4, v73
	v_and_b32_e32 v30, 0xf0f0f0f, v30
	v_dot4c_i32_i8_e32 v29, v30, v39
	v_and_b32_e32 v30, 0xf0f0f0f, v74
	v_dot4c_i32_i8_e32 v28, v30, v32
	v_lshrrev_b32_e32 v30, 4, v74
	v_and_b32_e32 v30, 0xf0f0f0f, v30
	v_dot4c_i32_i8_e32 v28, v30, v33
	v_and_b32_e32 v30, 0xf0f0f0f, v75
	v_dot4c_i32_i8_e32 v29, v30, v34
	v_lshrrev_b32_e32 v30, 4, v75
	v_and_b32_e32 v30, 0xf0f0f0f, v30
	v_dot4c_i32_i8_e32 v29, v30, v35
	s_waitcnt vmcnt(30)
	v_and_b32_e32 v31, 0xf0f0f0f, v24
	v_mov_b32_e32 v30, 0
	v_lshrrev_b32_e32 v24, 4, v24
	v_dot4c_i32_i8_e32 v30, v31, v36
	v_and_b32_e32 v24, 0xf0f0f0f, v24
	v_dot4c_i32_i8_e32 v30, v24, v37
	v_and_b32_e32 v24, 0xf0f0f0f, v25
	v_mov_b32_e32 v31, 0
	v_dot4c_i32_i8_e32 v31, v24, v38
	v_lshrrev_b32_e32 v24, 4, v25
	v_and_b32_e32 v24, 0xf0f0f0f, v24
	v_dot4c_i32_i8_e32 v31, v24, v39
	v_and_b32_e32 v24, 0xf0f0f0f, v26
	v_dot4c_i32_i8_e32 v30, v24, v32
	v_lshrrev_b32_e32 v24, 4, v26
	v_and_b32_e32 v24, 0xf0f0f0f, v24
	v_dot4c_i32_i8_e32 v30, v24, v33
	v_and_b32_e32 v24, 0xf0f0f0f, v27
	v_dot4c_i32_i8_e32 v31, v24, v34
	v_lshrrev_b32_e32 v24, 4, v27
	v_and_b32_e32 v24, 0xf0f0f0f, v24
	v_dot4c_i32_i8_e32 v31, v24, v35
	v_add_u32_e32 v26, v28, v29
	v_sub_u32_e32 v26, v26, v78
	s_waitcnt vmcnt(22)
	v_lshlrev_b32_e32 v25, 16, v232
	v_add_u32_e32 v27, v30, v31
	v_sub_u32_e32 v28, v27, v78
	v_cvt_f32_i32_e32 v27, v26
	v_cvt_f32_i32_e32 v26, v28
	v_lshlrev_b32_e32 v24, 16, v233
	s_cselect_b32 s44, s44, s45
	v_pk_fma_f32 v[110:111], v[24:25], v[26:27], v[110:111]
	v_and_b32_e32 v24, 0xf0f0f0f, v20
	v_mov_b32_e32 v25, 0
	v_lshrrev_b32_e32 v20, 4, v20
	v_dot4c_i32_i8_e32 v25, v24, v36
	v_and_b32_e32 v20, 0xf0f0f0f, v20
	v_dot4c_i32_i8_e32 v25, v20, v37
	v_and_b32_e32 v20, 0xf0f0f0f, v21
	v_mov_b32_e32 v24, 0
	v_dot4c_i32_i8_e32 v24, v20, v38
	v_lshrrev_b32_e32 v20, 4, v21
	v_and_b32_e32 v20, 0xf0f0f0f, v20
	v_dot4c_i32_i8_e32 v24, v20, v39
	v_and_b32_e32 v20, 0xf0f0f0f, v22
	v_dot4c_i32_i8_e32 v25, v20, v32
	v_lshrrev_b32_e32 v20, 4, v22
	v_and_b32_e32 v20, 0xf0f0f0f, v20
	v_dot4c_i32_i8_e32 v25, v20, v33
	v_and_b32_e32 v20, 0xf0f0f0f, v23
	v_dot4c_i32_i8_e32 v24, v20, v34
	v_lshrrev_b32_e32 v20, 4, v23
	v_and_b32_e32 v20, 0xf0f0f0f, v20
	v_dot4c_i32_i8_e32 v24, v20, v35
	v_and_b32_e32 v20, 0xf0f0f0f, v16
	v_mov_b32_e32 v21, 0
	v_lshrrev_b32_e32 v16, 4, v16
	v_dot4c_i32_i8_e32 v21, v20, v36
	v_and_b32_e32 v16, 0xf0f0f0f, v16
	v_dot4c_i32_i8_e32 v21, v16, v37
	v_and_b32_e32 v16, 0xf0f0f0f, v17
	v_mov_b32_e32 v20, 0
	v_dot4c_i32_i8_e32 v20, v16, v38
	v_lshrrev_b32_e32 v16, 4, v17
	v_and_b32_e32 v16, 0xf0f0f0f, v16
	v_dot4c_i32_i8_e32 v20, v16, v39
	v_and_b32_e32 v16, 0xf0f0f0f, v18
	v_dot4c_i32_i8_e32 v21, v16, v32
	v_lshrrev_b32_e32 v16, 4, v18
	v_and_b32_e32 v16, 0xf0f0f0f, v16
	v_dot4c_i32_i8_e32 v21, v16, v33
	v_and_b32_e32 v16, 0xf0f0f0f, v19
	v_dot4c_i32_i8_e32 v20, v16, v34
	v_lshrrev_b32_e32 v16, 4, v19
	v_and_b32_e32 v16, 0xf0f0f0f, v16
	v_dot4c_i32_i8_e32 v20, v16, v35
	v_add_u32_e32 v18, v25, v24
	v_sub_u32_e32 v18, v18, v78
	s_waitcnt vmcnt(20)
	v_lshlrev_b32_e32 v17, 16, v234
	v_add_u32_e32 v19, v21, v20
	v_sub_u32_e32 v20, v19, v78
	v_cvt_f32_i32_e32 v19, v18
	v_cvt_f32_i32_e32 v18, v20
	v_lshlrev_b32_e32 v16, 16, v235
	v_mov_b32_e32 v90, 0
	s_cmp_eq_u32 s45, 0x40000
	v_pk_fma_f32 v[108:109], v[16:17], v[18:19], v[108:109]
	v_and_b32_e32 v16, 0xf0f0f0f, v12
	v_mov_b32_e32 v17, 0
	v_lshrrev_b32_e32 v12, 4, v12
	v_dot4c_i32_i8_e32 v17, v16, v36
	v_and_b32_e32 v12, 0xf0f0f0f, v12
	v_dot4c_i32_i8_e32 v17, v12, v37
	v_and_b32_e32 v12, 0xf0f0f0f, v13
	v_mov_b32_e32 v16, 0
	v_dot4c_i32_i8_e32 v16, v12, v38
	v_lshrrev_b32_e32 v12, 4, v13
	v_and_b32_e32 v12, 0xf0f0f0f, v12
	v_dot4c_i32_i8_e32 v16, v12, v39
	v_and_b32_e32 v12, 0xf0f0f0f, v14
	v_dot4c_i32_i8_e32 v17, v12, v32
	v_lshrrev_b32_e32 v12, 4, v14
	v_and_b32_e32 v12, 0xf0f0f0f, v12
	v_dot4c_i32_i8_e32 v17, v12, v33
	v_and_b32_e32 v12, 0xf0f0f0f, v15
	v_dot4c_i32_i8_e32 v16, v12, v34
	v_lshrrev_b32_e32 v12, 4, v15
	v_and_b32_e32 v12, 0xf0f0f0f, v12
	v_dot4c_i32_i8_e32 v16, v12, v35
	v_and_b32_e32 v12, 0xf0f0f0f, v8
	v_mov_b32_e32 v13, 0
	v_lshrrev_b32_e32 v8, 4, v8
	v_dot4c_i32_i8_e32 v13, v12, v36
	v_and_b32_e32 v8, 0xf0f0f0f, v8
	v_dot4c_i32_i8_e32 v13, v8, v37
	v_and_b32_e32 v8, 0xf0f0f0f, v9
	v_mov_b32_e32 v12, 0
	v_dot4c_i32_i8_e32 v12, v8, v38
	v_lshrrev_b32_e32 v8, 4, v9
	v_and_b32_e32 v8, 0xf0f0f0f, v8
	v_dot4c_i32_i8_e32 v12, v8, v39
	v_and_b32_e32 v8, 0xf0f0f0f, v10
	v_dot4c_i32_i8_e32 v13, v8, v32
	v_lshrrev_b32_e32 v8, 4, v10
	v_and_b32_e32 v8, 0xf0f0f0f, v8
	v_dot4c_i32_i8_e32 v13, v8, v33
	v_and_b32_e32 v8, 0xf0f0f0f, v11
	v_dot4c_i32_i8_e32 v12, v8, v34
	v_lshrrev_b32_e32 v8, 4, v11
	v_and_b32_e32 v8, 0xf0f0f0f, v8
	v_dot4c_i32_i8_e32 v12, v8, v35
	v_add_u32_e32 v11, v17, v16
	s_waitcnt vmcnt(18)
; #define P12_ISSUE(c_, i_, h_, CW_, SC_) do { _Pragma("unroll") for (int bb = 0; bb < 8; ++bb) { const unsigned ro = (unsigned)(c_) * 16384u + (unsigned)EL[(i_) * 128 + ((h_) * 8 + bb) * 8 + g8]; \
;         CW_[bb] = *(const v4u*)(U4 + (size_t)(ro * 128u + 16u * (unsigned)k8)); SC_[bb] = USS[(size_t)(ro * 8u + (unsigned)k8)]; } } while (0)
; #define P12_COMP(i_, h_, CW_, SC_) do { _Pragma("unroll") for (int bb = 0; bb < 8; ++bb) { int a0 = 0, a1 = 0; P12_U4(CW_[bb].x, xa.x, xa.y, a0); P12_U4(CW_[bb].y, xa.z, xa.w, a1); P12_U4(CW_[bb].z, xb.x, xb.y, a0); P12_U4(CW_[bb].w, xb.z, xb.w, a1); \
;         psum[(i_)][(h_) * 8 + bb] += __uint_as_float(SC_[bb] << 16) * (float)((a0 + a1) - xo); } } while (0)
; #define P12_BAR() asm volatile("" ::: "memory")
; __device__ __forceinline__ void p12_peer(Frame& F) {
;     ...
;       for (int c = 0; c < 16; ++c) { const int cn = c + 1 < 16 ? c + 1 : 15;
;           P12_XQ(c, 0); P12_ISSUE(c, 0, 1, cwB, scB); P12_BAR(); P12_COMP(0, 0, cwA, scA); P12_ISSUE(c, 1, 0, cwA, scA); P12_BAR(); P12_COMP(0, 1, cwB, scB);
;           P12_XQ(c, 1); P12_ISSUE(c, 1, 1, cwB, scB); P12_BAR(); P12_COMP(1, 0, cwA, scA); P12_ISSUE(c, 2, 0, cwA, scA); P12_BAR(); P12_COMP(1, 1, cwB, scB);
;           P12_XQ(c, 2); P12_ISSUE(c, 2, 1, cwB, scB); P12_BAR(); P12_COMP(2, 0, cwA, scA); P12_ISSUE(c, 3, 0, cwA, scA); P12_BAR(); P12_COMP(2, 1, cwB, scB);
;           P12_XQ(c, 3); P12_ISSUE(c, 3, 1, cwB, scB); P12_BAR(); P12_COMP(3, 0, cwA, scA); P12_ISSUE(cn, 0, 0, cwA, scA); P12_BAR(); P12_COMP(3, 1, cwB, scB);
;       } }
	v_lshlrev_b32_e32 v9, 16, v237
	v_lshlrev_b32_e32 v8, 16, v236
	v_add_u32_e32 v10, v13, v12
	v_sub_u32_e32 v12, v11, v78
	v_sub_u32_e32 v10, v10, v78
	v_cvt_f32_i32_e32 v11, v10
	v_cvt_f32_i32_e32 v10, v12
	s_waitcnt vmcnt(15)
	v_and_b32_e32 v89, 0xf0f0f0f, v68
	v_lshrrev_b32_e32 v68, 4, v68
	v_dot4c_i32_i8_e32 v90, v89, v36
	v_pk_fma_f32 v[106:107], v[8:9], v[10:11], v[106:107]
	v_and_b32_e32 v8, 0xf0f0f0f, v4
	v_mov_b32_e32 v9, 0
	v_lshrrev_b32_e32 v4, 4, v4
	v_dot4c_i32_i8_e32 v9, v8, v36
	v_and_b32_e32 v4, 0xf0f0f0f, v4
	v_dot4c_i32_i8_e32 v9, v4, v37
	v_and_b32_e32 v4, 0xf0f0f0f, v5
	v_mov_b32_e32 v8, 0
	v_dot4c_i32_i8_e32 v8, v4, v38
	v_lshrrev_b32_e32 v4, 4, v5
	v_and_b32_e32 v4, 0xf0f0f0f, v4
	v_dot4c_i32_i8_e32 v8, v4, v39
	v_and_b32_e32 v4, 0xf0f0f0f, v6
	v_dot4c_i32_i8_e32 v9, v4, v32
	v_lshrrev_b32_e32 v4, 4, v6
	v_and_b32_e32 v4, 0xf0f0f0f, v4
	v_dot4c_i32_i8_e32 v9, v4, v33
	v_and_b32_e32 v4, 0xf0f0f0f, v7
	v_dot4c_i32_i8_e32 v8, v4, v34
	v_lshrrev_b32_e32 v4, 4, v7
	v_and_b32_e32 v4, 0xf0f0f0f, v4
	v_dot4c_i32_i8_e32 v8, v4, v35
	v_and_b32_e32 v4, 0xf0f0f0f, v0
	v_mov_b32_e32 v5, 0
	v_lshrrev_b32_e32 v0, 4, v0
	v_dot4c_i32_i8_e32 v5, v4, v36
	v_and_b32_e32 v0, 0xf0f0f0f, v0
	v_dot4c_i32_i8_e32 v5, v0, v37
	v_and_b32_e32 v0, 0xf0f0f0f, v1
	v_mov_b32_e32 v4, 0
	v_dot4c_i32_i8_e32 v4, v0, v38
	v_lshrrev_b32_e32 v0, 4, v1
	v_and_b32_e32 v0, 0xf0f0f0f, v0
	v_dot4c_i32_i8_e32 v4, v0, v39
	v_and_b32_e32 v0, 0xf0f0f0f, v2
	v_dot4c_i32_i8_e32 v5, v0, v32
	v_lshrrev_b32_e32 v0, 4, v2
	v_and_b32_e32 v0, 0xf0f0f0f, v0
	v_dot4c_i32_i8_e32 v5, v0, v33
	v_and_b32_e32 v0, 0xf0f0f0f, v3
	v_dot4c_i32_i8_e32 v4, v0, v34
	v_lshrrev_b32_e32 v0, 4, v3
	v_and_b32_e32 v0, 0xf0f0f0f, v0
	v_dot4c_i32_i8_e32 v4, v0, v35
	v_add_u32_e32 v3, v9, v8
	v_lshlrev_b32_e32 v1, 16, v239
	v_lshlrev_b32_e32 v0, 16, v238
	v_add_u32_e32 v2, v5, v4
	v_sub_u32_e32 v4, v3, v78
	v_sub_u32_e32 v2, v2, v78
	v_cvt_f32_i32_e32 v3, v2
	v_cvt_f32_i32_e32 v2, v4
	v_and_b32_e32 v68, 0xf0f0f0f, v68
	v_dot4c_i32_i8_e32 v90, v68, v37
	v_and_b32_e32 v68, 0xf0f0f0f, v69
	v_pk_fma_f32 v[104:105], v[0:1], v[2:3], v[104:105]
	ds_read_u16 v0, v93 offset:16384
	ds_read_u16 v1, v93 offset:16400
	ds_read_u16 v2, v93 offset:16416
	ds_read_u16 v3, v93 offset:16432
	v_mov_b32_e32 v89, 0
	s_waitcnt lgkmcnt(3)
	v_add_u32_e32 v0, s44, v0
	v_lshl_or_b32 v4, v0, 7, v165
	v_lshl_or_b32 v0, v0, 4, v95
	global_load_dwordx4 v[28:31], v4, s[0:1] sc1
	s_waitcnt lgkmcnt(2)
	v_add_u32_e32 v0, s44, v1
	v_dot4c_i32_i8_e32 v89, v68, v38
	v_lshrrev_b32_e32 v68, 4, v69
	v_lshl_or_b32 v1, v0, 7, v165
	v_lshl_or_b32 v0, v0, 4, v95
	v_and_b32_e32 v68, 0xf0f0f0f, v68
	global_load_dwordx4 v[24:27], v1, s[0:1] sc1
	s_waitcnt lgkmcnt(1)
	v_add_u32_e32 v0, s44, v2
	v_dot4c_i32_i8_e32 v89, v68, v39
	v_and_b32_e32 v68, 0xf0f0f0f, v70
	v_lshl_or_b32 v1, v0, 7, v165
	v_lshl_or_b32 v0, v0, 4, v95
	v_dot4c_i32_i8_e32 v90, v68, v32
	v_lshrrev_b32_e32 v68, 4, v70
	global_load_dwordx4 v[20:23], v1, s[0:1] sc1
	s_waitcnt lgkmcnt(0)
	v_add_u32_e32 v0, s44, v3
	v_and_b32_e32 v68, 0xf0f0f0f, v68
	v_lshl_or_b32 v1, v0, 7, v165
	v_lshl_or_b32 v0, v0, 4, v95
	v_dot4c_i32_i8_e32 v90, v68, v33
	v_and_b32_e32 v68, 0xf0f0f0f, v71
	global_load_dwordx4 v[16:19], v1, s[0:1] sc1
	ds_read_u16 v0, v93 offset:16448
	v_dot4c_i32_i8_e32 v89, v68, v34
	v_lshrrev_b32_e32 v68, 4, v71
	v_and_b32_e32 v68, 0xf0f0f0f, v68
	v_dot4c_i32_i8_e32 v89, v68, v35
	s_waitcnt vmcnt(18)
	v_and_b32_e32 v68, 0xf0f0f0f, v64
	v_mov_b32_e32 v69, 0
	v_lshrrev_b32_e32 v64, 4, v64
	v_dot4c_i32_i8_e32 v69, v68, v36
	v_and_b32_e32 v64, 0xf0f0f0f, v64
	v_dot4c_i32_i8_e32 v69, v64, v37
	v_and_b32_e32 v64, 0xf0f0f0f, v65
	v_mov_b32_e32 v68, 0
	s_waitcnt lgkmcnt(0)
	v_add_u32_e32 v0, s44, v0
	v_dot4c_i32_i8_e32 v68, v64, v38
	v_lshrrev_b32_e32 v64, 4, v65
	v_lshl_or_b32 v1, v0, 7, v165
	v_lshl_or_b32 v0, v0, 4, v95
	v_and_b32_e32 v64, 0xf0f0f0f, v64
	global_load_dwordx4 v[12:15], v1, s[0:1] sc1
	ds_read_u16 v0, v93 offset:16464
	v_dot4c_i32_i8_e32 v68, v64, v39
	v_and_b32_e32 v64, 0xf0f0f0f, v66
	v_dot4c_i32_i8_e32 v69, v64, v32
	v_lshrrev_b32_e32 v64, 4, v66
	v_and_b32_e32 v64, 0xf0f0f0f, v64
	v_dot4c_i32_i8_e32 v69, v64, v33
	v_and_b32_e32 v64, 0xf0f0f0f, v67
	v_dot4c_i32_i8_e32 v68, v64, v34
	v_lshrrev_b32_e32 v64, 4, v67
	s_waitcnt lgkmcnt(0)
	v_add_u32_e32 v0, s44, v0
	v_and_b32_e32 v64, 0xf0f0f0f, v64
	v_lshl_or_b32 v1, v0, 7, v165
	v_lshl_or_b32 v0, v0, 4, v95
	v_dot4c_i32_i8_e32 v68, v64, v35
	global_load_dwordx4 v[8:11], v1, s[0:1] sc1
	ds_read_u16 v0, v93 offset:16480
	v_add_u32_e32 v66, v90, v89
	v_sub_u32_e32 v67, v68, v78
	v_add_u32_e32 v67, v67, v69
	v_sub_u32_e32 v66, v66, v78
	v_cvt_f32_i32_e32 v66, v66
	v_cvt_f32_i32_e32 v67, v67
	s_waitcnt lgkmcnt(0)
	v_add_u32_e32 v0, s44, v0
	s_waitcnt vmcnt(12)
	v_lshlrev_b32_e32 v65, 16, v241
	v_lshlrev_b32_e32 v64, 16, v240
	v_lshl_or_b32 v1, v0, 7, v165
	v_lshl_or_b32 v0, v0, 4, v95
	v_pk_fma_f32 v[102:103], v[64:65], v[66:67], v[102:103]
	v_and_b32_e32 v64, 0xf0f0f0f, v60
	v_mov_b32_e32 v65, 0
	v_lshrrev_b32_e32 v60, 4, v60
	global_load_dwordx4 v[4:7], v1, s[0:1] sc1
	ds_read_u16 v0, v93 offset:16496
	v_dot4c_i32_i8_e32 v65, v64, v36
	v_and_b32_e32 v60, 0xf0f0f0f, v60
	v_dot4c_i32_i8_e32 v65, v60, v37
	v_and_b32_e32 v60, 0xf0f0f0f, v61
	v_mov_b32_e32 v64, 0
	v_dot4c_i32_i8_e32 v64, v60, v38
	v_lshrrev_b32_e32 v60, 4, v61
	v_and_b32_e32 v60, 0xf0f0f0f, v60
	v_dot4c_i32_i8_e32 v64, v60, v39
	v_and_b32_e32 v60, 0xf0f0f0f, v62
	s_waitcnt lgkmcnt(0)
; #define P12_ISSUE(c_, i_, h_, CW_, SC_) do { _Pragma("unroll") for (int bb = 0; bb < 8; ++bb) { const unsigned ro = (unsigned)(c_) * 16384u + (unsigned)EL[(i_) * 128 + ((h_) * 8 + bb) * 8 + g8]; \
;         CW_[bb] = *(const v4u*)(U4 + (size_t)(ro * 128u + 16u * (unsigned)k8)); SC_[bb] = USS[(size_t)(ro * 8u + (unsigned)k8)]; } } while (0)
; #define P12_COMP(i_, h_, CW_, SC_) do { _Pragma("unroll") for (int bb = 0; bb < 8; ++bb) { int a0 = 0, a1 = 0; P12_U4(CW_[bb].x, xa.x, xa.y, a0); P12_U4(CW_[bb].y, xa.z, xa.w, a1); P12_U4(CW_[bb].z, xb.x, xb.y, a0); P12_U4(CW_[bb].w, xb.z, xb.w, a1); \
;         psum[(i_)][(h_) * 8 + bb] += __uint_as_float(SC_[bb] << 16) * (float)((a0 + a1) - xo); } } while (0)
; #define P12_BAR() asm volatile("" ::: "memory")
; __device__ __forceinline__ void p12_peer(Frame& F) {
;     ...
;       for (int c = 0; c < 16; ++c) { const int cn = c + 1 < 16 ? c + 1 : 15;
;           P12_XQ(c, 0); P12_ISSUE(c, 0, 1, cwB, scB); P12_BAR(); P12_COMP(0, 0, cwA, scA); P12_ISSUE(c, 1, 0, cwA, scA); P12_BAR(); P12_COMP(0, 1, cwB, scB);
;           P12_XQ(c, 1); P12_ISSUE(c, 1, 1, cwB, scB); P12_BAR(); P12_COMP(1, 0, cwA, scA); P12_ISSUE(c, 2, 0, cwA, scA); P12_BAR(); P12_COMP(1, 1, cwB, scB);
;           P12_XQ(c, 2); P12_ISSUE(c, 2, 1, cwB, scB); P12_BAR(); P12_COMP(2, 0, cwA, scA); P12_ISSUE(c, 3, 0, cwA, scA); P12_BAR(); P12_COMP(2, 1, cwB, scB);
;           P12_XQ(c, 3); P12_ISSUE(c, 3, 1, cwB, scB); P12_BAR(); P12_COMP(3, 0, cwA, scA); P12_ISSUE(cn, 0, 0, cwA, scA); P12_BAR(); P12_COMP(3, 1, cwB, scB);
;       } }
	v_add_u32_e32 v88, s44, v0
	v_dot4c_i32_i8_e32 v65, v60, v32
	v_lshrrev_b32_e32 v60, 4, v62
	v_lshl_or_b32 v0, v88, 7, v165
	v_lshl_or_b32 v88, v88, 4, v95
	v_and_b32_e32 v60, 0xf0f0f0f, v60
	global_load_dwordx4 v[0:3], v0, s[0:1] sc1
	v_dot4c_i32_i8_e32 v65, v60, v33
	v_and_b32_e32 v60, 0xf0f0f0f, v63
	v_dot4c_i32_i8_e32 v64, v60, v34
	v_lshrrev_b32_e32 v60, 4, v63
	v_and_b32_e32 v60, 0xf0f0f0f, v60
	v_dot4c_i32_i8_e32 v64, v60, v35
	v_and_b32_e32 v60, 0xf0f0f0f, v56
	v_mov_b32_e32 v61, 0
	v_lshrrev_b32_e32 v56, 4, v56
	v_dot4c_i32_i8_e32 v61, v60, v36
	v_and_b32_e32 v56, 0xf0f0f0f, v56
	v_dot4c_i32_i8_e32 v61, v56, v37
	v_and_b32_e32 v56, 0xf0f0f0f, v57
	v_mov_b32_e32 v60, 0
	v_dot4c_i32_i8_e32 v60, v56, v38
	v_lshrrev_b32_e32 v56, 4, v57
	v_and_b32_e32 v56, 0xf0f0f0f, v56
	v_dot4c_i32_i8_e32 v60, v56, v39
	v_and_b32_e32 v56, 0xf0f0f0f, v58
	v_dot4c_i32_i8_e32 v61, v56, v32
	v_lshrrev_b32_e32 v56, 4, v58
	v_and_b32_e32 v56, 0xf0f0f0f, v56
	v_dot4c_i32_i8_e32 v61, v56, v33
	v_and_b32_e32 v56, 0xf0f0f0f, v59
	v_dot4c_i32_i8_e32 v60, v56, v34
	v_lshrrev_b32_e32 v56, 4, v59
	v_and_b32_e32 v56, 0xf0f0f0f, v56
	v_dot4c_i32_i8_e32 v60, v56, v35
	v_sub_u32_e32 v59, v64, v78
	s_waitcnt vmcnt(12)
	v_lshlrev_b32_e32 v57, 16, v243
	v_lshlrev_b32_e32 v56, 16, v242
	v_sub_u32_e32 v58, v60, v78
	v_add_u32_e32 v60, v59, v65
	v_add_u32_e32 v58, v58, v61
	v_cvt_f32_i32_e32 v59, v58
	v_cvt_f32_i32_e32 v58, v60
	s_mov_b32 s44, s45
	v_pk_fma_f32 v[100:101], v[56:57], v[58:59], v[100:101]
	v_and_b32_e32 v56, 0xf0f0f0f, v52
	v_mov_b32_e32 v57, 0
	v_lshrrev_b32_e32 v52, 4, v52
	v_dot4c_i32_i8_e32 v57, v56, v36
	v_and_b32_e32 v52, 0xf0f0f0f, v52
	v_dot4c_i32_i8_e32 v57, v52, v37
	v_and_b32_e32 v52, 0xf0f0f0f, v53
	v_mov_b32_e32 v56, 0
	v_dot4c_i32_i8_e32 v56, v52, v38
	v_lshrrev_b32_e32 v52, 4, v53
	v_and_b32_e32 v52, 0xf0f0f0f, v52
	v_dot4c_i32_i8_e32 v56, v52, v39
	v_and_b32_e32 v52, 0xf0f0f0f, v54
	v_dot4c_i32_i8_e32 v57, v52, v32
	v_lshrrev_b32_e32 v52, 4, v54
	v_and_b32_e32 v52, 0xf0f0f0f, v52
	v_dot4c_i32_i8_e32 v57, v52, v33
	v_and_b32_e32 v52, 0xf0f0f0f, v55
	v_dot4c_i32_i8_e32 v56, v52, v34
	v_lshrrev_b32_e32 v52, 4, v55
	v_and_b32_e32 v52, 0xf0f0f0f, v52
	v_dot4c_i32_i8_e32 v56, v52, v35
	v_and_b32_e32 v52, 0xf0f0f0f, v48
	v_mov_b32_e32 v53, 0
	v_lshrrev_b32_e32 v48, 4, v48
	v_dot4c_i32_i8_e32 v53, v52, v36
	v_and_b32_e32 v48, 0xf0f0f0f, v48
	v_dot4c_i32_i8_e32 v53, v48, v37
	v_and_b32_e32 v48, 0xf0f0f0f, v49
	v_mov_b32_e32 v52, 0
	v_dot4c_i32_i8_e32 v52, v48, v38
	v_lshrrev_b32_e32 v48, 4, v49
	v_and_b32_e32 v48, 0xf0f0f0f, v48
	v_dot4c_i32_i8_e32 v52, v48, v39
	v_and_b32_e32 v48, 0xf0f0f0f, v50
	v_dot4c_i32_i8_e32 v53, v48, v32
	v_lshrrev_b32_e32 v48, 4, v50
	v_and_b32_e32 v48, 0xf0f0f0f, v48
	v_dot4c_i32_i8_e32 v53, v48, v33
	v_and_b32_e32 v48, 0xf0f0f0f, v51
	v_dot4c_i32_i8_e32 v52, v48, v34
	v_lshrrev_b32_e32 v48, 4, v51
	v_and_b32_e32 v48, 0xf0f0f0f, v48
	v_dot4c_i32_i8_e32 v52, v48, v35
	v_sub_u32_e32 v51, v56, v78
	s_waitcnt vmcnt(10)
	v_lshlrev_b32_e32 v49, 16, v245
	v_lshlrev_b32_e32 v48, 16, v244
	v_sub_u32_e32 v50, v52, v78
	v_add_u32_e32 v52, v51, v57
	v_add_u32_e32 v50, v50, v53
	v_cvt_f32_i32_e32 v51, v50
	v_cvt_f32_i32_e32 v50, v52
	v_pk_fma_f32 v[98:99], v[48:49], v[50:51], v[98:99]
	v_and_b32_e32 v48, 0xf0f0f0f, v44
	v_mov_b32_e32 v49, 0
	v_lshrrev_b32_e32 v44, 4, v44
	v_dot4c_i32_i8_e32 v49, v48, v36
	v_and_b32_e32 v44, 0xf0f0f0f, v44
	v_dot4c_i32_i8_e32 v49, v44, v37
	v_and_b32_e32 v44, 0xf0f0f0f, v45
	v_mov_b32_e32 v48, 0
	v_dot4c_i32_i8_e32 v48, v44, v38
	v_lshrrev_b32_e32 v44, 4, v45
	v_and_b32_e32 v44, 0xf0f0f0f, v44
	v_dot4c_i32_i8_e32 v48, v44, v39
	v_and_b32_e32 v44, 0xf0f0f0f, v46
	v_dot4c_i32_i8_e32 v49, v44, v32
	v_lshrrev_b32_e32 v44, 4, v46
	v_and_b32_e32 v44, 0xf0f0f0f, v44
	v_dot4c_i32_i8_e32 v49, v44, v33
	v_and_b32_e32 v44, 0xf0f0f0f, v47
	v_dot4c_i32_i8_e32 v48, v44, v34
	v_lshrrev_b32_e32 v44, 4, v47
	v_and_b32_e32 v44, 0xf0f0f0f, v44
	v_dot4c_i32_i8_e32 v48, v44, v35
	v_and_b32_e32 v44, 0xf0f0f0f, v40
	v_mov_b32_e32 v45, 0
	v_dot4c_i32_i8_e32 v45, v44, v36
	v_lshrrev_b32_e32 v36, 4, v40
	v_and_b32_e32 v36, 0xf0f0f0f, v36
	v_dot4c_i32_i8_e32 v45, v36, v37
	v_and_b32_e32 v36, 0xf0f0f0f, v41
	v_mov_b32_e32 v37, 0
	v_dot4c_i32_i8_e32 v37, v36, v38
	v_lshrrev_b32_e32 v36, 4, v41
	v_and_b32_e32 v36, 0xf0f0f0f, v36
	v_dot4c_i32_i8_e32 v37, v36, v39
	v_and_b32_e32 v36, 0xf0f0f0f, v42
	v_dot4c_i32_i8_e32 v45, v36, v32
	v_lshrrev_b32_e32 v32, 4, v42
	v_and_b32_e32 v32, 0xf0f0f0f, v32
	v_dot4c_i32_i8_e32 v45, v32, v33
	v_and_b32_e32 v32, 0xf0f0f0f, v43
	v_dot4c_i32_i8_e32 v37, v32, v34
	v_lshrrev_b32_e32 v32, 4, v43
	v_and_b32_e32 v32, 0xf0f0f0f, v32
	v_dot4c_i32_i8_e32 v37, v32, v35
	v_sub_u32_e32 v35, v48, v78
	v_add_u32_e32 v36, v35, v49
	s_waitcnt vmcnt(8)
	v_lshlrev_b32_e32 v33, 16, v247
	v_sub_u32_e32 v34, v37, v78
	v_add_u32_e32 v34, v34, v45
	v_cvt_f32_i32_e32 v35, v34
	v_cvt_f32_i32_e32 v34, v36
	v_lshlrev_b32_e32 v32, 16, v246
	s_waitcnt vmcnt(0)
	v_perm_b32 v40, v190, v191, s48
	v_perm_b32 v41, v188, v189, s48
	v_pk_fma_f32 v[96:97], v[32:33], v[34:35], v[96:97]
	v_perm_b32 v42, v186, v187, s48
	v_perm_b32 v43, v184, v185, s48
	ds_read_b128 v[36:39], v166
	ds_read_b128 v[32:35], v166 offset:16
	ds_read_u16 v44, v93 offset:16512
	ds_read_u16 v45, v93 offset:16528
	ds_read_u16 v46, v93 offset:16544
	ds_read_u16 v47, v93 offset:16560
	v_mov_b32_e32 v48, 0
	s_waitcnt lgkmcnt(3)
	v_add_u32_e32 v44, s44, v44
	v_lshl_or_b32 v49, v44, 7, v165
	global_load_dwordx4 v[88:91], v49, s[0:1] sc1
	v_lshl_or_b32 v49, v44, 4, v95
	s_waitcnt lgkmcnt(2)
	v_add_u32_e32 v44, s44, v45
	v_lshl_or_b32 v45, v44, 7, v165
	v_lshl_or_b32 v50, v44, 4, v95
	s_waitcnt lgkmcnt(1)
	v_add_u32_e32 v44, s44, v46
	global_load_dwordx4 v[84:87], v45, s[0:1] sc1
	v_lshl_or_b32 v45, v44, 7, v165
	v_lshl_or_b32 v51, v44, 4, v95
	s_waitcnt lgkmcnt(0)
	v_add_u32_e32 v44, s44, v47
	global_load_dwordx4 v[80:83], v45, s[0:1] sc1
	v_lshl_or_b32 v45, v44, 7, v165
	v_lshl_or_b32 v56, v44, 4, v95
	ds_read_u16 v44, v93 offset:16576
	global_load_dwordx4 v[76:79], v45, s[0:1] sc1
	v_dot4c_i32_i8_e32 v48, 0x1010101, v36
	v_dot4c_i32_i8_e32 v48, 0x1010101, v37
	v_dot4c_i32_i8_e32 v48, 0x1010101, v38
	s_waitcnt lgkmcnt(0)
	v_add_u32_e32 v44, s44, v44
	v_lshl_or_b32 v45, v44, 7, v165
	v_lshl_or_b32 v57, v44, 4, v95
	ds_read_u16 v44, v93 offset:16592
	global_load_dwordx4 v[68:71], v45, s[0:1] sc1
	v_dot4c_i32_i8_e32 v48, 0x1010101, v39
	v_dot4c_i32_i8_e32 v48, 0x1010101, v32
	v_dot4c_i32_i8_e32 v48, 0x1010101, v33
	s_waitcnt lgkmcnt(0)
	v_add_u32_e32 v44, s44, v44
	v_lshl_or_b32 v45, v44, 7, v165
	v_lshl_or_b32 v58, v44, 4, v95
	ds_read_u16 v44, v93 offset:16608
	global_load_dwordx4 v[60:63], v45, s[0:1] sc1
	v_dot4c_i32_i8_e32 v48, 0x1010101, v34
	v_dot4c_i32_i8_e32 v48, 0x1010101, v35
	s_add_i32 s45, s44, 0x4000
	s_waitcnt lgkmcnt(0)
	v_add_u32_e32 v44, s44, v44
	v_lshl_or_b32 v45, v44, 7, v165
	v_lshl_or_b32 v59, v44, 4, v95
	ds_read_u16 v44, v93 offset:16624
	global_load_dwordx4 v[52:55], v45, s[0:1] sc1
	v_lshlrev_b32_e32 v171, 3, v48
	s_waitcnt vmcnt(10)
	v_and_b32_e32 v48, 0xf0f0f0f, v28
	v_lshrrev_b32_e32 v28, 4, v28
	s_waitcnt lgkmcnt(0)
	v_add_u32_e32 v64, s44, v44
	v_lshl_or_b32 v44, v64, 7, v165
	global_load_dwordx4 v[44:47], v44, s[0:1] sc1
	v_lshl_or_b32 v64, v64, 4, v95
	v_mov_b32_e32 v49, 0
	v_dot4c_i32_i8_e32 v49, v48, v36
	v_and_b32_e32 v28, 0xf0f0f0f, v28
	v_dot4c_i32_i8_e32 v49, v28, v37
	v_and_b32_e32 v28, 0xf0f0f0f, v29
	v_mov_b32_e32 v48, 0
	v_dot4c_i32_i8_e32 v48, v28, v38
	v_lshrrev_b32_e32 v28, 4, v29
	v_and_b32_e32 v28, 0xf0f0f0f, v28
	v_dot4c_i32_i8_e32 v48, v28, v39
	v_and_b32_e32 v28, 0xf0f0f0f, v30
	v_dot4c_i32_i8_e32 v49, v28, v32
	v_lshrrev_b32_e32 v28, 4, v30
	v_and_b32_e32 v28, 0xf0f0f0f, v28
	v_dot4c_i32_i8_e32 v49, v28, v33
	v_and_b32_e32 v28, 0xf0f0f0f, v31
	v_dot4c_i32_i8_e32 v48, v28, v34
	v_lshrrev_b32_e32 v28, 4, v31
	v_and_b32_e32 v28, 0xf0f0f0f, v28
	v_dot4c_i32_i8_e32 v48, v28, v35
	s_waitcnt vmcnt(11)
	v_and_b32_e32 v28, 0xf0f0f0f, v24
	v_mov_b32_e32 v29, 0
	v_lshrrev_b32_e32 v24, 4, v24
	v_dot4c_i32_i8_e32 v29, v28, v36
	v_and_b32_e32 v24, 0xf0f0f0f, v24
	v_dot4c_i32_i8_e32 v29, v24, v37
	v_and_b32_e32 v24, 0xf0f0f0f, v25
	v_mov_b32_e32 v28, 0
	v_dot4c_i32_i8_e32 v28, v24, v38
	v_lshrrev_b32_e32 v24, 4, v25
	v_and_b32_e32 v24, 0xf0f0f0f, v24
	v_dot4c_i32_i8_e32 v28, v24, v39
	v_and_b32_e32 v24, 0xf0f0f0f, v26
	v_dot4c_i32_i8_e32 v29, v24, v32
	v_lshrrev_b32_e32 v24, 4, v26
	v_and_b32_e32 v24, 0xf0f0f0f, v24
	v_dot4c_i32_i8_e32 v29, v24, v33
	v_and_b32_e32 v24, 0xf0f0f0f, v27
	v_dot4c_i32_i8_e32 v28, v24, v34
	v_lshrrev_b32_e32 v24, 4, v27
	v_and_b32_e32 v24, 0xf0f0f0f, v24
	v_dot4c_i32_i8_e32 v28, v24, v35
	v_add_u32_e32 v26, v49, v48
	v_sub_u32_e32 v26, v26, v171
	v_and_b32_e32 v25, 0xffff0000, v43
	v_add_u32_e32 v27, v29, v28
	v_sub_u32_e32 v28, v27, v171
	v_cvt_f32_i32_e32 v27, v26
	v_cvt_f32_i32_e32 v26, v28
	v_lshlrev_b32_e32 v24, 16, v43
	s_cmp_eq_u32 s44, 0x3c000
	v_pk_fma_f32 v[158:159], v[24:25], v[26:27], v[158:159]
	s_waitcnt vmcnt(10)
	v_and_b32_e32 v24, 0xf0f0f0f, v20
	v_mov_b32_e32 v25, 0
	v_lshrrev_b32_e32 v20, 4, v20
	v_dot4c_i32_i8_e32 v25, v24, v36
	v_and_b32_e32 v20, 0xf0f0f0f, v20
	v_dot4c_i32_i8_e32 v25, v20, v37
	v_and_b32_e32 v20, 0xf0f0f0f, v21
	v_mov_b32_e32 v24, 0
	v_dot4c_i32_i8_e32 v24, v20, v38
	v_lshrrev_b32_e32 v20, 4, v21
	v_and_b32_e32 v20, 0xf0f0f0f, v20
	v_dot4c_i32_i8_e32 v24, v20, v39
	v_and_b32_e32 v20, 0xf0f0f0f, v22
	v_dot4c_i32_i8_e32 v25, v20, v32
	v_lshrrev_b32_e32 v20, 4, v22
	v_and_b32_e32 v20, 0xf0f0f0f, v20
	v_dot4c_i32_i8_e32 v25, v20, v33
	v_and_b32_e32 v20, 0xf0f0f0f, v23
	v_dot4c_i32_i8_e32 v24, v20, v34
	v_lshrrev_b32_e32 v20, 4, v23
	v_and_b32_e32 v20, 0xf0f0f0f, v20
	v_dot4c_i32_i8_e32 v24, v20, v35
	s_waitcnt vmcnt(10)
	v_and_b32_e32 v20, 0xf0f0f0f, v16
	v_mov_b32_e32 v21, 0
	v_lshrrev_b32_e32 v16, 4, v16
	v_dot4c_i32_i8_e32 v21, v20, v36
	v_and_b32_e32 v16, 0xf0f0f0f, v16
	v_dot4c_i32_i8_e32 v21, v16, v37
	v_and_b32_e32 v16, 0xf0f0f0f, v17
	v_mov_b32_e32 v20, 0
	v_dot4c_i32_i8_e32 v20, v16, v38
	v_lshrrev_b32_e32 v16, 4, v17
	v_and_b32_e32 v16, 0xf0f0f0f, v16
	v_dot4c_i32_i8_e32 v20, v16, v39
	v_and_b32_e32 v16, 0xf0f0f0f, v18
	v_dot4c_i32_i8_e32 v21, v16, v32
	v_lshrrev_b32_e32 v16, 4, v18
	v_and_b32_e32 v16, 0xf0f0f0f, v16
	v_dot4c_i32_i8_e32 v21, v16, v33
	v_and_b32_e32 v16, 0xf0f0f0f, v19
	v_dot4c_i32_i8_e32 v20, v16, v34
	v_lshrrev_b32_e32 v16, 4, v19
	v_and_b32_e32 v16, 0xf0f0f0f, v16
	v_dot4c_i32_i8_e32 v20, v16, v35
	v_add_u32_e32 v18, v25, v24
	v_sub_u32_e32 v18, v18, v171
	v_and_b32_e32 v17, 0xffff0000, v42
	v_add_u32_e32 v19, v21, v20
	v_sub_u32_e32 v20, v19, v171
	v_cvt_f32_i32_e32 v19, v18
	v_cvt_f32_i32_e32 v18, v20
	v_lshlrev_b32_e32 v16, 16, v42
	v_pk_fma_f32 v[156:157], v[16:17], v[18:19], v[156:157]
	s_waitcnt vmcnt(9)
	v_and_b32_e32 v16, 0xf0f0f0f, v12
	v_mov_b32_e32 v17, 0
	v_lshrrev_b32_e32 v12, 4, v12
	v_dot4c_i32_i8_e32 v17, v16, v36
	v_and_b32_e32 v12, 0xf0f0f0f, v12
	v_dot4c_i32_i8_e32 v17, v12, v37
	v_and_b32_e32 v12, 0xf0f0f0f, v13
	v_mov_b32_e32 v16, 0
	v_dot4c_i32_i8_e32 v16, v12, v38
	v_lshrrev_b32_e32 v12, 4, v13
	v_and_b32_e32 v12, 0xf0f0f0f, v12
	v_dot4c_i32_i8_e32 v16, v12, v39
	v_and_b32_e32 v12, 0xf0f0f0f, v14
	v_dot4c_i32_i8_e32 v17, v12, v32
	v_lshrrev_b32_e32 v12, 4, v14
	v_and_b32_e32 v12, 0xf0f0f0f, v12
	v_dot4c_i32_i8_e32 v17, v12, v33
	v_and_b32_e32 v12, 0xf0f0f0f, v15
	v_dot4c_i32_i8_e32 v16, v12, v34
	v_lshrrev_b32_e32 v12, 4, v15
	v_and_b32_e32 v12, 0xf0f0f0f, v12
	v_dot4c_i32_i8_e32 v16, v12, v35
	s_waitcnt vmcnt(9)
	v_and_b32_e32 v12, 0xf0f0f0f, v8
	v_mov_b32_e32 v13, 0
	v_lshrrev_b32_e32 v8, 4, v8
	v_dot4c_i32_i8_e32 v13, v12, v36
	v_and_b32_e32 v8, 0xf0f0f0f, v8
	v_dot4c_i32_i8_e32 v13, v8, v37
	v_and_b32_e32 v8, 0xf0f0f0f, v9
	v_mov_b32_e32 v12, 0
	v_dot4c_i32_i8_e32 v12, v8, v38
	v_lshrrev_b32_e32 v8, 4, v9
	v_and_b32_e32 v8, 0xf0f0f0f, v8
	v_dot4c_i32_i8_e32 v12, v8, v39
	v_and_b32_e32 v8, 0xf0f0f0f, v10
	v_dot4c_i32_i8_e32 v13, v8, v32
	v_lshrrev_b32_e32 v8, 4, v10
	v_and_b32_e32 v8, 0xf0f0f0f, v8
	v_dot4c_i32_i8_e32 v13, v8, v33
	v_and_b32_e32 v8, 0xf0f0f0f, v11
	v_dot4c_i32_i8_e32 v12, v8, v34
	v_lshrrev_b32_e32 v8, 4, v11
	v_and_b32_e32 v8, 0xf0f0f0f, v8
	v_dot4c_i32_i8_e32 v12, v8, v35
	v_add_u32_e32 v10, v17, v16
	v_sub_u32_e32 v10, v10, v171
	v_and_b32_e32 v9, 0xffff0000, v41
	v_add_u32_e32 v11, v13, v12
	v_sub_u32_e32 v12, v11, v171
	v_cvt_f32_i32_e32 v11, v10
	v_cvt_f32_i32_e32 v10, v12
	v_lshlrev_b32_e32 v8, 16, v41
	v_pk_fma_f32 v[154:155], v[8:9], v[10:11], v[154:155]
	s_waitcnt vmcnt(8)
	v_and_b32_e32 v8, 0xf0f0f0f, v4
	v_mov_b32_e32 v9, 0
	v_lshrrev_b32_e32 v4, 4, v4
	v_dot4c_i32_i8_e32 v9, v8, v36
	v_and_b32_e32 v4, 0xf0f0f0f, v4
	v_dot4c_i32_i8_e32 v9, v4, v37
	v_and_b32_e32 v4, 0xf0f0f0f, v5
	v_mov_b32_e32 v8, 0
	v_dot4c_i32_i8_e32 v8, v4, v38
	v_lshrrev_b32_e32 v4, 4, v5
	v_and_b32_e32 v4, 0xf0f0f0f, v4
	v_dot4c_i32_i8_e32 v8, v4, v39
	v_and_b32_e32 v4, 0xf0f0f0f, v6
	v_dot4c_i32_i8_e32 v9, v4, v32
	v_lshrrev_b32_e32 v4, 4, v6
	v_and_b32_e32 v4, 0xf0f0f0f, v4
	v_dot4c_i32_i8_e32 v9, v4, v33
	v_and_b32_e32 v4, 0xf0f0f0f, v7
	v_dot4c_i32_i8_e32 v8, v4, v34
	v_lshrrev_b32_e32 v4, 4, v7
	v_and_b32_e32 v4, 0xf0f0f0f, v4
	v_dot4c_i32_i8_e32 v8, v4, v35
	s_waitcnt vmcnt(8)
	v_and_b32_e32 v4, 0xf0f0f0f, v0
	v_mov_b32_e32 v5, 0
	v_lshrrev_b32_e32 v0, 4, v0
	v_dot4c_i32_i8_e32 v5, v4, v36
	v_and_b32_e32 v0, 0xf0f0f0f, v0
	v_dot4c_i32_i8_e32 v5, v0, v37
	v_and_b32_e32 v0, 0xf0f0f0f, v1
	v_mov_b32_e32 v4, 0
	v_dot4c_i32_i8_e32 v4, v0, v38
	v_lshrrev_b32_e32 v0, 4, v1
	v_and_b32_e32 v0, 0xf0f0f0f, v0
	v_dot4c_i32_i8_e32 v4, v0, v39
	v_and_b32_e32 v0, 0xf0f0f0f, v2
	v_dot4c_i32_i8_e32 v5, v0, v32
	v_lshrrev_b32_e32 v0, 4, v2
	v_and_b32_e32 v0, 0xf0f0f0f, v0
	v_dot4c_i32_i8_e32 v5, v0, v33
	v_and_b32_e32 v0, 0xf0f0f0f, v3
	v_dot4c_i32_i8_e32 v4, v0, v34
	v_lshrrev_b32_e32 v0, 4, v3
	v_and_b32_e32 v0, 0xf0f0f0f, v0
	v_dot4c_i32_i8_e32 v4, v0, v35
	v_add_u32_e32 v2, v9, v8
	v_sub_u32_e32 v2, v2, v171
	v_and_b32_e32 v1, 0xffff0000, v40
	v_add_u32_e32 v3, v5, v4
	v_sub_u32_e32 v4, v3, v171
	v_cvt_f32_i32_e32 v3, v2
	v_cvt_f32_i32_e32 v2, v4
	v_lshlrev_b32_e32 v0, 16, v40
	v_pk_fma_f32 v[152:153], v[0:1], v[2:3], v[152:153]
	ds_read_u16 v0, v93 offset:16640
	ds_read_u16 v1, v93 offset:16656
	ds_read_u16 v2, v93 offset:16672
	ds_read_u16 v3, v93 offset:16688
	s_waitcnt lgkmcnt(3)
	v_add_u32_e32 v0, s44, v0
	v_lshl_or_b32 v4, v0, 7, v165
	s_waitcnt lgkmcnt(2)
	v_add_u32_e32 v1, s44, v1
	global_load_dwordx4 v[72:75], v4, s[0:1] sc1
	v_lshl_or_b32 v4, v1, 7, v165
	s_waitcnt lgkmcnt(1)
	v_add_u32_e32 v2, s44, v2
	global_load_dwordx4 v[64:67], v4, s[0:1] sc1
	v_lshl_or_b32 v4, v2, 7, v165
	s_waitcnt lgkmcnt(0)
	v_add_u32_e32 v3, s44, v3
	global_load_dwordx4 v[56:59], v4, s[0:1] sc1
	v_lshl_or_b32 v4, v3, 7, v165
	global_load_dwordx4 v[48:51], v4, s[0:1] sc1
	ds_read_u16 v4, v93 offset:16704
	v_lshl_or_b32 v0, v0, 4, v95
	v_lshl_or_b32 v1, v1, 4, v95
	v_lshl_or_b32 v2, v2, 4, v95
	v_lshl_or_b32 v3, v3, 4, v95
	s_waitcnt lgkmcnt(0)
	v_add_u32_e32 v4, s44, v4
	v_lshl_or_b32 v5, v4, 7, v165
	global_load_dwordx4 v[40:43], v5, s[0:1] sc1
	ds_read_u16 v5, v93 offset:16720
	v_lshl_or_b32 v4, v4, 4, v95
	s_waitcnt lgkmcnt(0)
	v_add_u32_e32 v5, s44, v5
	v_lshl_or_b32 v6, v5, 7, v165
	global_load_dwordx4 v[24:27], v6, s[0:1] sc1
	ds_read_u16 v6, v93 offset:16736
	v_lshl_or_b32 v5, v5, 4, v95
	s_waitcnt lgkmcnt(0)
	v_add_u32_e32 v6, s44, v6
	v_lshl_or_b32 v7, v6, 7, v165
	global_load_dwordx4 v[12:15], v7, s[0:1] sc1
	ds_read_u16 v7, v93 offset:16752
	v_lshl_or_b32 v6, v6, 4, v95
	s_waitcnt lgkmcnt(0)
	v_add_u32_e32 v7, s44, v7
	v_lshl_or_b32 v8, v7, 7, v165
	global_load_dwordx4 v[8:11], v8, s[0:1] sc1
	v_lshl_or_b32 v7, v7, 4, v95
	s_waitcnt vmcnt(15)
	v_and_b32_e32 v0, 0xf0f0f0f, v88
	v_mov_b32_e32 v2, 0
	v_dot4c_i32_i8_e32 v2, v0, v36
	v_lshrrev_b32_e32 v0, 4, v88
	v_and_b32_e32 v0, 0xf0f0f0f, v0
	v_dot4c_i32_i8_e32 v2, v0, v37
	v_and_b32_e32 v0, 0xf0f0f0f, v89
	v_mov_b32_e32 v3, 0
	v_dot4c_i32_i8_e32 v3, v0, v38
	v_lshrrev_b32_e32 v0, 4, v89
	v_and_b32_e32 v0, 0xf0f0f0f, v0
	v_dot4c_i32_i8_e32 v3, v0, v39
	v_and_b32_e32 v0, 0xf0f0f0f, v90
	v_dot4c_i32_i8_e32 v2, v0, v32
	v_lshrrev_b32_e32 v0, 4, v90
	v_and_b32_e32 v0, 0xf0f0f0f, v0
	v_dot4c_i32_i8_e32 v2, v0, v33
	v_and_b32_e32 v0, 0xf0f0f0f, v91
	v_dot4c_i32_i8_e32 v3, v0, v34
	v_lshrrev_b32_e32 v0, 4, v91
	v_and_b32_e32 v0, 0xf0f0f0f, v0
	v_dot4c_i32_i8_e32 v3, v0, v35
	s_waitcnt vmcnt(14)
	v_and_b32_e32 v0, 0xf0f0f0f, v84
	v_mov_b32_e32 v4, 0
	v_dot4c_i32_i8_e32 v4, v0, v36
	v_lshrrev_b32_e32 v0, 4, v84
	v_and_b32_e32 v0, 0xf0f0f0f, v0
	v_dot4c_i32_i8_e32 v4, v0, v37
	v_and_b32_e32 v0, 0xf0f0f0f, v85
	v_mov_b32_e32 v5, 0
	v_dot4c_i32_i8_e32 v5, v0, v38
	v_lshrrev_b32_e32 v0, 4, v85
	v_and_b32_e32 v0, 0xf0f0f0f, v0
	v_dot4c_i32_i8_e32 v5, v0, v39
	v_and_b32_e32 v0, 0xf0f0f0f, v86
	v_dot4c_i32_i8_e32 v4, v0, v32
	v_lshrrev_b32_e32 v0, 4, v86
	v_and_b32_e32 v0, 0xf0f0f0f, v0
	v_dot4c_i32_i8_e32 v4, v0, v33
	v_and_b32_e32 v0, 0xf0f0f0f, v87
	v_dot4c_i32_i8_e32 v5, v0, v34
	v_lshrrev_b32_e32 v0, 4, v87
	v_and_b32_e32 v0, 0xf0f0f0f, v0
	v_dot4c_i32_i8_e32 v5, v0, v35
	v_add_u32_e32 v2, v2, v3
	v_sub_u32_e32 v2, v2, v171
	s_waitcnt vmcnt(8)
	v_and_b32_e32 v1, 0xffff0000, v192
	v_sub_u32_e32 v3, v5, v171
	v_add_u32_e32 v4, v3, v4
	v_cvt_f32_i32_e32 v3, v2
	v_cvt_f32_i32_e32 v2, v4
	v_and_b32_e32 v0, 0xffff0000, v193
	v_mov_b32_e32 v4, 0
	v_mov_b32_e32 v5, 0
	v_pk_fma_f32 v[150:151], v[0:1], v[2:3], v[150:151]
	v_and_b32_e32 v0, 0xf0f0f0f, v80
	v_mov_b32_e32 v2, 0
	v_dot4c_i32_i8_e32 v2, v0, v36
	v_lshrrev_b32_e32 v0, 4, v80
	v_and_b32_e32 v0, 0xf0f0f0f, v0
	v_dot4c_i32_i8_e32 v2, v0, v37
	v_and_b32_e32 v0, 0xf0f0f0f, v81
	v_mov_b32_e32 v3, 0
	v_dot4c_i32_i8_e32 v3, v0, v38
	v_lshrrev_b32_e32 v0, 4, v81
	v_and_b32_e32 v0, 0xf0f0f0f, v0
	v_dot4c_i32_i8_e32 v3, v0, v39
	v_and_b32_e32 v0, 0xf0f0f0f, v82
	v_dot4c_i32_i8_e32 v2, v0, v32
	v_lshrrev_b32_e32 v0, 4, v82
	v_and_b32_e32 v0, 0xf0f0f0f, v0
	v_dot4c_i32_i8_e32 v2, v0, v33
	v_and_b32_e32 v0, 0xf0f0f0f, v83
	v_dot4c_i32_i8_e32 v3, v0, v34
	v_lshrrev_b32_e32 v0, 4, v83
	v_and_b32_e32 v0, 0xf0f0f0f, v0
	v_dot4c_i32_i8_e32 v3, v0, v35
	v_and_b32_e32 v0, 0xf0f0f0f, v76
	v_dot4c_i32_i8_e32 v4, v0, v36
	v_lshrrev_b32_e32 v0, 4, v76
	v_and_b32_e32 v0, 0xf0f0f0f, v0
	v_dot4c_i32_i8_e32 v4, v0, v37
	v_and_b32_e32 v0, 0xf0f0f0f, v77
	v_dot4c_i32_i8_e32 v5, v0, v38
	v_lshrrev_b32_e32 v0, 4, v77
	v_and_b32_e32 v0, 0xf0f0f0f, v0
	v_dot4c_i32_i8_e32 v5, v0, v39
	v_and_b32_e32 v0, 0xf0f0f0f, v78
	v_dot4c_i32_i8_e32 v4, v0, v32
	v_lshrrev_b32_e32 v0, 4, v78
	v_and_b32_e32 v0, 0xf0f0f0f, v0
	v_dot4c_i32_i8_e32 v4, v0, v33
	v_and_b32_e32 v0, 0xf0f0f0f, v79
	v_dot4c_i32_i8_e32 v5, v0, v34
	v_lshrrev_b32_e32 v0, 4, v79
	v_and_b32_e32 v0, 0xf0f0f0f, v0
	v_dot4c_i32_i8_e32 v5, v0, v35
	v_sub_u32_e32 v3, v3, v171
	v_add_u32_e32 v2, v3, v2
	v_cvt_f32_i32_e32 v3, v2
	v_sub_u32_e32 v5, v5, v171
	v_add_u32_e32 v4, v5, v4
	v_cvt_f32_i32_e32 v2, v4
	s_waitcnt vmcnt(8)
	v_and_b32_e32 v1, 0xffff0000, v194
	v_and_b32_e32 v0, 0xffff0000, v195
	v_mov_b32_e32 v4, 0
	v_pk_fma_f32 v[148:149], v[0:1], v[2:3], v[148:149]
	v_and_b32_e32 v0, 0xf0f0f0f, v68
	v_mov_b32_e32 v2, 0
	v_dot4c_i32_i8_e32 v2, v0, v36
	v_lshrrev_b32_e32 v0, 4, v68
	v_and_b32_e32 v0, 0xf0f0f0f, v0
	v_dot4c_i32_i8_e32 v2, v0, v37
	v_and_b32_e32 v0, 0xf0f0f0f, v69
	v_mov_b32_e32 v3, 0
	v_dot4c_i32_i8_e32 v3, v0, v38
	v_lshrrev_b32_e32 v0, 4, v69
	v_and_b32_e32 v0, 0xf0f0f0f, v0
	v_dot4c_i32_i8_e32 v3, v0, v39
	v_and_b32_e32 v0, 0xf0f0f0f, v70
	v_dot4c_i32_i8_e32 v2, v0, v32
	v_lshrrev_b32_e32 v0, 4, v70
	v_and_b32_e32 v0, 0xf0f0f0f, v0
	v_dot4c_i32_i8_e32 v2, v0, v33
	v_and_b32_e32 v0, 0xf0f0f0f, v71
	v_dot4c_i32_i8_e32 v3, v0, v34
	v_lshrrev_b32_e32 v0, 4, v71
	v_and_b32_e32 v0, 0xf0f0f0f, v0
	v_dot4c_i32_i8_e32 v3, v0, v35
	v_and_b32_e32 v0, 0xf0f0f0f, v60
	v_dot4c_i32_i8_e32 v4, v0, v36
	v_lshrrev_b32_e32 v0, 4, v60
	v_and_b32_e32 v0, 0xf0f0f0f, v0
	v_dot4c_i32_i8_e32 v4, v0, v37
	v_and_b32_e32 v0, 0xf0f0f0f, v61
	v_mov_b32_e32 v5, 0
	v_dot4c_i32_i8_e32 v5, v0, v38
	v_lshrrev_b32_e32 v0, 4, v61
	v_and_b32_e32 v0, 0xf0f0f0f, v0
	v_dot4c_i32_i8_e32 v5, v0, v39
	v_and_b32_e32 v0, 0xf0f0f0f, v62
	v_dot4c_i32_i8_e32 v4, v0, v32
	v_lshrrev_b32_e32 v0, 4, v62
	v_and_b32_e32 v0, 0xf0f0f0f, v0
	v_dot4c_i32_i8_e32 v4, v0, v33
	v_and_b32_e32 v0, 0xf0f0f0f, v63
	v_dot4c_i32_i8_e32 v5, v0, v34
	v_lshrrev_b32_e32 v0, 4, v63
	v_and_b32_e32 v0, 0xf0f0f0f, v0
	v_dot4c_i32_i8_e32 v5, v0, v35
	v_sub_u32_e32 v3, v3, v171
	v_add_u32_e32 v2, v3, v2
	v_cvt_f32_i32_e32 v3, v2
	v_sub_u32_e32 v5, v5, v171
	v_add_u32_e32 v4, v5, v4
	v_cvt_f32_i32_e32 v2, v4
	s_waitcnt vmcnt(8)
	v_and_b32_e32 v1, 0xffff0000, v196
	v_and_b32_e32 v0, 0xffff0000, v197
	v_mov_b32_e32 v4, 0
	v_pk_fma_f32 v[146:147], v[0:1], v[2:3], v[146:147]
	v_and_b32_e32 v0, 0xf0f0f0f, v52
	v_mov_b32_e32 v2, 0
	v_dot4c_i32_i8_e32 v2, v0, v36
	v_lshrrev_b32_e32 v0, 4, v52
	v_and_b32_e32 v0, 0xf0f0f0f, v0
	v_dot4c_i32_i8_e32 v2, v0, v37
	v_and_b32_e32 v0, 0xf0f0f0f, v53
	v_mov_b32_e32 v3, 0
	v_dot4c_i32_i8_e32 v3, v0, v38
	v_lshrrev_b32_e32 v0, 4, v53
	v_and_b32_e32 v0, 0xf0f0f0f, v0
	v_dot4c_i32_i8_e32 v3, v0, v39
	v_and_b32_e32 v0, 0xf0f0f0f, v54
	v_dot4c_i32_i8_e32 v2, v0, v32
	v_lshrrev_b32_e32 v0, 4, v54
	v_and_b32_e32 v0, 0xf0f0f0f, v0
	v_dot4c_i32_i8_e32 v2, v0, v33
	v_and_b32_e32 v0, 0xf0f0f0f, v55
	v_dot4c_i32_i8_e32 v3, v0, v34
	v_lshrrev_b32_e32 v0, 4, v55
	v_and_b32_e32 v0, 0xf0f0f0f, v0
	v_dot4c_i32_i8_e32 v3, v0, v35
	v_and_b32_e32 v0, 0xf0f0f0f, v44
	v_dot4c_i32_i8_e32 v4, v0, v36
	v_lshrrev_b32_e32 v0, 4, v44
	v_and_b32_e32 v0, 0xf0f0f0f, v0
	v_dot4c_i32_i8_e32 v4, v0, v37
	v_and_b32_e32 v0, 0xf0f0f0f, v45
	v_mov_b32_e32 v5, 0
	v_dot4c_i32_i8_e32 v5, v0, v38
	v_lshrrev_b32_e32 v0, 4, v45
	v_and_b32_e32 v0, 0xf0f0f0f, v0
	v_dot4c_i32_i8_e32 v5, v0, v39
	v_and_b32_e32 v0, 0xf0f0f0f, v46
	v_dot4c_i32_i8_e32 v4, v0, v32
	v_lshrrev_b32_e32 v0, 4, v46
	v_and_b32_e32 v0, 0xf0f0f0f, v0
	v_dot4c_i32_i8_e32 v4, v0, v33
	v_and_b32_e32 v0, 0xf0f0f0f, v47
	v_dot4c_i32_i8_e32 v5, v0, v34
	v_lshrrev_b32_e32 v0, 4, v47
	v_and_b32_e32 v0, 0xf0f0f0f, v0
	v_dot4c_i32_i8_e32 v5, v0, v35
	v_sub_u32_e32 v3, v3, v171
	v_add_u32_e32 v2, v3, v2
	v_cvt_f32_i32_e32 v3, v2
	v_sub_u32_e32 v5, v5, v171
	v_add_u32_e32 v4, v5, v4
	v_cvt_f32_i32_e32 v2, v4
	s_waitcnt vmcnt(8)
	v_and_b32_e32 v1, 0xffff0000, v198
	v_and_b32_e32 v0, 0xffff0000, v199
	v_pk_fma_f32 v[144:145], v[0:1], v[2:3], v[144:145]
	ds_read_b128 v[4:7], v166 offset:4096
	ds_read_b128 v[0:3], v166 offset:4112
	ds_read_u16 v16, v93 offset:16768
	ds_read_u16 v17, v93 offset:16784
	ds_read_u16 v18, v93 offset:16800
	ds_read_u16 v19, v93 offset:16816
	v_mov_b32_e32 v44, 0
	s_waitcnt lgkmcnt(3)
	v_add_u32_e32 v16, s44, v16
	v_lshl_or_b32 v20, v16, 7, v165
	v_lshl_or_b32 v45, v16, 4, v95
	s_waitcnt lgkmcnt(2)
	v_add_u32_e32 v16, s44, v17
	v_lshl_or_b32 v17, v16, 7, v165
	v_lshl_or_b32 v46, v16, 4, v95
	s_waitcnt lgkmcnt(1)
	v_add_u32_e32 v16, s44, v18
	global_load_dwordx4 v[80:83], v20, s[0:1] sc1
	global_load_dwordx4 v[68:71], v17, s[0:1] sc1
	v_lshl_or_b32 v17, v16, 7, v165
	v_lshl_or_b32 v47, v16, 4, v95
	s_waitcnt lgkmcnt(0)
	v_add_u32_e32 v16, s44, v19
	global_load_dwordx4 v[52:55], v17, s[0:1] sc1
	v_lshl_or_b32 v17, v16, 7, v165
	v_lshl_or_b32 v60, v16, 4, v95
	ds_read_u16 v16, v93 offset:16832
	global_load_dwordx4 v[36:39], v17, s[0:1] sc1
	v_dot4c_i32_i8_e32 v44, 0x1010101, v4
	v_dot4c_i32_i8_e32 v44, 0x1010101, v5
	v_dot4c_i32_i8_e32 v44, 0x1010101, v6
	s_waitcnt lgkmcnt(0)
	v_add_u32_e32 v16, s44, v16
	v_lshl_or_b32 v17, v16, 7, v165
	v_lshl_or_b32 v61, v16, 4, v95
	ds_read_u16 v16, v93 offset:16848
	global_load_dwordx4 v[32:35], v17, s[0:1] sc1
	v_dot4c_i32_i8_e32 v44, 0x1010101, v7
	v_dot4c_i32_i8_e32 v44, 0x1010101, v0
	v_dot4c_i32_i8_e32 v44, 0x1010101, v1
	s_waitcnt lgkmcnt(0)
	v_add_u32_e32 v16, s44, v16
	v_lshl_or_b32 v17, v16, 7, v165
	v_lshl_or_b32 v62, v16, 4, v95
	ds_read_u16 v16, v93 offset:16864
	global_load_dwordx4 v[28:31], v17, s[0:1] sc1
	v_dot4c_i32_i8_e32 v44, 0x1010101, v2
	v_dot4c_i32_i8_e32 v44, 0x1010101, v3
	s_waitcnt lgkmcnt(0)
	v_add_u32_e32 v16, s44, v16
	v_lshl_or_b32 v17, v16, 7, v165
	v_lshl_or_b32 v63, v16, 4, v95
	ds_read_u16 v16, v93 offset:16880
	global_load_dwordx4 v[20:23], v17, s[0:1] sc1
	v_lshlrev_b32_e32 v84, 3, v44
	s_waitcnt vmcnt(14)
	v_and_b32_e32 v44, 0xf0f0f0f, v72
	s_waitcnt lgkmcnt(0)
	v_add_u32_e32 v76, s44, v16
	v_lshl_or_b32 v16, v76, 7, v165
	global_load_dwordx4 v[16:19], v16, s[0:1] sc1
	v_lshl_or_b32 v76, v76, 4, v95
	v_mov_b32_e32 v46, 0
	v_dot4c_i32_i8_e32 v46, v44, v4
	v_lshrrev_b32_e32 v44, 4, v72
	v_and_b32_e32 v44, 0xf0f0f0f, v44
	v_dot4c_i32_i8_e32 v46, v44, v5
	v_and_b32_e32 v44, 0xf0f0f0f, v73
	v_mov_b32_e32 v47, 0
	v_dot4c_i32_i8_e32 v47, v44, v6
	v_lshrrev_b32_e32 v44, 4, v73
	v_and_b32_e32 v44, 0xf0f0f0f, v44
	v_dot4c_i32_i8_e32 v47, v44, v7
	v_and_b32_e32 v44, 0xf0f0f0f, v74
	v_dot4c_i32_i8_e32 v46, v44, v0
	v_lshrrev_b32_e32 v44, 4, v74
	v_and_b32_e32 v44, 0xf0f0f0f, v44
	v_dot4c_i32_i8_e32 v46, v44, v1
	v_and_b32_e32 v44, 0xf0f0f0f, v75
	v_dot4c_i32_i8_e32 v47, v44, v2
	v_lshrrev_b32_e32 v44, 4, v75
	v_and_b32_e32 v44, 0xf0f0f0f, v44
	v_dot4c_i32_i8_e32 v47, v44, v3
	s_waitcnt vmcnt(14)
	v_and_b32_e32 v44, 0xf0f0f0f, v64
	v_mov_b32_e32 v60, 0
	v_dot4c_i32_i8_e32 v60, v44, v4
	v_lshrrev_b32_e32 v44, 4, v64
	v_and_b32_e32 v44, 0xf0f0f0f, v44
	v_dot4c_i32_i8_e32 v60, v44, v5
	v_and_b32_e32 v44, 0xf0f0f0f, v65
	v_mov_b32_e32 v61, 0
	v_dot4c_i32_i8_e32 v61, v44, v6
	v_lshrrev_b32_e32 v44, 4, v65
	v_and_b32_e32 v44, 0xf0f0f0f, v44
	v_dot4c_i32_i8_e32 v61, v44, v7
	v_and_b32_e32 v44, 0xf0f0f0f, v66
	v_dot4c_i32_i8_e32 v60, v44, v0
	v_lshrrev_b32_e32 v44, 4, v66
	v_and_b32_e32 v44, 0xf0f0f0f, v44
	v_dot4c_i32_i8_e32 v60, v44, v1
	v_and_b32_e32 v44, 0xf0f0f0f, v67
	v_dot4c_i32_i8_e32 v61, v44, v2
	v_lshrrev_b32_e32 v44, 4, v67
	v_and_b32_e32 v44, 0xf0f0f0f, v44
	v_dot4c_i32_i8_e32 v61, v44, v3
	v_add_u32_e32 v46, v46, v47
	v_sub_u32_e32 v46, v46, v84
	s_waitcnt vmcnt(8)
	v_and_b32_e32 v45, 0xffff0000, v200
	v_add_u32_e32 v47, v60, v61
	v_sub_u32_e32 v60, v47, v84
	v_cvt_f32_i32_e32 v47, v46
	v_cvt_f32_i32_e32 v46, v60
	v_and_b32_e32 v44, 0xffff0000, v201
	v_pk_fma_f32 v[142:143], v[44:45], v[46:47], v[142:143]
	v_and_b32_e32 v44, 0xf0f0f0f, v56
	v_mov_b32_e32 v46, 0
	v_dot4c_i32_i8_e32 v46, v44, v4
	v_lshrrev_b32_e32 v44, 4, v56
	v_and_b32_e32 v44, 0xf0f0f0f, v44
	v_dot4c_i32_i8_e32 v46, v44, v5
	v_and_b32_e32 v44, 0xf0f0f0f, v57
	v_mov_b32_e32 v47, 0
	v_dot4c_i32_i8_e32 v47, v44, v6
	v_lshrrev_b32_e32 v44, 4, v57
	v_and_b32_e32 v44, 0xf0f0f0f, v44
	v_dot4c_i32_i8_e32 v47, v44, v7
	v_and_b32_e32 v44, 0xf0f0f0f, v58
	v_dot4c_i32_i8_e32 v46, v44, v0
	v_lshrrev_b32_e32 v44, 4, v58
	v_and_b32_e32 v44, 0xf0f0f0f, v44
	v_dot4c_i32_i8_e32 v46, v44, v1
	v_and_b32_e32 v44, 0xf0f0f0f, v59
	v_dot4c_i32_i8_e32 v47, v44, v2
	v_lshrrev_b32_e32 v44, 4, v59
	v_and_b32_e32 v44, 0xf0f0f0f, v44
	v_dot4c_i32_i8_e32 v47, v44, v3
	v_and_b32_e32 v44, 0xf0f0f0f, v48
	v_mov_b32_e32 v56, 0
	v_dot4c_i32_i8_e32 v56, v44, v4
	v_lshrrev_b32_e32 v44, 4, v48
	v_and_b32_e32 v44, 0xf0f0f0f, v44
	v_dot4c_i32_i8_e32 v56, v44, v5
	v_and_b32_e32 v44, 0xf0f0f0f, v49
	v_mov_b32_e32 v48, 0
	v_dot4c_i32_i8_e32 v48, v44, v6
	v_lshrrev_b32_e32 v44, 4, v49
	v_and_b32_e32 v44, 0xf0f0f0f, v44
	v_dot4c_i32_i8_e32 v48, v44, v7
	v_and_b32_e32 v44, 0xf0f0f0f, v50
	v_dot4c_i32_i8_e32 v56, v44, v0
	v_lshrrev_b32_e32 v44, 4, v50
	v_and_b32_e32 v44, 0xf0f0f0f, v44
	v_dot4c_i32_i8_e32 v56, v44, v1
	v_and_b32_e32 v44, 0xf0f0f0f, v51
	v_dot4c_i32_i8_e32 v48, v44, v2
	v_lshrrev_b32_e32 v44, 4, v51
	v_and_b32_e32 v44, 0xf0f0f0f, v44
	v_dot4c_i32_i8_e32 v48, v44, v3
	v_add_u32_e32 v46, v46, v47
	v_sub_u32_e32 v46, v46, v84
	s_waitcnt vmcnt(8)
	v_and_b32_e32 v45, 0xffff0000, v202
	v_add_u32_e32 v47, v56, v48
	v_sub_u32_e32 v48, v47, v84
	v_cvt_f32_i32_e32 v47, v46
	v_cvt_f32_i32_e32 v46, v48
	v_and_b32_e32 v44, 0xffff0000, v203
	v_pk_fma_f32 v[140:141], v[44:45], v[46:47], v[140:141]
	v_and_b32_e32 v44, 0xf0f0f0f, v40
	v_mov_b32_e32 v45, 0
	v_lshrrev_b32_e32 v40, 4, v40
	v_dot4c_i32_i8_e32 v45, v44, v4
	v_and_b32_e32 v40, 0xf0f0f0f, v40
	v_dot4c_i32_i8_e32 v45, v40, v5
	v_and_b32_e32 v40, 0xf0f0f0f, v41
	v_mov_b32_e32 v44, 0
	v_dot4c_i32_i8_e32 v44, v40, v6
	v_lshrrev_b32_e32 v40, 4, v41
	v_and_b32_e32 v40, 0xf0f0f0f, v40
	v_dot4c_i32_i8_e32 v44, v40, v7
	v_and_b32_e32 v40, 0xf0f0f0f, v42
	v_dot4c_i32_i8_e32 v45, v40, v0
	v_lshrrev_b32_e32 v40, 4, v42
	v_and_b32_e32 v40, 0xf0f0f0f, v40
	v_dot4c_i32_i8_e32 v45, v40, v1
	v_and_b32_e32 v40, 0xf0f0f0f, v43
	v_dot4c_i32_i8_e32 v44, v40, v2
	v_lshrrev_b32_e32 v40, 4, v43
	v_and_b32_e32 v40, 0xf0f0f0f, v40
	v_dot4c_i32_i8_e32 v44, v40, v3
	v_and_b32_e32 v40, 0xf0f0f0f, v24
	v_mov_b32_e32 v41, 0
	v_lshrrev_b32_e32 v24, 4, v24
	v_dot4c_i32_i8_e32 v41, v40, v4
	v_and_b32_e32 v24, 0xf0f0f0f, v24
	v_dot4c_i32_i8_e32 v41, v24, v5
	v_and_b32_e32 v24, 0xf0f0f0f, v25
	v_mov_b32_e32 v40, 0
	v_dot4c_i32_i8_e32 v40, v24, v6
	v_lshrrev_b32_e32 v24, 4, v25
	v_and_b32_e32 v24, 0xf0f0f0f, v24
	v_dot4c_i32_i8_e32 v40, v24, v7
	v_and_b32_e32 v24, 0xf0f0f0f, v26
	v_dot4c_i32_i8_e32 v41, v24, v0
	v_lshrrev_b32_e32 v24, 4, v26
	v_and_b32_e32 v24, 0xf0f0f0f, v24
	v_dot4c_i32_i8_e32 v41, v24, v1
	v_and_b32_e32 v24, 0xf0f0f0f, v27
	v_dot4c_i32_i8_e32 v40, v24, v2
	v_lshrrev_b32_e32 v24, 4, v27
	v_and_b32_e32 v24, 0xf0f0f0f, v24
	v_dot4c_i32_i8_e32 v40, v24, v3
	v_add_u32_e32 v26, v45, v44
	v_sub_u32_e32 v26, v26, v84
	s_waitcnt vmcnt(8)
	v_and_b32_e32 v25, 0xffff0000, v204
	v_add_u32_e32 v27, v41, v40
	v_sub_u32_e32 v40, v27, v84
	v_cvt_f32_i32_e32 v27, v26
	v_cvt_f32_i32_e32 v26, v40
	v_and_b32_e32 v24, 0xffff0000, v205
	v_pk_fma_f32 v[138:139], v[24:25], v[26:27], v[138:139]
	v_and_b32_e32 v24, 0xf0f0f0f, v12
	v_mov_b32_e32 v25, 0
	v_lshrrev_b32_e32 v12, 4, v12
	v_dot4c_i32_i8_e32 v25, v24, v4
	v_and_b32_e32 v12, 0xf0f0f0f, v12
	v_dot4c_i32_i8_e32 v25, v12, v5
	v_and_b32_e32 v12, 0xf0f0f0f, v13
	v_mov_b32_e32 v24, 0
	v_dot4c_i32_i8_e32 v24, v12, v6
	v_lshrrev_b32_e32 v12, 4, v13
	v_and_b32_e32 v12, 0xf0f0f0f, v12
	v_dot4c_i32_i8_e32 v24, v12, v7
	v_and_b32_e32 v12, 0xf0f0f0f, v14
	v_dot4c_i32_i8_e32 v25, v12, v0
	v_lshrrev_b32_e32 v12, 4, v14
	v_and_b32_e32 v12, 0xf0f0f0f, v12
	v_dot4c_i32_i8_e32 v25, v12, v1
	v_and_b32_e32 v12, 0xf0f0f0f, v15
	v_dot4c_i32_i8_e32 v24, v12, v2
	v_lshrrev_b32_e32 v12, 4, v15
	v_and_b32_e32 v12, 0xf0f0f0f, v12
	v_dot4c_i32_i8_e32 v24, v12, v3
	v_and_b32_e32 v12, 0xf0f0f0f, v8
	v_mov_b32_e32 v13, 0
	v_lshrrev_b32_e32 v8, 4, v8
	v_dot4c_i32_i8_e32 v13, v12, v4
	v_and_b32_e32 v8, 0xf0f0f0f, v8
	v_dot4c_i32_i8_e32 v13, v8, v5
	v_and_b32_e32 v8, 0xf0f0f0f, v9
	v_mov_b32_e32 v12, 0
	v_dot4c_i32_i8_e32 v12, v8, v6
	v_lshrrev_b32_e32 v8, 4, v9
	v_and_b32_e32 v8, 0xf0f0f0f, v8
	v_dot4c_i32_i8_e32 v12, v8, v7
	v_and_b32_e32 v8, 0xf0f0f0f, v10
	v_dot4c_i32_i8_e32 v13, v8, v0
	v_lshrrev_b32_e32 v8, 4, v10
	v_and_b32_e32 v8, 0xf0f0f0f, v8
	v_dot4c_i32_i8_e32 v13, v8, v1
	v_and_b32_e32 v8, 0xf0f0f0f, v11
	v_dot4c_i32_i8_e32 v12, v8, v2
	v_lshrrev_b32_e32 v8, 4, v11
	v_and_b32_e32 v8, 0xf0f0f0f, v8
	v_dot4c_i32_i8_e32 v12, v8, v3
	v_add_u32_e32 v10, v25, v24
	v_sub_u32_e32 v10, v10, v84
	s_waitcnt vmcnt(8)
	v_and_b32_e32 v9, 0xffff0000, v206
	v_add_u32_e32 v11, v13, v12
	v_sub_u32_e32 v12, v11, v84
	v_cvt_f32_i32_e32 v11, v10
	v_cvt_f32_i32_e32 v10, v12
	v_and_b32_e32 v8, 0xffff0000, v207
	v_pk_fma_f32 v[136:137], v[8:9], v[10:11], v[136:137]
	ds_read_u16 v8, v93 offset:16896
	ds_read_u16 v9, v93 offset:16912
	ds_read_u16 v10, v93 offset:16928
	ds_read_u16 v11, v93 offset:16944
	s_waitcnt lgkmcnt(3)
	v_add_u32_e32 v8, s44, v8
	v_lshl_or_b32 v12, v8, 7, v165
	v_lshl_or_b32 v40, v8, 4, v95
	s_waitcnt lgkmcnt(2)
	v_add_u32_e32 v8, s44, v9
	v_lshl_or_b32 v9, v8, 7, v165
	v_lshl_or_b32 v41, v8, 4, v95
	s_waitcnt lgkmcnt(1)
	v_add_u32_e32 v8, s44, v10
	global_load_dwordx4 v[76:79], v12, s[0:1] sc1
	global_load_dwordx4 v[72:75], v9, s[0:1] sc1
	v_lshl_or_b32 v9, v8, 7, v165
	v_lshl_or_b32 v42, v8, 4, v95
	s_waitcnt lgkmcnt(0)
	v_add_u32_e32 v8, s44, v11
	global_load_dwordx4 v[60:63], v9, s[0:1] sc1
	v_lshl_or_b32 v9, v8, 7, v165
	v_lshl_or_b32 v43, v8, 4, v95
	ds_read_u16 v8, v93 offset:16960
	global_load_dwordx4 v[56:59], v9, s[0:1] sc1
	s_waitcnt lgkmcnt(0)
	v_add_u32_e32 v8, s44, v8
	v_lshl_or_b32 v9, v8, 7, v165
	v_lshl_or_b32 v48, v8, 4, v95
	ds_read_u16 v8, v93 offset:16976
	global_load_dwordx4 v[44:47], v9, s[0:1] sc1
	s_waitcnt lgkmcnt(0)
	v_add_u32_e32 v8, s44, v8
	v_lshl_or_b32 v9, v8, 7, v165
	v_lshl_or_b32 v49, v8, 4, v95
	ds_read_u16 v8, v93 offset:16992
	global_load_dwordx4 v[24:27], v9, s[0:1] sc1
	s_waitcnt lgkmcnt(0)
	v_add_u32_e32 v8, s44, v8
	v_lshl_or_b32 v9, v8, 7, v165
	v_lshl_or_b32 v50, v8, 4, v95
	ds_read_u16 v8, v93 offset:17008
	global_load_dwordx4 v[12:15], v9, s[0:1] sc1
	s_waitcnt lgkmcnt(0)
	v_add_u32_e32 v51, s44, v8
	v_lshl_or_b32 v8, v51, 7, v165
	global_load_dwordx4 v[8:11], v8, s[0:1] sc1
	v_lshl_or_b32 v51, v51, 4, v95
	s_waitcnt vmcnt(15)
	v_and_b32_e32 v40, 0xf0f0f0f, v80
	v_mov_b32_e32 v42, 0
	v_dot4c_i32_i8_e32 v42, v40, v4
	v_lshrrev_b32_e32 v40, 4, v80
	v_and_b32_e32 v40, 0xf0f0f0f, v40
	v_dot4c_i32_i8_e32 v42, v40, v5
	v_and_b32_e32 v40, 0xf0f0f0f, v81
	v_mov_b32_e32 v43, 0
	v_dot4c_i32_i8_e32 v43, v40, v6
	v_lshrrev_b32_e32 v40, 4, v81
	v_and_b32_e32 v40, 0xf0f0f0f, v40
	v_dot4c_i32_i8_e32 v43, v40, v7
	v_and_b32_e32 v40, 0xf0f0f0f, v82
	v_dot4c_i32_i8_e32 v42, v40, v0
	v_lshrrev_b32_e32 v40, 4, v82
	v_and_b32_e32 v40, 0xf0f0f0f, v40
	v_dot4c_i32_i8_e32 v42, v40, v1
	v_and_b32_e32 v40, 0xf0f0f0f, v83
	v_dot4c_i32_i8_e32 v43, v40, v2
	v_lshrrev_b32_e32 v40, 4, v83
	v_and_b32_e32 v40, 0xf0f0f0f, v40
	v_dot4c_i32_i8_e32 v43, v40, v3
	s_waitcnt vmcnt(14)
	v_and_b32_e32 v40, 0xf0f0f0f, v68
	v_mov_b32_e32 v48, 0
	v_dot4c_i32_i8_e32 v48, v40, v4
	v_lshrrev_b32_e32 v40, 4, v68
	v_and_b32_e32 v40, 0xf0f0f0f, v40
	v_dot4c_i32_i8_e32 v48, v40, v5
	v_and_b32_e32 v40, 0xf0f0f0f, v69
	v_mov_b32_e32 v49, 0
	v_dot4c_i32_i8_e32 v49, v40, v6
	v_lshrrev_b32_e32 v40, 4, v69
	v_and_b32_e32 v40, 0xf0f0f0f, v40
	v_dot4c_i32_i8_e32 v49, v40, v7
	v_and_b32_e32 v40, 0xf0f0f0f, v70
	v_dot4c_i32_i8_e32 v48, v40, v0
	v_lshrrev_b32_e32 v40, 4, v70
	v_and_b32_e32 v40, 0xf0f0f0f, v40
	v_dot4c_i32_i8_e32 v48, v40, v1
	v_and_b32_e32 v40, 0xf0f0f0f, v71
	v_dot4c_i32_i8_e32 v49, v40, v2
	v_lshrrev_b32_e32 v40, 4, v71
	v_and_b32_e32 v40, 0xf0f0f0f, v40
	v_dot4c_i32_i8_e32 v49, v40, v3
	v_add_u32_e32 v42, v42, v43
	v_sub_u32_e32 v42, v42, v84
	s_waitcnt vmcnt(8)
	v_and_b32_e32 v41, 0xffff0000, v208
	v_sub_u32_e32 v43, v49, v84
	v_add_u32_e32 v48, v43, v48
	v_cvt_f32_i32_e32 v43, v42
	v_cvt_f32_i32_e32 v42, v48
	v_and_b32_e32 v40, 0xffff0000, v209
	v_pk_fma_f32 v[134:135], v[40:41], v[42:43], v[134:135]
	v_and_b32_e32 v40, 0xf0f0f0f, v52
	v_mov_b32_e32 v41, 0
	v_dot4c_i32_i8_e32 v41, v40, v4
	v_lshrrev_b32_e32 v40, 4, v52
	v_and_b32_e32 v40, 0xf0f0f0f, v40
	v_dot4c_i32_i8_e32 v41, v40, v5
	v_and_b32_e32 v40, 0xf0f0f0f, v53
	v_mov_b32_e32 v42, 0
	v_dot4c_i32_i8_e32 v42, v40, v6
	v_lshrrev_b32_e32 v40, 4, v53
	v_and_b32_e32 v40, 0xf0f0f0f, v40
	v_dot4c_i32_i8_e32 v42, v40, v7
	v_and_b32_e32 v40, 0xf0f0f0f, v54
	v_dot4c_i32_i8_e32 v41, v40, v0
	v_lshrrev_b32_e32 v40, 4, v54
	v_and_b32_e32 v40, 0xf0f0f0f, v40
	v_dot4c_i32_i8_e32 v41, v40, v1
	v_and_b32_e32 v40, 0xf0f0f0f, v55
	v_dot4c_i32_i8_e32 v42, v40, v2
	v_lshrrev_b32_e32 v40, 4, v55
	v_and_b32_e32 v40, 0xf0f0f0f, v40
	v_dot4c_i32_i8_e32 v42, v40, v3
	v_and_b32_e32 v40, 0xf0f0f0f, v36
	v_mov_b32_e32 v43, 0
	v_lshrrev_b32_e32 v36, 4, v36
	v_dot4c_i32_i8_e32 v43, v40, v4
	v_and_b32_e32 v36, 0xf0f0f0f, v36
	v_dot4c_i32_i8_e32 v43, v36, v5
	v_and_b32_e32 v36, 0xf0f0f0f, v37
	v_mov_b32_e32 v40, 0
	v_dot4c_i32_i8_e32 v40, v36, v6
	v_lshrrev_b32_e32 v36, 4, v37
	v_and_b32_e32 v36, 0xf0f0f0f, v36
	v_dot4c_i32_i8_e32 v40, v36, v7
	v_and_b32_e32 v36, 0xf0f0f0f, v38
	v_dot4c_i32_i8_e32 v43, v36, v0
	v_lshrrev_b32_e32 v36, 4, v38
	v_and_b32_e32 v36, 0xf0f0f0f, v36
	v_dot4c_i32_i8_e32 v43, v36, v1
	v_and_b32_e32 v36, 0xf0f0f0f, v39
	v_dot4c_i32_i8_e32 v40, v36, v2
	v_lshrrev_b32_e32 v36, 4, v39
	v_and_b32_e32 v36, 0xf0f0f0f, v36
	v_dot4c_i32_i8_e32 v40, v36, v3
	v_sub_u32_e32 v38, v42, v84
	v_add_u32_e32 v38, v38, v41
	s_waitcnt vmcnt(8)
	v_and_b32_e32 v37, 0xffff0000, v210
	v_sub_u32_e32 v39, v40, v84
	v_add_u32_e32 v40, v39, v43
	v_cvt_f32_i32_e32 v39, v38
	v_cvt_f32_i32_e32 v38, v40
	v_and_b32_e32 v36, 0xffff0000, v211
	v_pk_fma_f32 v[132:133], v[36:37], v[38:39], v[132:133]
	v_and_b32_e32 v36, 0xf0f0f0f, v32
	v_mov_b32_e32 v37, 0
	v_lshrrev_b32_e32 v32, 4, v32
	v_dot4c_i32_i8_e32 v37, v36, v4
	v_and_b32_e32 v32, 0xf0f0f0f, v32
	v_dot4c_i32_i8_e32 v37, v32, v5
	v_and_b32_e32 v32, 0xf0f0f0f, v33
	v_mov_b32_e32 v36, 0
	v_dot4c_i32_i8_e32 v36, v32, v6
	v_lshrrev_b32_e32 v32, 4, v33
	v_and_b32_e32 v32, 0xf0f0f0f, v32
	v_dot4c_i32_i8_e32 v36, v32, v7
	v_and_b32_e32 v32, 0xf0f0f0f, v34
	v_dot4c_i32_i8_e32 v37, v32, v0
	v_lshrrev_b32_e32 v32, 4, v34
	v_and_b32_e32 v32, 0xf0f0f0f, v32
	v_dot4c_i32_i8_e32 v37, v32, v1
	v_and_b32_e32 v32, 0xf0f0f0f, v35
	v_dot4c_i32_i8_e32 v36, v32, v2
	v_lshrrev_b32_e32 v32, 4, v35
	v_and_b32_e32 v32, 0xf0f0f0f, v32
	v_dot4c_i32_i8_e32 v36, v32, v3
	v_and_b32_e32 v32, 0xf0f0f0f, v28
	v_mov_b32_e32 v33, 0
	v_lshrrev_b32_e32 v28, 4, v28
	v_dot4c_i32_i8_e32 v33, v32, v4
	v_and_b32_e32 v28, 0xf0f0f0f, v28
	v_dot4c_i32_i8_e32 v33, v28, v5
	v_and_b32_e32 v28, 0xf0f0f0f, v29
	v_mov_b32_e32 v32, 0
	v_dot4c_i32_i8_e32 v32, v28, v6
	v_lshrrev_b32_e32 v28, 4, v29
	v_and_b32_e32 v28, 0xf0f0f0f, v28
	v_dot4c_i32_i8_e32 v32, v28, v7
	v_and_b32_e32 v28, 0xf0f0f0f, v30
	v_dot4c_i32_i8_e32 v33, v28, v0
	v_lshrrev_b32_e32 v28, 4, v30
	v_and_b32_e32 v28, 0xf0f0f0f, v28
	v_dot4c_i32_i8_e32 v33, v28, v1
	v_and_b32_e32 v28, 0xf0f0f0f, v31
	v_dot4c_i32_i8_e32 v32, v28, v2
	v_lshrrev_b32_e32 v28, 4, v31
	v_and_b32_e32 v28, 0xf0f0f0f, v28
	v_dot4c_i32_i8_e32 v32, v28, v3
	v_sub_u32_e32 v30, v36, v84
	v_add_u32_e32 v30, v30, v37
	s_waitcnt vmcnt(8)
	v_and_b32_e32 v29, 0xffff0000, v212
	v_sub_u32_e32 v31, v32, v84
	v_add_u32_e32 v32, v31, v33
	v_cvt_f32_i32_e32 v31, v30
	v_cvt_f32_i32_e32 v30, v32
	v_and_b32_e32 v28, 0xffff0000, v213
	v_pk_fma_f32 v[130:131], v[28:29], v[30:31], v[130:131]
	v_and_b32_e32 v28, 0xf0f0f0f, v20
	v_mov_b32_e32 v29, 0
	v_lshrrev_b32_e32 v20, 4, v20
	v_dot4c_i32_i8_e32 v29, v28, v4
	v_and_b32_e32 v20, 0xf0f0f0f, v20
	v_dot4c_i32_i8_e32 v29, v20, v5
	v_and_b32_e32 v20, 0xf0f0f0f, v21
	v_mov_b32_e32 v28, 0
	v_dot4c_i32_i8_e32 v28, v20, v6
	v_lshrrev_b32_e32 v20, 4, v21
	v_and_b32_e32 v20, 0xf0f0f0f, v20
	v_dot4c_i32_i8_e32 v28, v20, v7
	v_and_b32_e32 v20, 0xf0f0f0f, v22
	v_dot4c_i32_i8_e32 v29, v20, v0
	v_lshrrev_b32_e32 v20, 4, v22
	v_and_b32_e32 v20, 0xf0f0f0f, v20
	v_dot4c_i32_i8_e32 v29, v20, v1
	v_and_b32_e32 v20, 0xf0f0f0f, v23
	v_dot4c_i32_i8_e32 v28, v20, v2
	v_lshrrev_b32_e32 v20, 4, v23
	v_and_b32_e32 v20, 0xf0f0f0f, v20
	v_dot4c_i32_i8_e32 v28, v20, v3
	v_and_b32_e32 v20, 0xf0f0f0f, v16
	v_mov_b32_e32 v21, 0
	v_dot4c_i32_i8_e32 v21, v20, v4
	v_lshrrev_b32_e32 v4, 4, v16
	v_and_b32_e32 v4, 0xf0f0f0f, v4
	v_dot4c_i32_i8_e32 v21, v4, v5
	v_and_b32_e32 v4, 0xf0f0f0f, v17
	v_mov_b32_e32 v5, 0
	v_dot4c_i32_i8_e32 v5, v4, v6
	v_lshrrev_b32_e32 v4, 4, v17
	v_and_b32_e32 v4, 0xf0f0f0f, v4
	v_dot4c_i32_i8_e32 v5, v4, v7
	v_and_b32_e32 v4, 0xf0f0f0f, v18
	v_dot4c_i32_i8_e32 v21, v4, v0
	v_lshrrev_b32_e32 v0, 4, v18
	v_and_b32_e32 v0, 0xf0f0f0f, v0
	v_dot4c_i32_i8_e32 v21, v0, v1
	v_and_b32_e32 v0, 0xf0f0f0f, v19
	v_dot4c_i32_i8_e32 v5, v0, v2
	v_lshrrev_b32_e32 v0, 4, v19
	v_and_b32_e32 v0, 0xf0f0f0f, v0
	v_dot4c_i32_i8_e32 v5, v0, v3
	v_sub_u32_e32 v2, v28, v84
	v_add_u32_e32 v2, v2, v29
	s_waitcnt vmcnt(8)
	v_and_b32_e32 v1, 0xffff0000, v214
	v_sub_u32_e32 v3, v5, v84
	v_add_u32_e32 v4, v3, v21
	v_cvt_f32_i32_e32 v3, v2
	v_cvt_f32_i32_e32 v2, v4
	v_and_b32_e32 v0, 0xffff0000, v215
	ds_read_b128 v[32:35], v166 offset:8192
	ds_read_b128 v[28:31], v166 offset:8208
	v_pk_fma_f32 v[128:129], v[0:1], v[2:3], v[128:129]
	ds_read_u16 v1, v93 offset:17024
	ds_read_u16 v2, v93 offset:17040
	ds_read_u16 v3, v93 offset:17056
	ds_read_u16 v4, v93 offset:17072
	v_mov_b32_e32 v0, 0
	s_waitcnt lgkmcnt(3)
	v_add_u32_e32 v1, s44, v1
	v_lshl_or_b32 v5, v1, 7, v165
	s_waitcnt lgkmcnt(2)
	v_add_u32_e32 v2, s44, v2
	global_load_dwordx4 v[84:87], v5, s[0:1] sc1
	v_lshl_or_b32 v5, v2, 7, v165
	s_waitcnt lgkmcnt(1)
	v_add_u32_e32 v3, s44, v3
	global_load_dwordx4 v[80:83], v5, s[0:1] sc1
	v_lshl_or_b32 v5, v3, 7, v165
	s_waitcnt lgkmcnt(0)
	v_add_u32_e32 v4, s44, v4
	global_load_dwordx4 v[68:71], v5, s[0:1] sc1
	v_lshl_or_b32 v5, v4, 7, v165
	global_load_dwordx4 v[64:67], v5, s[0:1] sc1
	ds_read_u16 v5, v93 offset:17088
	v_dot4c_i32_i8_e32 v0, 0x1010101, v32
	v_dot4c_i32_i8_e32 v0, 0x1010101, v33
	v_dot4c_i32_i8_e32 v0, 0x1010101, v34
	v_dot4c_i32_i8_e32 v0, 0x1010101, v35
	s_waitcnt lgkmcnt(0)
	v_add_u32_e32 v5, s44, v5
	v_lshl_or_b32 v6, v5, 7, v165
	global_load_dwordx4 v[52:55], v6, s[0:1] sc1
	ds_read_u16 v6, v93 offset:17104
	v_dot4c_i32_i8_e32 v0, 0x1010101, v28
	v_dot4c_i32_i8_e32 v0, 0x1010101, v29
	v_dot4c_i32_i8_e32 v0, 0x1010101, v30
	v_dot4c_i32_i8_e32 v0, 0x1010101, v31
	s_waitcnt lgkmcnt(0)
	v_add_u32_e32 v6, s44, v6
	v_lshl_or_b32 v7, v6, 7, v165
	global_load_dwordx4 v[48:51], v7, s[0:1] sc1
	ds_read_u16 v7, v93 offset:17120
	v_lshl_or_b32 v2, v2, 4, v95
	v_lshl_or_b32 v1, v1, 4, v95
	v_lshl_or_b32 v3, v3, 4, v95
	v_lshl_or_b32 v4, v4, 4, v95
	s_waitcnt lgkmcnt(0)
	v_add_u32_e32 v7, s44, v7
	v_lshl_or_b32 v16, v7, 7, v165
	global_load_dwordx4 v[40:43], v16, s[0:1] sc1
	ds_read_u16 v16, v93 offset:17136
	v_lshl_or_b32 v5, v5, 4, v95
	v_lshl_or_b32 v6, v6, 4, v95
	v_lshl_or_b32 v7, v7, 4, v95
	v_lshlrev_b32_e32 v169, 3, v0
	s_waitcnt lgkmcnt(0)
	v_add_u32_e32 v16, s44, v16
	v_lshl_or_b32 v17, v16, 7, v165
	global_load_dwordx4 v[36:39], v17, s[0:1] sc1
	v_lshl_or_b32 v16, v16, 4, v95
	s_waitcnt vmcnt(15)
	v_and_b32_e32 v0, 0xf0f0f0f, v76
	v_mov_b32_e32 v2, 0
	v_dot4c_i32_i8_e32 v2, v0, v32
	v_lshrrev_b32_e32 v0, 4, v76
	v_and_b32_e32 v0, 0xf0f0f0f, v0
	v_dot4c_i32_i8_e32 v2, v0, v33
	v_and_b32_e32 v0, 0xf0f0f0f, v77
	v_mov_b32_e32 v3, 0
	v_dot4c_i32_i8_e32 v3, v0, v34
	v_lshrrev_b32_e32 v0, 4, v77
	v_and_b32_e32 v0, 0xf0f0f0f, v0
	v_dot4c_i32_i8_e32 v3, v0, v35
	v_and_b32_e32 v0, 0xf0f0f0f, v78
	v_dot4c_i32_i8_e32 v2, v0, v28
	v_lshrrev_b32_e32 v0, 4, v78
	v_and_b32_e32 v0, 0xf0f0f0f, v0
	v_dot4c_i32_i8_e32 v2, v0, v29
	v_and_b32_e32 v0, 0xf0f0f0f, v79
	v_dot4c_i32_i8_e32 v3, v0, v30
	v_lshrrev_b32_e32 v0, 4, v79
	v_and_b32_e32 v0, 0xf0f0f0f, v0
	v_dot4c_i32_i8_e32 v3, v0, v31
	s_waitcnt vmcnt(14)
	v_and_b32_e32 v0, 0xf0f0f0f, v72
	v_mov_b32_e32 v4, 0
	v_dot4c_i32_i8_e32 v4, v0, v32
	v_lshrrev_b32_e32 v0, 4, v72
	v_and_b32_e32 v0, 0xf0f0f0f, v0
	v_dot4c_i32_i8_e32 v4, v0, v33
	v_and_b32_e32 v0, 0xf0f0f0f, v73
	v_mov_b32_e32 v5, 0
	v_dot4c_i32_i8_e32 v5, v0, v34
	v_lshrrev_b32_e32 v0, 4, v73
	v_and_b32_e32 v0, 0xf0f0f0f, v0
	v_dot4c_i32_i8_e32 v5, v0, v35
	v_and_b32_e32 v0, 0xf0f0f0f, v74
	v_dot4c_i32_i8_e32 v4, v0, v28
	v_lshrrev_b32_e32 v0, 4, v74
	v_and_b32_e32 v0, 0xf0f0f0f, v0
	v_dot4c_i32_i8_e32 v4, v0, v29
	v_and_b32_e32 v0, 0xf0f0f0f, v75
	v_dot4c_i32_i8_e32 v5, v0, v30
	v_lshrrev_b32_e32 v0, 4, v75
	v_and_b32_e32 v0, 0xf0f0f0f, v0
	v_dot4c_i32_i8_e32 v5, v0, v31
	v_add_u32_e32 v2, v2, v3
	v_sub_u32_e32 v2, v2, v169
	s_waitcnt vmcnt(8)
	v_and_b32_e32 v1, 0xffff0000, v216
	v_add_u32_e32 v3, v4, v5
	v_sub_u32_e32 v4, v3, v169
	v_cvt_f32_i32_e32 v3, v2
	v_cvt_f32_i32_e32 v2, v4
	v_and_b32_e32 v0, 0xffff0000, v217
	v_mov_b32_e32 v4, 0
	v_mov_b32_e32 v5, 0
	v_pk_fma_f32 v[126:127], v[0:1], v[2:3], v[126:127]
	v_and_b32_e32 v0, 0xf0f0f0f, v60
	v_mov_b32_e32 v2, 0
	v_dot4c_i32_i8_e32 v2, v0, v32
	v_lshrrev_b32_e32 v0, 4, v60
	v_and_b32_e32 v0, 0xf0f0f0f, v0
	v_dot4c_i32_i8_e32 v2, v0, v33
	v_and_b32_e32 v0, 0xf0f0f0f, v61
	v_mov_b32_e32 v3, 0
	v_dot4c_i32_i8_e32 v3, v0, v34
	v_lshrrev_b32_e32 v0, 4, v61
	v_and_b32_e32 v0, 0xf0f0f0f, v0
	v_dot4c_i32_i8_e32 v3, v0, v35
	v_and_b32_e32 v0, 0xf0f0f0f, v62
	v_dot4c_i32_i8_e32 v2, v0, v28
	v_lshrrev_b32_e32 v0, 4, v62
	v_and_b32_e32 v0, 0xf0f0f0f, v0
	v_dot4c_i32_i8_e32 v2, v0, v29
	v_and_b32_e32 v0, 0xf0f0f0f, v63
	v_dot4c_i32_i8_e32 v3, v0, v30
	v_lshrrev_b32_e32 v0, 4, v63
	v_and_b32_e32 v0, 0xf0f0f0f, v0
	v_dot4c_i32_i8_e32 v3, v0, v31
	v_and_b32_e32 v0, 0xf0f0f0f, v56
	v_dot4c_i32_i8_e32 v4, v0, v32
	v_lshrrev_b32_e32 v0, 4, v56
	v_and_b32_e32 v0, 0xf0f0f0f, v0
	v_dot4c_i32_i8_e32 v4, v0, v33
	v_and_b32_e32 v0, 0xf0f0f0f, v57
	v_dot4c_i32_i8_e32 v5, v0, v34
	v_lshrrev_b32_e32 v0, 4, v57
	v_and_b32_e32 v0, 0xf0f0f0f, v0
	v_dot4c_i32_i8_e32 v5, v0, v35
	v_and_b32_e32 v0, 0xf0f0f0f, v58
	v_dot4c_i32_i8_e32 v4, v0, v28
	v_lshrrev_b32_e32 v0, 4, v58
	v_and_b32_e32 v0, 0xf0f0f0f, v0
	v_dot4c_i32_i8_e32 v4, v0, v29
	v_and_b32_e32 v0, 0xf0f0f0f, v59
	v_dot4c_i32_i8_e32 v5, v0, v30
	v_lshrrev_b32_e32 v0, 4, v59
	v_and_b32_e32 v0, 0xf0f0f0f, v0
	v_dot4c_i32_i8_e32 v5, v0, v31
	v_add_u32_e32 v2, v2, v3
	v_sub_u32_e32 v2, v2, v169
	s_waitcnt vmcnt(8)
	v_and_b32_e32 v1, 0xffff0000, v218
	v_add_u32_e32 v3, v4, v5
	v_sub_u32_e32 v4, v3, v169
	v_cvt_f32_i32_e32 v3, v2
	v_cvt_f32_i32_e32 v2, v4
	v_and_b32_e32 v0, 0xffff0000, v219
	v_mov_b32_e32 v4, 0
	v_mov_b32_e32 v5, 0
	v_pk_fma_f32 v[124:125], v[0:1], v[2:3], v[124:125]
	v_and_b32_e32 v0, 0xf0f0f0f, v44
	v_mov_b32_e32 v2, 0
	v_dot4c_i32_i8_e32 v2, v0, v32
	v_lshrrev_b32_e32 v0, 4, v44
	v_and_b32_e32 v0, 0xf0f0f0f, v0
	v_dot4c_i32_i8_e32 v2, v0, v33
	v_and_b32_e32 v0, 0xf0f0f0f, v45
	v_mov_b32_e32 v3, 0
	v_dot4c_i32_i8_e32 v3, v0, v34
	v_lshrrev_b32_e32 v0, 4, v45
	v_and_b32_e32 v0, 0xf0f0f0f, v0
	v_dot4c_i32_i8_e32 v3, v0, v35
	v_and_b32_e32 v0, 0xf0f0f0f, v46
	v_dot4c_i32_i8_e32 v2, v0, v28
	v_lshrrev_b32_e32 v0, 4, v46
	v_and_b32_e32 v0, 0xf0f0f0f, v0
	v_dot4c_i32_i8_e32 v2, v0, v29
	v_and_b32_e32 v0, 0xf0f0f0f, v47
	v_dot4c_i32_i8_e32 v3, v0, v30
	v_lshrrev_b32_e32 v0, 4, v47
	v_and_b32_e32 v0, 0xf0f0f0f, v0
	v_dot4c_i32_i8_e32 v3, v0, v31
	v_and_b32_e32 v0, 0xf0f0f0f, v24
	v_dot4c_i32_i8_e32 v4, v0, v32
	v_lshrrev_b32_e32 v0, 4, v24
	v_and_b32_e32 v0, 0xf0f0f0f, v0
	v_dot4c_i32_i8_e32 v4, v0, v33
	v_and_b32_e32 v0, 0xf0f0f0f, v25
	v_dot4c_i32_i8_e32 v5, v0, v34
	v_lshrrev_b32_e32 v0, 4, v25
	v_and_b32_e32 v0, 0xf0f0f0f, v0
	v_dot4c_i32_i8_e32 v5, v0, v35
	v_and_b32_e32 v0, 0xf0f0f0f, v26
	v_dot4c_i32_i8_e32 v4, v0, v28
	v_lshrrev_b32_e32 v0, 4, v26
	v_and_b32_e32 v0, 0xf0f0f0f, v0
	v_dot4c_i32_i8_e32 v4, v0, v29
	v_and_b32_e32 v0, 0xf0f0f0f, v27
	v_dot4c_i32_i8_e32 v5, v0, v30
	v_lshrrev_b32_e32 v0, 4, v27
	v_and_b32_e32 v0, 0xf0f0f0f, v0
	v_dot4c_i32_i8_e32 v5, v0, v31
	v_add_u32_e32 v2, v2, v3
	v_sub_u32_e32 v2, v2, v169
	s_waitcnt vmcnt(8)
	v_and_b32_e32 v1, 0xffff0000, v220
	v_add_u32_e32 v3, v4, v5
	v_sub_u32_e32 v4, v3, v169
	v_cvt_f32_i32_e32 v3, v2
	v_cvt_f32_i32_e32 v2, v4
	v_and_b32_e32 v0, 0xffff0000, v221
	v_mov_b32_e32 v4, 0
	v_mov_b32_e32 v5, 0
	v_pk_fma_f32 v[122:123], v[0:1], v[2:3], v[122:123]
	v_and_b32_e32 v0, 0xf0f0f0f, v12
	v_mov_b32_e32 v2, 0
	v_dot4c_i32_i8_e32 v2, v0, v32
	v_lshrrev_b32_e32 v0, 4, v12
	v_and_b32_e32 v0, 0xf0f0f0f, v0
	v_dot4c_i32_i8_e32 v2, v0, v33
	v_and_b32_e32 v0, 0xf0f0f0f, v13
	v_mov_b32_e32 v3, 0
	v_dot4c_i32_i8_e32 v3, v0, v34
	v_lshrrev_b32_e32 v0, 4, v13
	v_and_b32_e32 v0, 0xf0f0f0f, v0
	v_dot4c_i32_i8_e32 v3, v0, v35
	v_and_b32_e32 v0, 0xf0f0f0f, v14
	v_dot4c_i32_i8_e32 v2, v0, v28
	v_lshrrev_b32_e32 v0, 4, v14
	v_and_b32_e32 v0, 0xf0f0f0f, v0
	v_dot4c_i32_i8_e32 v2, v0, v29
	v_and_b32_e32 v0, 0xf0f0f0f, v15
	v_dot4c_i32_i8_e32 v3, v0, v30
	v_lshrrev_b32_e32 v0, 4, v15
	v_and_b32_e32 v0, 0xf0f0f0f, v0
	v_dot4c_i32_i8_e32 v3, v0, v31
	v_and_b32_e32 v0, 0xf0f0f0f, v8
	v_dot4c_i32_i8_e32 v4, v0, v32
	v_lshrrev_b32_e32 v0, 4, v8
	v_and_b32_e32 v0, 0xf0f0f0f, v0
	v_dot4c_i32_i8_e32 v4, v0, v33
	v_and_b32_e32 v0, 0xf0f0f0f, v9
	v_dot4c_i32_i8_e32 v5, v0, v34
	v_lshrrev_b32_e32 v0, 4, v9
	v_and_b32_e32 v0, 0xf0f0f0f, v0
	v_dot4c_i32_i8_e32 v5, v0, v35
	v_and_b32_e32 v0, 0xf0f0f0f, v10
	v_dot4c_i32_i8_e32 v4, v0, v28
	v_lshrrev_b32_e32 v0, 4, v10
	v_and_b32_e32 v0, 0xf0f0f0f, v0
	v_dot4c_i32_i8_e32 v4, v0, v29
	v_and_b32_e32 v0, 0xf0f0f0f, v11
	v_dot4c_i32_i8_e32 v5, v0, v30
	v_lshrrev_b32_e32 v0, 4, v11
	v_and_b32_e32 v0, 0xf0f0f0f, v0
	v_dot4c_i32_i8_e32 v5, v0, v31
	v_add_u32_e32 v2, v2, v3
	v_sub_u32_e32 v2, v2, v169
	s_waitcnt vmcnt(8)
	v_and_b32_e32 v1, 0xffff0000, v222
	v_add_u32_e32 v3, v4, v5
	v_sub_u32_e32 v4, v3, v169
	v_cvt_f32_i32_e32 v3, v2
	v_cvt_f32_i32_e32 v2, v4
	v_and_b32_e32 v0, 0xffff0000, v223
	v_pk_fma_f32 v[120:121], v[0:1], v[2:3], v[120:121]
	ds_read_u16 v0, v93 offset:17152
	ds_read_u16 v1, v93 offset:17168
	ds_read_u16 v2, v93 offset:17184
	ds_read_u16 v3, v93 offset:17200
	s_waitcnt lgkmcnt(3)
	v_add_u32_e32 v0, s44, v0
	v_lshl_or_b32 v4, v0, 7, v165
	v_lshl_or_b32 v44, v0, 4, v95
	s_waitcnt lgkmcnt(2)
	v_add_u32_e32 v0, s44, v1
	v_lshl_or_b32 v1, v0, 7, v165
	v_lshl_or_b32 v45, v0, 4, v95
	s_waitcnt lgkmcnt(1)
	v_add_u32_e32 v0, s44, v2
	global_load_dwordx4 v[72:75], v4, s[0:1] sc1
	global_load_dwordx4 v[24:27], v1, s[0:1] sc1
	v_lshl_or_b32 v1, v0, 7, v165
	v_lshl_or_b32 v46, v0, 4, v95
	s_waitcnt lgkmcnt(0)
	v_add_u32_e32 v0, s44, v3
	global_load_dwordx4 v[20:23], v1, s[0:1] sc1
	v_lshl_or_b32 v1, v0, 7, v165
	v_lshl_or_b32 v47, v0, 4, v95
	ds_read_u16 v0, v93 offset:17216
	global_load_dwordx4 v[16:19], v1, s[0:1] sc1
	s_waitcnt lgkmcnt(0)
	v_add_u32_e32 v0, s44, v0
	v_lshl_or_b32 v1, v0, 7, v165
	v_lshl_or_b32 v56, v0, 4, v95
	ds_read_u16 v0, v93 offset:17232
	global_load_dwordx4 v[12:15], v1, s[0:1] sc1
	s_waitcnt lgkmcnt(0)
	v_add_u32_e32 v0, s44, v0
	v_lshl_or_b32 v1, v0, 7, v165
	v_lshl_or_b32 v57, v0, 4, v95
	ds_read_u16 v0, v93 offset:17248
	global_load_dwordx4 v[8:11], v1, s[0:1] sc1
	s_waitcnt lgkmcnt(0)
	v_add_u32_e32 v0, s44, v0
	v_lshl_or_b32 v1, v0, 7, v165
	v_lshl_or_b32 v58, v0, 4, v95
	ds_read_u16 v0, v93 offset:17264
	global_load_dwordx4 v[4:7], v1, s[0:1] sc1
	s_waitcnt lgkmcnt(0)
	v_add_u32_e32 v59, s44, v0
	v_lshl_or_b32 v0, v59, 7, v165
	global_load_dwordx4 v[0:3], v0, s[0:1] sc1
	v_lshl_or_b32 v59, v59, 4, v95
	s_waitcnt vmcnt(15)
	v_and_b32_e32 v44, 0xf0f0f0f, v84
	v_mov_b32_e32 v46, 0
	v_dot4c_i32_i8_e32 v46, v44, v32
	v_lshrrev_b32_e32 v44, 4, v84
	v_and_b32_e32 v44, 0xf0f0f0f, v44
	v_dot4c_i32_i8_e32 v46, v44, v33
	v_and_b32_e32 v44, 0xf0f0f0f, v85
	v_mov_b32_e32 v47, 0
	v_dot4c_i32_i8_e32 v47, v44, v34
	v_lshrrev_b32_e32 v44, 4, v85
	v_and_b32_e32 v44, 0xf0f0f0f, v44
	v_dot4c_i32_i8_e32 v47, v44, v35
	v_and_b32_e32 v44, 0xf0f0f0f, v86
	v_dot4c_i32_i8_e32 v46, v44, v28
	v_lshrrev_b32_e32 v44, 4, v86
	v_and_b32_e32 v44, 0xf0f0f0f, v44
	v_dot4c_i32_i8_e32 v46, v44, v29
	v_and_b32_e32 v44, 0xf0f0f0f, v87
	v_dot4c_i32_i8_e32 v47, v44, v30
	v_lshrrev_b32_e32 v44, 4, v87
	v_and_b32_e32 v44, 0xf0f0f0f, v44
	v_dot4c_i32_i8_e32 v47, v44, v31
	s_waitcnt vmcnt(14)
	v_and_b32_e32 v44, 0xf0f0f0f, v80
	v_mov_b32_e32 v56, 0
	v_dot4c_i32_i8_e32 v56, v44, v32
	v_lshrrev_b32_e32 v44, 4, v80
	v_and_b32_e32 v44, 0xf0f0f0f, v44
	v_dot4c_i32_i8_e32 v56, v44, v33
	v_and_b32_e32 v44, 0xf0f0f0f, v81
	v_mov_b32_e32 v57, 0
	v_dot4c_i32_i8_e32 v57, v44, v34
	v_lshrrev_b32_e32 v44, 4, v81
	v_and_b32_e32 v44, 0xf0f0f0f, v44
	v_dot4c_i32_i8_e32 v57, v44, v35
	v_and_b32_e32 v44, 0xf0f0f0f, v82
	v_dot4c_i32_i8_e32 v56, v44, v28
	v_lshrrev_b32_e32 v44, 4, v82
	v_and_b32_e32 v44, 0xf0f0f0f, v44
	v_dot4c_i32_i8_e32 v56, v44, v29
	v_and_b32_e32 v44, 0xf0f0f0f, v83
	v_dot4c_i32_i8_e32 v57, v44, v30
	v_lshrrev_b32_e32 v44, 4, v83
	v_and_b32_e32 v44, 0xf0f0f0f, v44
	v_dot4c_i32_i8_e32 v57, v44, v31
	v_add_u32_e32 v46, v46, v47
	v_sub_u32_e32 v46, v46, v169
	s_waitcnt vmcnt(8)
	v_and_b32_e32 v45, 0xffff0000, v224
	v_sub_u32_e32 v47, v57, v169
	v_add_u32_e32 v56, v47, v56
	v_cvt_f32_i32_e32 v47, v46
	v_cvt_f32_i32_e32 v46, v56
	v_and_b32_e32 v44, 0xffff0000, v225
	v_mov_b32_e32 v56, 0
	v_mov_b32_e32 v57, 0
	v_pk_fma_f32 v[118:119], v[44:45], v[46:47], v[118:119]
	v_and_b32_e32 v44, 0xf0f0f0f, v68
	v_mov_b32_e32 v46, 0
	v_dot4c_i32_i8_e32 v46, v44, v32
	v_lshrrev_b32_e32 v44, 4, v68
	v_and_b32_e32 v44, 0xf0f0f0f, v44
	v_dot4c_i32_i8_e32 v46, v44, v33
	v_and_b32_e32 v44, 0xf0f0f0f, v69
	v_mov_b32_e32 v47, 0
	v_dot4c_i32_i8_e32 v47, v44, v34
	v_lshrrev_b32_e32 v44, 4, v69
	v_and_b32_e32 v44, 0xf0f0f0f, v44
	v_dot4c_i32_i8_e32 v47, v44, v35
	v_and_b32_e32 v44, 0xf0f0f0f, v70
	v_dot4c_i32_i8_e32 v46, v44, v28
	v_lshrrev_b32_e32 v44, 4, v70
	v_and_b32_e32 v44, 0xf0f0f0f, v44
	v_dot4c_i32_i8_e32 v46, v44, v29
	v_and_b32_e32 v44, 0xf0f0f0f, v71
	v_dot4c_i32_i8_e32 v47, v44, v30
	v_lshrrev_b32_e32 v44, 4, v71
	v_and_b32_e32 v44, 0xf0f0f0f, v44
	v_dot4c_i32_i8_e32 v47, v44, v31
	v_and_b32_e32 v44, 0xf0f0f0f, v64
	v_dot4c_i32_i8_e32 v56, v44, v32
	v_lshrrev_b32_e32 v44, 4, v64
	v_and_b32_e32 v44, 0xf0f0f0f, v44
	v_dot4c_i32_i8_e32 v56, v44, v33
	v_and_b32_e32 v44, 0xf0f0f0f, v65
	v_dot4c_i32_i8_e32 v57, v44, v34
	v_lshrrev_b32_e32 v44, 4, v65
	v_and_b32_e32 v44, 0xf0f0f0f, v44
	v_dot4c_i32_i8_e32 v57, v44, v35
	v_and_b32_e32 v44, 0xf0f0f0f, v66
	v_dot4c_i32_i8_e32 v56, v44, v28
	v_lshrrev_b32_e32 v44, 4, v66
	v_and_b32_e32 v44, 0xf0f0f0f, v44
	v_dot4c_i32_i8_e32 v56, v44, v29
	v_and_b32_e32 v44, 0xf0f0f0f, v67
	v_dot4c_i32_i8_e32 v57, v44, v30
	v_lshrrev_b32_e32 v44, 4, v67
	v_and_b32_e32 v44, 0xf0f0f0f, v44
	v_dot4c_i32_i8_e32 v57, v44, v31
	v_sub_u32_e32 v47, v47, v169
	v_add_u32_e32 v46, v47, v46
	v_cvt_f32_i32_e32 v47, v46
	v_sub_u32_e32 v57, v57, v169
	v_add_u32_e32 v56, v57, v56
	v_cvt_f32_i32_e32 v46, v56
	s_waitcnt vmcnt(8)
	v_and_b32_e32 v45, 0xffff0000, v226
	v_and_b32_e32 v44, 0xffff0000, v227
	v_pk_fma_f32 v[116:117], v[44:45], v[46:47], v[116:117]
	v_and_b32_e32 v44, 0xf0f0f0f, v52
	v_mov_b32_e32 v46, 0
	v_dot4c_i32_i8_e32 v46, v44, v32
	v_lshrrev_b32_e32 v44, 4, v52
	v_and_b32_e32 v44, 0xf0f0f0f, v44
	v_dot4c_i32_i8_e32 v46, v44, v33
	v_and_b32_e32 v44, 0xf0f0f0f, v53
	v_mov_b32_e32 v47, 0
	v_dot4c_i32_i8_e32 v47, v44, v34
	v_lshrrev_b32_e32 v44, 4, v53
	v_and_b32_e32 v44, 0xf0f0f0f, v44
	v_dot4c_i32_i8_e32 v47, v44, v35
	v_and_b32_e32 v44, 0xf0f0f0f, v54
	v_dot4c_i32_i8_e32 v46, v44, v28
	v_lshrrev_b32_e32 v44, 4, v54
	v_and_b32_e32 v44, 0xf0f0f0f, v44
	v_dot4c_i32_i8_e32 v46, v44, v29
	v_and_b32_e32 v44, 0xf0f0f0f, v55
	v_dot4c_i32_i8_e32 v47, v44, v30
	v_lshrrev_b32_e32 v44, 4, v55
	v_and_b32_e32 v44, 0xf0f0f0f, v44
	v_dot4c_i32_i8_e32 v47, v44, v31
	v_and_b32_e32 v44, 0xf0f0f0f, v48
	v_mov_b32_e32 v52, 0
	v_dot4c_i32_i8_e32 v52, v44, v32
	v_lshrrev_b32_e32 v44, 4, v48
	v_and_b32_e32 v44, 0xf0f0f0f, v44
	v_dot4c_i32_i8_e32 v52, v44, v33
	v_and_b32_e32 v44, 0xf0f0f0f, v49
	v_mov_b32_e32 v48, 0
	v_dot4c_i32_i8_e32 v48, v44, v34
	v_lshrrev_b32_e32 v44, 4, v49
	v_and_b32_e32 v44, 0xf0f0f0f, v44
	v_dot4c_i32_i8_e32 v48, v44, v35
	v_and_b32_e32 v44, 0xf0f0f0f, v50
	v_dot4c_i32_i8_e32 v52, v44, v28
	v_lshrrev_b32_e32 v44, 4, v50
	v_and_b32_e32 v44, 0xf0f0f0f, v44
	v_dot4c_i32_i8_e32 v52, v44, v29
	v_and_b32_e32 v44, 0xf0f0f0f, v51
	v_dot4c_i32_i8_e32 v48, v44, v30
	v_lshrrev_b32_e32 v44, 4, v51
	v_and_b32_e32 v44, 0xf0f0f0f, v44
	v_dot4c_i32_i8_e32 v48, v44, v31
	v_sub_u32_e32 v47, v47, v169
	v_add_u32_e32 v46, v47, v46
	v_cvt_f32_i32_e32 v47, v46
	v_sub_u32_e32 v48, v48, v169
	v_add_u32_e32 v48, v48, v52
	v_cvt_f32_i32_e32 v46, v48
	s_waitcnt vmcnt(8)
	v_and_b32_e32 v45, 0xffff0000, v228
	v_and_b32_e32 v44, 0xffff0000, v229
	v_pk_fma_f32 v[114:115], v[44:45], v[46:47], v[114:115]
	v_and_b32_e32 v44, 0xf0f0f0f, v40
	v_mov_b32_e32 v45, 0
	v_lshrrev_b32_e32 v40, 4, v40
	v_dot4c_i32_i8_e32 v45, v44, v32
	v_and_b32_e32 v40, 0xf0f0f0f, v40
	v_dot4c_i32_i8_e32 v45, v40, v33
	v_and_b32_e32 v40, 0xf0f0f0f, v41
	v_mov_b32_e32 v44, 0
	v_dot4c_i32_i8_e32 v44, v40, v34
	v_lshrrev_b32_e32 v40, 4, v41
	v_and_b32_e32 v40, 0xf0f0f0f, v40
	v_dot4c_i32_i8_e32 v44, v40, v35
	v_and_b32_e32 v40, 0xf0f0f0f, v42
	v_dot4c_i32_i8_e32 v45, v40, v28
	v_lshrrev_b32_e32 v40, 4, v42
	v_and_b32_e32 v40, 0xf0f0f0f, v40
	v_dot4c_i32_i8_e32 v45, v40, v29
	v_and_b32_e32 v40, 0xf0f0f0f, v43
	v_dot4c_i32_i8_e32 v44, v40, v30
	v_lshrrev_b32_e32 v40, 4, v43
	v_and_b32_e32 v40, 0xf0f0f0f, v40
	v_dot4c_i32_i8_e32 v44, v40, v31
	v_and_b32_e32 v40, 0xf0f0f0f, v36
	v_mov_b32_e32 v41, 0
	v_dot4c_i32_i8_e32 v41, v40, v32
	v_lshrrev_b32_e32 v32, 4, v36
	v_and_b32_e32 v32, 0xf0f0f0f, v32
	v_dot4c_i32_i8_e32 v41, v32, v33
	v_and_b32_e32 v32, 0xf0f0f0f, v37
	v_mov_b32_e32 v33, 0
	v_dot4c_i32_i8_e32 v33, v32, v34
	v_lshrrev_b32_e32 v32, 4, v37
	v_and_b32_e32 v32, 0xf0f0f0f, v32
	v_dot4c_i32_i8_e32 v33, v32, v35
	v_and_b32_e32 v32, 0xf0f0f0f, v38
	v_dot4c_i32_i8_e32 v41, v32, v28
	v_lshrrev_b32_e32 v28, 4, v38
	v_and_b32_e32 v28, 0xf0f0f0f, v28
	v_dot4c_i32_i8_e32 v41, v28, v29
	v_and_b32_e32 v28, 0xf0f0f0f, v39
	v_dot4c_i32_i8_e32 v33, v28, v30
	v_lshrrev_b32_e32 v28, 4, v39
	v_and_b32_e32 v28, 0xf0f0f0f, v28
	v_dot4c_i32_i8_e32 v33, v28, v31
	v_sub_u32_e32 v30, v44, v169
	v_add_u32_e32 v30, v30, v45
	s_waitcnt vmcnt(8)
; #define P12_ISSUE(c_, i_, h_, CW_, SC_) do { _Pragma("unroll") for (int bb = 0; bb < 8; ++bb) { const unsigned ro = (unsigned)(c_) * 16384u + (unsigned)EL[(i_) * 128 + ((h_) * 8 + bb) * 8 + g8]; \
;         CW_[bb] = *(const v4u*)(U4 + (size_t)(ro * 128u + 16u * (unsigned)k8)); SC_[bb] = USS[(size_t)(ro * 8u + (unsigned)k8)]; } } while (0)
; #define P12_COMP(i_, h_, CW_, SC_) do { _Pragma("unroll") for (int bb = 0; bb < 8; ++bb) { int a0 = 0, a1 = 0; P12_U4(CW_[bb].x, xa.x, xa.y, a0); P12_U4(CW_[bb].y, xa.z, xa.w, a1); P12_U4(CW_[bb].z, xb.x, xb.y, a0); P12_U4(CW_[bb].w, xb.z, xb.w, a1); \
;         psum[(i_)][(h_) * 8 + bb] += __uint_as_float(SC_[bb] << 16) * (float)((a0 + a1) - xo); } } while (0)
; #define P12_BAR() asm volatile("" ::: "memory")
; __device__ __forceinline__ void p12_peer(Frame& F) {
;     ...
;     { v4u cwA[8], cwB[8]; unsigned scA[8], scB[8]; v4u xa, xb; int xo;
;       P12_ISSUE(0, 0, 0, cwA, scA);
; _Pragma("nounroll")
;       for (int c = 0; c < 16; ++c) { const int cn = c + 1 < 16 ? c + 1 : 15;
;           P12_XQ(c, 0); P12_ISSUE(c, 0, 1, cwB, scB); P12_BAR(); P12_COMP(0, 0, cwA, scA); P12_ISSUE(c, 1, 0, cwA, scA); P12_BAR(); P12_COMP(0, 1, cwB, scB);
;           P12_XQ(c, 1); P12_ISSUE(c, 1, 1, cwB, scB); P12_BAR(); P12_COMP(1, 0, cwA, scA); P12_ISSUE(c, 2, 0, cwA, scA); P12_BAR(); P12_COMP(1, 1, cwB, scB);
;           P12_XQ(c, 2); P12_ISSUE(c, 2, 1, cwB, scB); P12_BAR(); P12_COMP(2, 0, cwA, scA); P12_ISSUE(c, 3, 0, cwA, scA); P12_BAR(); P12_COMP(2, 1, cwB, scB);
;           P12_XQ(c, 3); P12_ISSUE(c, 3, 1, cwB, scB); P12_BAR(); P12_COMP(3, 0, cwA, scA); P12_ISSUE(cn, 0, 0, cwA, scA); P12_BAR(); P12_COMP(3, 1, cwB, scB);
	v_and_b32_e32 v29, 0xffff0000, v230
	v_sub_u32_e32 v31, v33, v169
	v_add_u32_e32 v32, v31, v41
	v_cvt_f32_i32_e32 v31, v30
	v_cvt_f32_i32_e32 v30, v32
	v_and_b32_e32 v28, 0xffff0000, v231
	ds_read_b128 v[36:39], v166 offset:12288
	ds_read_b128 v[32:35], v166 offset:12304
	v_add_u32_e32 v166, 0x100, v166
	v_pk_fma_f32 v[112:113], v[28:29], v[30:31], v[112:113]
	ds_read_u16 v29, v93 offset:17280
	ds_read_u16 v30, v93 offset:17296
	ds_read_u16 v31, v93 offset:17312
	ds_read_u16 v40, v93 offset:17328
	v_mov_b32_e32 v28, 0
	s_waitcnt lgkmcnt(3)
	v_add_u32_e32 v29, s44, v29
	v_lshl_or_b32 v41, v29, 7, v165
	s_waitcnt lgkmcnt(2)
	v_add_u32_e32 v30, s44, v30
	global_load_dwordx4 v[68:71], v41, s[0:1] sc1
	v_lshl_or_b32 v41, v30, 7, v165
	s_waitcnt lgkmcnt(1)
	v_add_u32_e32 v31, s44, v31
	global_load_dwordx4 v[64:67], v41, s[0:1] sc1
	v_lshl_or_b32 v41, v31, 7, v165
	s_waitcnt lgkmcnt(0)
	v_add_u32_e32 v40, s44, v40
	global_load_dwordx4 v[60:63], v41, s[0:1] sc1
	v_lshl_or_b32 v41, v40, 7, v165
	v_lshl_or_b32 v79, v40, 4, v95
	ds_read_u16 v40, v93 offset:17344
	global_load_dwordx4 v[56:59], v41, s[0:1] sc1
	v_dot4c_i32_i8_e32 v28, 0x1010101, v36
	v_dot4c_i32_i8_e32 v28, 0x1010101, v37
	v_dot4c_i32_i8_e32 v28, 0x1010101, v38
	s_waitcnt lgkmcnt(0)
	v_add_u32_e32 v40, s44, v40
	v_lshl_or_b32 v41, v40, 7, v165
	v_lshl_or_b32 v80, v40, 4, v95
	ds_read_u16 v40, v93 offset:17360
	global_load_dwordx4 v[52:55], v41, s[0:1] sc1
	v_dot4c_i32_i8_e32 v28, 0x1010101, v39
	v_dot4c_i32_i8_e32 v28, 0x1010101, v32
	v_dot4c_i32_i8_e32 v28, 0x1010101, v33
	s_waitcnt lgkmcnt(0)
	v_add_u32_e32 v40, s44, v40
	v_lshl_or_b32 v41, v40, 7, v165
	v_lshl_or_b32 v82, v40, 4, v95
	ds_read_u16 v40, v93 offset:17376
	global_load_dwordx4 v[48:51], v41, s[0:1] sc1
	v_dot4c_i32_i8_e32 v28, 0x1010101, v34
	v_dot4c_i32_i8_e32 v28, 0x1010101, v35
	v_lshl_or_b32 v29, v29, 4, v95
	s_waitcnt lgkmcnt(0)
	v_add_u32_e32 v40, s44, v40
	v_lshl_or_b32 v41, v40, 7, v165
	v_lshl_or_b32 v87, v40, 4, v95
	ds_read_u16 v40, v93 offset:17392
	v_lshl_or_b32 v30, v30, 4, v95
	v_lshl_or_b32 v31, v31, 4, v95
	global_load_dwordx4 v[44:47], v41, s[0:1] sc1
	s_waitcnt lgkmcnt(0)
	v_add_u32_e32 v78, s44, v40
	v_lshl_or_b32 v40, v78, 7, v165
	global_load_dwordx4 v[40:43], v40, s[0:1] sc1
	v_lshl_or_b32 v169, v78, 4, v95
	v_lshlrev_b32_e32 v78, 3, v28
	s_nop 0
	s_nop 0
	s_waitcnt vmcnt(15)
	v_and_b32_e32 v29, 0xf0f0f0f, v72
	v_mov_b32_e32 v28, 0
	v_dot4c_i32_i8_e32 v28, v29, v36
	v_lshrrev_b32_e32 v29, 4, v72
	v_and_b32_e32 v29, 0xf0f0f0f, v29
	v_dot4c_i32_i8_e32 v28, v29, v37
	v_and_b32_e32 v30, 0xf0f0f0f, v73
	v_mov_b32_e32 v29, 0
	v_dot4c_i32_i8_e32 v29, v30, v38
	v_lshrrev_b32_e32 v30, 4, v73
	v_and_b32_e32 v30, 0xf0f0f0f, v30
	v_dot4c_i32_i8_e32 v29, v30, v39
	v_and_b32_e32 v30, 0xf0f0f0f, v74
	v_dot4c_i32_i8_e32 v28, v30, v32
	v_lshrrev_b32_e32 v30, 4, v74
	v_and_b32_e32 v30, 0xf0f0f0f, v30
	v_dot4c_i32_i8_e32 v28, v30, v33
	v_and_b32_e32 v30, 0xf0f0f0f, v75
	v_dot4c_i32_i8_e32 v29, v30, v34
	v_lshrrev_b32_e32 v30, 4, v75
	v_and_b32_e32 v30, 0xf0f0f0f, v30
	v_dot4c_i32_i8_e32 v29, v30, v35
	s_waitcnt vmcnt(14)
	v_and_b32_e32 v31, 0xf0f0f0f, v24
	v_mov_b32_e32 v30, 0
	v_lshrrev_b32_e32 v24, 4, v24
	v_dot4c_i32_i8_e32 v30, v31, v36
	v_and_b32_e32 v24, 0xf0f0f0f, v24
	v_dot4c_i32_i8_e32 v30, v24, v37
	v_and_b32_e32 v24, 0xf0f0f0f, v25
	v_mov_b32_e32 v31, 0
	v_dot4c_i32_i8_e32 v31, v24, v38
	v_lshrrev_b32_e32 v24, 4, v25
	v_and_b32_e32 v24, 0xf0f0f0f, v24
	v_dot4c_i32_i8_e32 v31, v24, v39
	v_and_b32_e32 v24, 0xf0f0f0f, v26
	v_dot4c_i32_i8_e32 v30, v24, v32
	v_lshrrev_b32_e32 v24, 4, v26
	v_and_b32_e32 v24, 0xf0f0f0f, v24
	v_dot4c_i32_i8_e32 v30, v24, v33
	v_and_b32_e32 v24, 0xf0f0f0f, v27
	v_dot4c_i32_i8_e32 v31, v24, v34
	v_lshrrev_b32_e32 v24, 4, v27
	v_and_b32_e32 v24, 0xf0f0f0f, v24
	v_dot4c_i32_i8_e32 v31, v24, v35
	v_add_u32_e32 v26, v28, v29
	v_sub_u32_e32 v26, v26, v78
	s_waitcnt vmcnt(8)
	v_and_b32_e32 v25, 0xffff0000, v232
	v_add_u32_e32 v27, v30, v31
	v_sub_u32_e32 v28, v27, v78
	v_cvt_f32_i32_e32 v27, v26
	v_cvt_f32_i32_e32 v26, v28
	v_and_b32_e32 v24, 0xffff0000, v233
	s_cselect_b32 s44, s44, s45
	s_lshl_b32 s49, s44, 4
	s_sub_u32 s46, s18, s49
	s_subb_u32 s47, s19, 0
	s_cmp_eq_u32 s45, 0x40000
	v_pk_fma_f32 v[110:111], v[24:25], v[26:27], v[110:111]
	v_and_b32_e32 v24, 0xf0f0f0f, v20
	v_mov_b32_e32 v25, 0
	v_lshrrev_b32_e32 v20, 4, v20
	v_dot4c_i32_i8_e32 v25, v24, v36
	v_and_b32_e32 v20, 0xf0f0f0f, v20
	v_dot4c_i32_i8_e32 v25, v20, v37
	v_and_b32_e32 v20, 0xf0f0f0f, v21
	v_mov_b32_e32 v24, 0
	v_dot4c_i32_i8_e32 v24, v20, v38
	v_lshrrev_b32_e32 v20, 4, v21
	v_and_b32_e32 v20, 0xf0f0f0f, v20
	v_dot4c_i32_i8_e32 v24, v20, v39
	v_and_b32_e32 v20, 0xf0f0f0f, v22
	v_dot4c_i32_i8_e32 v25, v20, v32
	v_lshrrev_b32_e32 v20, 4, v22
	v_and_b32_e32 v20, 0xf0f0f0f, v20
	v_dot4c_i32_i8_e32 v25, v20, v33
	v_and_b32_e32 v20, 0xf0f0f0f, v23
	v_dot4c_i32_i8_e32 v24, v20, v34
	v_lshrrev_b32_e32 v20, 4, v23
	v_and_b32_e32 v20, 0xf0f0f0f, v20
	v_dot4c_i32_i8_e32 v24, v20, v35
	v_and_b32_e32 v20, 0xf0f0f0f, v16
	v_mov_b32_e32 v21, 0
	v_lshrrev_b32_e32 v16, 4, v16
	v_dot4c_i32_i8_e32 v21, v20, v36
	v_and_b32_e32 v16, 0xf0f0f0f, v16
	v_dot4c_i32_i8_e32 v21, v16, v37
	v_and_b32_e32 v16, 0xf0f0f0f, v17
	v_mov_b32_e32 v20, 0
	v_dot4c_i32_i8_e32 v20, v16, v38
	v_lshrrev_b32_e32 v16, 4, v17
	v_and_b32_e32 v16, 0xf0f0f0f, v16
	v_dot4c_i32_i8_e32 v20, v16, v39
	v_and_b32_e32 v16, 0xf0f0f0f, v18
	v_dot4c_i32_i8_e32 v21, v16, v32
	v_lshrrev_b32_e32 v16, 4, v18
	v_and_b32_e32 v16, 0xf0f0f0f, v16
	v_dot4c_i32_i8_e32 v21, v16, v33
	v_and_b32_e32 v16, 0xf0f0f0f, v19
	v_dot4c_i32_i8_e32 v20, v16, v34
	v_lshrrev_b32_e32 v16, 4, v19
	v_and_b32_e32 v16, 0xf0f0f0f, v16
	v_dot4c_i32_i8_e32 v20, v16, v35
	v_add_u32_e32 v18, v25, v24
	v_sub_u32_e32 v18, v18, v78
	s_waitcnt vmcnt(8)
; #define P12_ISSUE(c_, i_, h_, CW_, SC_) do { _Pragma("unroll") for (int bb = 0; bb < 8; ++bb) { const unsigned ro = (unsigned)(c_) * 16384u + (unsigned)EL[(i_) * 128 + ((h_) * 8 + bb) * 8 + g8]; \
;         CW_[bb] = *(const v4u*)(U4 + (size_t)(ro * 128u + 16u * (unsigned)k8)); SC_[bb] = USS[(size_t)(ro * 8u + (unsigned)k8)]; } } while (0)
; #define P12_COMP(i_, h_, CW_, SC_) do { _Pragma("unroll") for (int bb = 0; bb < 8; ++bb) { int a0 = 0, a1 = 0; P12_U4(CW_[bb].x, xa.x, xa.y, a0); P12_U4(CW_[bb].y, xa.z, xa.w, a1); P12_U4(CW_[bb].z, xb.x, xb.y, a0); P12_U4(CW_[bb].w, xb.z, xb.w, a1); \
;         psum[(i_)][(h_) * 8 + bb] += __uint_as_float(SC_[bb] << 16) * (float)((a0 + a1) - xo); } } while (0)
; #define P12_BAR() asm volatile("" ::: "memory")
; __device__ __forceinline__ void p12_peer(Frame& F) {
;     ...
;     { v4u cwA[8], cwB[8]; unsigned scA[8], scB[8]; v4u xa, xb; int xo;
;       P12_ISSUE(0, 0, 0, cwA, scA);
; _Pragma("nounroll")
;       for (int c = 0; c < 16; ++c) { const int cn = c + 1 < 16 ? c + 1 : 15;
;           P12_XQ(c, 0); P12_ISSUE(c, 0, 1, cwB, scB); P12_BAR(); P12_COMP(0, 0, cwA, scA); P12_ISSUE(c, 1, 0, cwA, scA); P12_BAR(); P12_COMP(0, 1, cwB, scB);
;           P12_XQ(c, 1); P12_ISSUE(c, 1, 1, cwB, scB); P12_BAR(); P12_COMP(1, 0, cwA, scA); P12_ISSUE(c, 2, 0, cwA, scA); P12_BAR(); P12_COMP(1, 1, cwB, scB);
;           P12_XQ(c, 2); P12_ISSUE(c, 2, 1, cwB, scB); P12_BAR(); P12_COMP(2, 0, cwA, scA); P12_ISSUE(c, 3, 0, cwA, scA); P12_BAR(); P12_COMP(2, 1, cwB, scB);
;           P12_XQ(c, 3); P12_ISSUE(c, 3, 1, cwB, scB); P12_BAR(); P12_COMP(3, 0, cwA, scA); P12_ISSUE(cn, 0, 0, cwA, scA); P12_BAR(); P12_COMP(3, 1, cwB, scB);
	v_and_b32_e32 v17, 0xffff0000, v234
	v_add_u32_e32 v19, v21, v20
	v_sub_u32_e32 v20, v19, v78
	v_cvt_f32_i32_e32 v19, v18
	v_cvt_f32_i32_e32 v18, v20
	v_and_b32_e32 v16, 0xffff0000, v235
	v_mov_b32_e32 v90, 0
	s_cmp_eq_u32 s45, 0x40000
	v_pk_fma_f32 v[108:109], v[16:17], v[18:19], v[108:109]
	v_and_b32_e32 v16, 0xf0f0f0f, v12
	v_mov_b32_e32 v17, 0
	v_lshrrev_b32_e32 v12, 4, v12
	v_dot4c_i32_i8_e32 v17, v16, v36
	v_and_b32_e32 v12, 0xf0f0f0f, v12
	v_dot4c_i32_i8_e32 v17, v12, v37
	v_and_b32_e32 v12, 0xf0f0f0f, v13
	v_mov_b32_e32 v16, 0
	v_dot4c_i32_i8_e32 v16, v12, v38
	v_lshrrev_b32_e32 v12, 4, v13
	v_and_b32_e32 v12, 0xf0f0f0f, v12
	v_dot4c_i32_i8_e32 v16, v12, v39
	v_and_b32_e32 v12, 0xf0f0f0f, v14
	v_dot4c_i32_i8_e32 v17, v12, v32
	v_lshrrev_b32_e32 v12, 4, v14
	v_and_b32_e32 v12, 0xf0f0f0f, v12
	v_dot4c_i32_i8_e32 v17, v12, v33
	v_and_b32_e32 v12, 0xf0f0f0f, v15
	v_dot4c_i32_i8_e32 v16, v12, v34
	v_lshrrev_b32_e32 v12, 4, v15
	v_and_b32_e32 v12, 0xf0f0f0f, v12
	v_dot4c_i32_i8_e32 v16, v12, v35
	v_and_b32_e32 v12, 0xf0f0f0f, v8
	v_mov_b32_e32 v13, 0
	v_lshrrev_b32_e32 v8, 4, v8
	v_dot4c_i32_i8_e32 v13, v12, v36
	v_and_b32_e32 v8, 0xf0f0f0f, v8
	v_dot4c_i32_i8_e32 v13, v8, v37
	v_and_b32_e32 v8, 0xf0f0f0f, v9
	v_mov_b32_e32 v12, 0
	v_dot4c_i32_i8_e32 v12, v8, v38
	v_lshrrev_b32_e32 v8, 4, v9
	v_and_b32_e32 v8, 0xf0f0f0f, v8
	v_dot4c_i32_i8_e32 v12, v8, v39
	v_and_b32_e32 v8, 0xf0f0f0f, v10
	v_dot4c_i32_i8_e32 v13, v8, v32
	v_lshrrev_b32_e32 v8, 4, v10
	v_and_b32_e32 v8, 0xf0f0f0f, v8
	v_dot4c_i32_i8_e32 v13, v8, v33
	v_and_b32_e32 v8, 0xf0f0f0f, v11
	v_dot4c_i32_i8_e32 v12, v8, v34
	v_lshrrev_b32_e32 v8, 4, v11
	v_and_b32_e32 v8, 0xf0f0f0f, v8
	v_dot4c_i32_i8_e32 v12, v8, v35
	v_add_u32_e32 v11, v17, v16
	s_waitcnt vmcnt(8)
	v_and_b32_e32 v9, 0xffff0000, v237
	v_and_b32_e32 v8, 0xffff0000, v236
	v_add_u32_e32 v10, v13, v12
	v_sub_u32_e32 v12, v11, v78
	v_sub_u32_e32 v10, v10, v78
	v_cvt_f32_i32_e32 v11, v10
	v_cvt_f32_i32_e32 v10, v12
	s_waitcnt vmcnt(7)
	v_and_b32_e32 v89, 0xf0f0f0f, v68
	v_lshrrev_b32_e32 v68, 4, v68
	v_dot4c_i32_i8_e32 v90, v89, v36
	v_pk_fma_f32 v[106:107], v[8:9], v[10:11], v[106:107]
	v_and_b32_e32 v8, 0xf0f0f0f, v4
	v_mov_b32_e32 v9, 0
	v_lshrrev_b32_e32 v4, 4, v4
	v_dot4c_i32_i8_e32 v9, v8, v36
	v_and_b32_e32 v4, 0xf0f0f0f, v4
	v_dot4c_i32_i8_e32 v9, v4, v37
	v_and_b32_e32 v4, 0xf0f0f0f, v5
	v_mov_b32_e32 v8, 0
	v_dot4c_i32_i8_e32 v8, v4, v38
	v_lshrrev_b32_e32 v4, 4, v5
	v_and_b32_e32 v4, 0xf0f0f0f, v4
	v_dot4c_i32_i8_e32 v8, v4, v39
	v_and_b32_e32 v4, 0xf0f0f0f, v6
	v_dot4c_i32_i8_e32 v9, v4, v32
	v_lshrrev_b32_e32 v4, 4, v6
	v_and_b32_e32 v4, 0xf0f0f0f, v4
	v_dot4c_i32_i8_e32 v9, v4, v33
	v_and_b32_e32 v4, 0xf0f0f0f, v7
	v_dot4c_i32_i8_e32 v8, v4, v34
	v_lshrrev_b32_e32 v4, 4, v7
	v_and_b32_e32 v4, 0xf0f0f0f, v4
	v_dot4c_i32_i8_e32 v8, v4, v35
	v_and_b32_e32 v4, 0xf0f0f0f, v0
	v_mov_b32_e32 v5, 0
	v_lshrrev_b32_e32 v0, 4, v0
	v_dot4c_i32_i8_e32 v5, v4, v36
	v_and_b32_e32 v0, 0xf0f0f0f, v0
	v_dot4c_i32_i8_e32 v5, v0, v37
	v_and_b32_e32 v0, 0xf0f0f0f, v1
	v_mov_b32_e32 v4, 0
	v_dot4c_i32_i8_e32 v4, v0, v38
	v_lshrrev_b32_e32 v0, 4, v1
	v_and_b32_e32 v0, 0xf0f0f0f, v0
	v_dot4c_i32_i8_e32 v4, v0, v39
	v_and_b32_e32 v0, 0xf0f0f0f, v2
	v_dot4c_i32_i8_e32 v5, v0, v32
	v_lshrrev_b32_e32 v0, 4, v2
	v_and_b32_e32 v0, 0xf0f0f0f, v0
	v_dot4c_i32_i8_e32 v5, v0, v33
	v_and_b32_e32 v0, 0xf0f0f0f, v3
	v_dot4c_i32_i8_e32 v4, v0, v34
	v_lshrrev_b32_e32 v0, 4, v3
	v_and_b32_e32 v0, 0xf0f0f0f, v0
	v_dot4c_i32_i8_e32 v4, v0, v35
	v_add_u32_e32 v3, v9, v8
	v_and_b32_e32 v1, 0xffff0000, v239
	v_and_b32_e32 v0, 0xffff0000, v238
	v_add_u32_e32 v2, v5, v4
	v_sub_u32_e32 v4, v3, v78
	v_sub_u32_e32 v2, v2, v78
	v_cvt_f32_i32_e32 v3, v2
	v_cvt_f32_i32_e32 v2, v4
	v_and_b32_e32 v68, 0xf0f0f0f, v68
	v_dot4c_i32_i8_e32 v90, v68, v37
	v_and_b32_e32 v68, 0xf0f0f0f, v69
	v_pk_fma_f32 v[104:105], v[0:1], v[2:3], v[104:105]
	ds_read_u16 v0, v93 offset:16384
	ds_read_u16 v1, v93 offset:16400
	ds_read_u16 v2, v93 offset:16416
	ds_read_u16 v3, v93 offset:16432
	v_mov_b32_e32 v89, 0
	s_waitcnt lgkmcnt(3)
	v_add_u32_e32 v0, s44, v0
	v_lshl_or_b32 v4, v0, 7, v165
	v_lshl_or_b32 v0, v0, 5, v248
	global_load_dwordx4 v[28:31], v4, s[0:1] sc1
	global_load_dword v184, v0, s[46:47]
	s_waitcnt lgkmcnt(2)
	v_add_u32_e32 v0, s44, v1
	v_dot4c_i32_i8_e32 v89, v68, v38
	v_lshrrev_b32_e32 v68, 4, v69
	v_lshl_or_b32 v1, v0, 7, v165
	v_lshl_or_b32 v0, v0, 5, v248
	v_and_b32_e32 v68, 0xf0f0f0f, v68
	global_load_dwordx4 v[24:27], v1, s[0:1] sc1
	global_load_dword v185, v0, s[46:47]
	s_waitcnt lgkmcnt(1)
	v_add_u32_e32 v0, s44, v2
	v_dot4c_i32_i8_e32 v89, v68, v39
	v_and_b32_e32 v68, 0xf0f0f0f, v70
	v_lshl_or_b32 v1, v0, 7, v165
	v_lshl_or_b32 v0, v0, 5, v248
	v_dot4c_i32_i8_e32 v90, v68, v32
	v_lshrrev_b32_e32 v68, 4, v70
	global_load_dwordx4 v[20:23], v1, s[0:1] sc1
	global_load_dword v186, v0, s[46:47]
	s_waitcnt lgkmcnt(0)
	v_add_u32_e32 v0, s44, v3
	v_and_b32_e32 v68, 0xf0f0f0f, v68
	v_lshl_or_b32 v1, v0, 7, v165
	v_lshl_or_b32 v0, v0, 5, v248
	v_dot4c_i32_i8_e32 v90, v68, v33
	v_and_b32_e32 v68, 0xf0f0f0f, v71
	global_load_dwordx4 v[16:19], v1, s[0:1] sc1
	global_load_dword v187, v0, s[46:47]
	ds_read_u16 v0, v93 offset:16448
	v_dot4c_i32_i8_e32 v89, v68, v34
	v_lshrrev_b32_e32 v68, 4, v71
	v_and_b32_e32 v68, 0xf0f0f0f, v68
	v_dot4c_i32_i8_e32 v89, v68, v35
	s_waitcnt vmcnt(14)
	v_and_b32_e32 v68, 0xf0f0f0f, v64
	v_mov_b32_e32 v69, 0
	v_lshrrev_b32_e32 v64, 4, v64
	v_dot4c_i32_i8_e32 v69, v68, v36
	v_and_b32_e32 v64, 0xf0f0f0f, v64
	v_dot4c_i32_i8_e32 v69, v64, v37
	v_and_b32_e32 v64, 0xf0f0f0f, v65
	v_mov_b32_e32 v68, 0
	s_waitcnt lgkmcnt(0)
; #define P12_ISSUE(c_, i_, h_, CW_, SC_) do { _Pragma("unroll") for (int bb = 0; bb < 8; ++bb) { const unsigned ro = (unsigned)(c_) * 16384u + (unsigned)EL[(i_) * 128 + ((h_) * 8 + bb) * 8 + g8]; \
;         CW_[bb] = *(const v4u*)(U4 + (size_t)(ro * 128u + 16u * (unsigned)k8)); SC_[bb] = USS[(size_t)(ro * 8u + (unsigned)k8)]; } } while (0)
; #define P12_COMP(i_, h_, CW_, SC_) do { _Pragma("unroll") for (int bb = 0; bb < 8; ++bb) { int a0 = 0, a1 = 0; P12_U4(CW_[bb].x, xa.x, xa.y, a0); P12_U4(CW_[bb].y, xa.z, xa.w, a1); P12_U4(CW_[bb].z, xb.x, xb.y, a0); P12_U4(CW_[bb].w, xb.z, xb.w, a1); \
;         psum[(i_)][(h_) * 8 + bb] += __uint_as_float(SC_[bb] << 16) * (float)((a0 + a1) - xo); } } while (0)
; #define P12_BAR() asm volatile("" ::: "memory")
; __device__ __forceinline__ void p12_peer(Frame& F) {
;     ...
;     { v4u cwA[8], cwB[8]; unsigned scA[8], scB[8]; v4u xa, xb; int xo;
;       P12_ISSUE(0, 0, 0, cwA, scA);
; _Pragma("nounroll")
;       for (int c = 0; c < 16; ++c) { const int cn = c + 1 < 16 ? c + 1 : 15;
;           P12_XQ(c, 0); P12_ISSUE(c, 0, 1, cwB, scB); P12_BAR(); P12_COMP(0, 0, cwA, scA); P12_ISSUE(c, 1, 0, cwA, scA); P12_BAR(); P12_COMP(0, 1, cwB, scB);
;           P12_XQ(c, 1); P12_ISSUE(c, 1, 1, cwB, scB); P12_BAR(); P12_COMP(1, 0, cwA, scA); P12_ISSUE(c, 2, 0, cwA, scA); P12_BAR(); P12_COMP(1, 1, cwB, scB);
;           P12_XQ(c, 2); P12_ISSUE(c, 2, 1, cwB, scB); P12_BAR(); P12_COMP(2, 0, cwA, scA); P12_ISSUE(c, 3, 0, cwA, scA); P12_BAR(); P12_COMP(2, 1, cwB, scB);
;           P12_XQ(c, 3); P12_ISSUE(c, 3, 1, cwB, scB); P12_BAR(); P12_COMP(3, 0, cwA, scA); P12_ISSUE(cn, 0, 0, cwA, scA); P12_BAR(); P12_COMP(3, 1, cwB, scB);
	v_add_u32_e32 v0, s44, v0
	v_dot4c_i32_i8_e32 v68, v64, v38
	v_lshrrev_b32_e32 v64, 4, v65
	v_lshl_or_b32 v1, v0, 7, v165
	v_lshl_or_b32 v0, v0, 5, v248
	v_and_b32_e32 v64, 0xf0f0f0f, v64
	global_load_dwordx4 v[12:15], v1, s[0:1] sc1
	global_load_dword v188, v0, s[46:47]
	ds_read_u16 v0, v93 offset:16464
	v_dot4c_i32_i8_e32 v68, v64, v39
	v_and_b32_e32 v64, 0xf0f0f0f, v66
	v_dot4c_i32_i8_e32 v69, v64, v32
	v_lshrrev_b32_e32 v64, 4, v66
	v_and_b32_e32 v64, 0xf0f0f0f, v64
	v_dot4c_i32_i8_e32 v69, v64, v33
	v_and_b32_e32 v64, 0xf0f0f0f, v67
	v_dot4c_i32_i8_e32 v68, v64, v34
	v_lshrrev_b32_e32 v64, 4, v67
	s_waitcnt lgkmcnt(0)
	v_add_u32_e32 v0, s44, v0
	v_and_b32_e32 v64, 0xf0f0f0f, v64
	v_lshl_or_b32 v1, v0, 7, v165
	v_lshl_or_b32 v0, v0, 5, v248
	v_dot4c_i32_i8_e32 v68, v64, v35
	global_load_dwordx4 v[8:11], v1, s[0:1] sc1
	global_load_dword v189, v0, s[46:47]
	ds_read_u16 v0, v93 offset:16480
	v_add_u32_e32 v66, v90, v89
	v_sub_u32_e32 v67, v68, v78
	v_add_u32_e32 v67, v67, v69
	v_sub_u32_e32 v66, v66, v78
	v_cvt_f32_i32_e32 v66, v66
	v_cvt_f32_i32_e32 v67, v67
	s_waitcnt lgkmcnt(0)
	v_add_u32_e32 v0, s44, v0
	s_waitcnt vmcnt(12)
	v_and_b32_e32 v65, 0xffff0000, v241
	v_and_b32_e32 v64, 0xffff0000, v240
	v_lshl_or_b32 v1, v0, 7, v165
	v_lshl_or_b32 v0, v0, 5, v248
	v_pk_fma_f32 v[102:103], v[64:65], v[66:67], v[102:103]
	v_and_b32_e32 v64, 0xf0f0f0f, v60
	v_mov_b32_e32 v65, 0
	v_lshrrev_b32_e32 v60, 4, v60
	global_load_dwordx4 v[4:7], v1, s[0:1] sc1
	global_load_dword v190, v0, s[46:47]
	ds_read_u16 v0, v93 offset:16496
	v_dot4c_i32_i8_e32 v65, v64, v36
	v_and_b32_e32 v60, 0xf0f0f0f, v60
	v_dot4c_i32_i8_e32 v65, v60, v37
	v_and_b32_e32 v60, 0xf0f0f0f, v61
	v_mov_b32_e32 v64, 0
	v_dot4c_i32_i8_e32 v64, v60, v38
	v_lshrrev_b32_e32 v60, 4, v61
	v_and_b32_e32 v60, 0xf0f0f0f, v60
	v_dot4c_i32_i8_e32 v64, v60, v39
	v_and_b32_e32 v60, 0xf0f0f0f, v62
	s_waitcnt lgkmcnt(0)
	v_add_u32_e32 v88, s44, v0
	v_dot4c_i32_i8_e32 v65, v60, v32
	v_lshrrev_b32_e32 v60, 4, v62
	v_lshl_or_b32 v0, v88, 7, v165
	v_lshl_or_b32 v88, v88, 5, v248
	v_and_b32_e32 v60, 0xf0f0f0f, v60
	global_load_dwordx4 v[0:3], v0, s[0:1] sc1
	v_dot4c_i32_i8_e32 v65, v60, v33
	global_load_dword v191, v88, s[46:47]
	v_and_b32_e32 v60, 0xf0f0f0f, v63
	v_dot4c_i32_i8_e32 v64, v60, v34
	v_lshrrev_b32_e32 v60, 4, v63
	v_and_b32_e32 v60, 0xf0f0f0f, v60
	v_dot4c_i32_i8_e32 v64, v60, v35
	v_and_b32_e32 v60, 0xf0f0f0f, v56
	v_mov_b32_e32 v61, 0
	v_lshrrev_b32_e32 v56, 4, v56
	v_dot4c_i32_i8_e32 v61, v60, v36
	v_and_b32_e32 v56, 0xf0f0f0f, v56
	v_dot4c_i32_i8_e32 v61, v56, v37
	v_and_b32_e32 v56, 0xf0f0f0f, v57
	v_mov_b32_e32 v60, 0
	v_dot4c_i32_i8_e32 v60, v56, v38
	v_lshrrev_b32_e32 v56, 4, v57
	v_and_b32_e32 v56, 0xf0f0f0f, v56
	v_dot4c_i32_i8_e32 v60, v56, v39
	v_and_b32_e32 v56, 0xf0f0f0f, v58
	v_dot4c_i32_i8_e32 v61, v56, v32
	v_lshrrev_b32_e32 v56, 4, v58
	v_and_b32_e32 v56, 0xf0f0f0f, v56
	v_dot4c_i32_i8_e32 v61, v56, v33
	v_and_b32_e32 v56, 0xf0f0f0f, v59
	v_dot4c_i32_i8_e32 v60, v56, v34
	v_lshrrev_b32_e32 v56, 4, v59
	v_and_b32_e32 v56, 0xf0f0f0f, v56
	v_dot4c_i32_i8_e32 v60, v56, v35
	v_sub_u32_e32 v59, v64, v78
	s_waitcnt vmcnt(16)
	v_and_b32_e32 v57, 0xffff0000, v243
	v_and_b32_e32 v56, 0xffff0000, v242
	v_sub_u32_e32 v58, v60, v78
	v_add_u32_e32 v60, v59, v65
	v_add_u32_e32 v58, v58, v61
	v_cvt_f32_i32_e32 v59, v58
	v_cvt_f32_i32_e32 v58, v60
	s_mov_b32 s44, s45
	v_pk_fma_f32 v[100:101], v[56:57], v[58:59], v[100:101]
	v_and_b32_e32 v56, 0xf0f0f0f, v52
	v_mov_b32_e32 v57, 0
	v_lshrrev_b32_e32 v52, 4, v52
	v_dot4c_i32_i8_e32 v57, v56, v36
	v_and_b32_e32 v52, 0xf0f0f0f, v52
	v_dot4c_i32_i8_e32 v57, v52, v37
	v_and_b32_e32 v52, 0xf0f0f0f, v53
	v_mov_b32_e32 v56, 0
	v_dot4c_i32_i8_e32 v56, v52, v38
	v_lshrrev_b32_e32 v52, 4, v53
	v_and_b32_e32 v52, 0xf0f0f0f, v52
	v_dot4c_i32_i8_e32 v56, v52, v39
	v_and_b32_e32 v52, 0xf0f0f0f, v54
	v_dot4c_i32_i8_e32 v57, v52, v32
	v_lshrrev_b32_e32 v52, 4, v54
	v_and_b32_e32 v52, 0xf0f0f0f, v52
	v_dot4c_i32_i8_e32 v57, v52, v33
	v_and_b32_e32 v52, 0xf0f0f0f, v55
	v_dot4c_i32_i8_e32 v56, v52, v34
	v_lshrrev_b32_e32 v52, 4, v55
	v_and_b32_e32 v52, 0xf0f0f0f, v52
	v_dot4c_i32_i8_e32 v56, v52, v35
	v_and_b32_e32 v52, 0xf0f0f0f, v48
	v_mov_b32_e32 v53, 0
	v_lshrrev_b32_e32 v48, 4, v48
	v_dot4c_i32_i8_e32 v53, v52, v36
	v_and_b32_e32 v48, 0xf0f0f0f, v48
	v_dot4c_i32_i8_e32 v53, v48, v37
	v_and_b32_e32 v48, 0xf0f0f0f, v49
	v_mov_b32_e32 v52, 0
	v_dot4c_i32_i8_e32 v52, v48, v38
	v_lshrrev_b32_e32 v48, 4, v49
	v_and_b32_e32 v48, 0xf0f0f0f, v48
	v_dot4c_i32_i8_e32 v52, v48, v39
	v_and_b32_e32 v48, 0xf0f0f0f, v50
	v_dot4c_i32_i8_e32 v53, v48, v32
	v_lshrrev_b32_e32 v48, 4, v50
	v_and_b32_e32 v48, 0xf0f0f0f, v48
	v_dot4c_i32_i8_e32 v53, v48, v33
	v_and_b32_e32 v48, 0xf0f0f0f, v51
	v_dot4c_i32_i8_e32 v52, v48, v34
	v_lshrrev_b32_e32 v48, 4, v51
	v_and_b32_e32 v48, 0xf0f0f0f, v48
	v_dot4c_i32_i8_e32 v52, v48, v35
	v_sub_u32_e32 v51, v56, v78
	s_waitcnt vmcnt(16)
; #define P12_ISSUE(c_, i_, h_, CW_, SC_) do { _Pragma("unroll") for (int bb = 0; bb < 8; ++bb) { const unsigned ro = (unsigned)(c_) * 16384u + (unsigned)EL[(i_) * 128 + ((h_) * 8 + bb) * 8 + g8]; \
;         CW_[bb] = *(const v4u*)(U4 + (size_t)(ro * 128u + 16u * (unsigned)k8)); SC_[bb] = USS[(size_t)(ro * 8u + (unsigned)k8)]; } } while (0)
; #define P12_COMP(i_, h_, CW_, SC_) do { _Pragma("unroll") for (int bb = 0; bb < 8; ++bb) { int a0 = 0, a1 = 0; P12_U4(CW_[bb].x, xa.x, xa.y, a0); P12_U4(CW_[bb].y, xa.z, xa.w, a1); P12_U4(CW_[bb].z, xb.x, xb.y, a0); P12_U4(CW_[bb].w, xb.z, xb.w, a1); \
;         psum[(i_)][(h_) * 8 + bb] += __uint_as_float(SC_[bb] << 16) * (float)((a0 + a1) - xo); } } while (0)
; #define P12_BAR() asm volatile("" ::: "memory")
; __device__ __forceinline__ void p12_peer(Frame& F) {
;     ...
;     { v4u cwA[8], cwB[8]; unsigned scA[8], scB[8]; v4u xa, xb; int xo;
;       P12_ISSUE(0, 0, 0, cwA, scA);
; _Pragma("nounroll")
;       for (int c = 0; c < 16; ++c) { const int cn = c + 1 < 16 ? c + 1 : 15;
;           P12_XQ(c, 0); P12_ISSUE(c, 0, 1, cwB, scB); P12_BAR(); P12_COMP(0, 0, cwA, scA); P12_ISSUE(c, 1, 0, cwA, scA); P12_BAR(); P12_COMP(0, 1, cwB, scB);
;           P12_XQ(c, 1); P12_ISSUE(c, 1, 1, cwB, scB); P12_BAR(); P12_COMP(1, 0, cwA, scA); P12_ISSUE(c, 2, 0, cwA, scA); P12_BAR(); P12_COMP(1, 1, cwB, scB);
;           P12_XQ(c, 2); P12_ISSUE(c, 2, 1, cwB, scB); P12_BAR(); P12_COMP(2, 0, cwA, scA); P12_ISSUE(c, 3, 0, cwA, scA); P12_BAR(); P12_COMP(2, 1, cwB, scB);
;           P12_XQ(c, 3); P12_ISSUE(c, 3, 1, cwB, scB); P12_BAR(); P12_COMP(3, 0, cwA, scA); P12_ISSUE(cn, 0, 0, cwA, scA); P12_BAR(); P12_COMP(3, 1, cwB, scB);
	v_and_b32_e32 v49, 0xffff0000, v245
	v_and_b32_e32 v48, 0xffff0000, v244
	v_sub_u32_e32 v50, v52, v78
	v_add_u32_e32 v52, v51, v57
	v_add_u32_e32 v50, v50, v53
	v_cvt_f32_i32_e32 v51, v50
	v_cvt_f32_i32_e32 v50, v52
	v_pk_fma_f32 v[98:99], v[48:49], v[50:51], v[98:99]
	v_and_b32_e32 v48, 0xf0f0f0f, v44
	v_mov_b32_e32 v49, 0
	v_lshrrev_b32_e32 v44, 4, v44
	v_dot4c_i32_i8_e32 v49, v48, v36
	v_and_b32_e32 v44, 0xf0f0f0f, v44
	v_dot4c_i32_i8_e32 v49, v44, v37
	v_and_b32_e32 v44, 0xf0f0f0f, v45
	v_mov_b32_e32 v48, 0
	v_dot4c_i32_i8_e32 v48, v44, v38
	v_lshrrev_b32_e32 v44, 4, v45
	v_and_b32_e32 v44, 0xf0f0f0f, v44
	v_dot4c_i32_i8_e32 v48, v44, v39
	v_and_b32_e32 v44, 0xf0f0f0f, v46
	v_dot4c_i32_i8_e32 v49, v44, v32
	v_lshrrev_b32_e32 v44, 4, v46
	v_and_b32_e32 v44, 0xf0f0f0f, v44
	v_dot4c_i32_i8_e32 v49, v44, v33
	v_and_b32_e32 v44, 0xf0f0f0f, v47
	v_dot4c_i32_i8_e32 v48, v44, v34
	v_lshrrev_b32_e32 v44, 4, v47
	v_and_b32_e32 v44, 0xf0f0f0f, v44
	v_dot4c_i32_i8_e32 v48, v44, v35
	v_and_b32_e32 v44, 0xf0f0f0f, v40
	v_mov_b32_e32 v45, 0
	v_dot4c_i32_i8_e32 v45, v44, v36
	v_lshrrev_b32_e32 v36, 4, v40
	v_and_b32_e32 v36, 0xf0f0f0f, v36
	v_dot4c_i32_i8_e32 v45, v36, v37
	v_and_b32_e32 v36, 0xf0f0f0f, v41
	v_mov_b32_e32 v37, 0
	v_dot4c_i32_i8_e32 v37, v36, v38
	v_lshrrev_b32_e32 v36, 4, v41
	v_and_b32_e32 v36, 0xf0f0f0f, v36
	v_dot4c_i32_i8_e32 v37, v36, v39
	v_and_b32_e32 v36, 0xf0f0f0f, v42
	v_dot4c_i32_i8_e32 v45, v36, v32
	v_lshrrev_b32_e32 v32, 4, v42
	v_and_b32_e32 v32, 0xf0f0f0f, v32
	v_dot4c_i32_i8_e32 v45, v32, v33
	v_and_b32_e32 v32, 0xf0f0f0f, v43
	v_dot4c_i32_i8_e32 v37, v32, v34
	v_lshrrev_b32_e32 v32, 4, v43
	v_and_b32_e32 v32, 0xf0f0f0f, v32
	v_dot4c_i32_i8_e32 v37, v32, v35
	v_sub_u32_e32 v35, v48, v78
	v_add_u32_e32 v36, v35, v49
	s_waitcnt vmcnt(16)
	v_and_b32_e32 v33, 0xffff0000, v247
	v_sub_u32_e32 v34, v37, v78
	v_add_u32_e32 v34, v34, v45
	v_cvt_f32_i32_e32 v35, v34
	v_cvt_f32_i32_e32 v34, v36
	v_and_b32_e32 v32, 0xffff0000, v246
	s_waitcnt vmcnt(0)
	v_perm_b32 v40, v190, v191, s43
	v_perm_b32 v41, v188, v189, s43
	v_pk_fma_f32 v[96:97], v[32:33], v[34:35], v[96:97]
	v_perm_b32 v42, v186, v187, s43
	v_perm_b32 v43, v184, v185, s43
	s_cbranch_scc0 .LBB0_3272
; #define LDS_WAIT() asm volatile("s_waitcnt lgkmcnt(0)" ::: "memory")
; __device__ __forceinline__ float wave_sum(float v) { v = dpp_add16(v); return (rdlane(v, 0) + rdlane(v, 16)) + (rdlane(v, 32) + rdlane(v, 48)); }
; __device__ __forceinline__ float wave_max(float v) { v = dpp_max16(v); return fmaxf(fmaxf(rdlane(v, 0), rdlane(v, 16)), fmaxf(rdlane(v, 32), rdlane(v, 48))); }
; __device__ __forceinline__ void p12_peer(Frame& F) {
;     ...
;         mxa = wave_max(mxa); const float inv = mxa > 0.f ? 127.0f / mxa : 0.f;
;         const float rsn = 1.0f / sqrtf(wave_sum(PSQ[(size_t)t * 64 + F.lane]) * (1.f / D_) + 1e-6f);
;         sx[i] = mxa * rsn * (1.0f / 127.0f);
;     ...
;     asm volatile("" ::: "memory"); LDS_WAIT();
; #pragma unroll
;     for (int i = 0; i < 4; ++i) { const int t = F.gw + i * F.NGW;
; #pragma unroll
;         for (int b = 0; b < 16; ++b) { float d = psum[i][b];
;             d += __builtin_bit_cast(float, __builtin_amdgcn_update_dpp(0, __builtin_bit_cast(int, d), 0xB1, 0xF, 0xF, false));
;             d += __builtin_bit_cast(float, __builtin_amdgcn_update_dpp(0, __builtin_bit_cast(int, d), 0x4E, 0xF, 0xF, false));
;             d += __builtin_bit_cast(float, __builtin_amdgcn_update_dpp(0, __builtin_bit_cast(int, d), 0x141, 0xF, 0xF, false));
;             const int idx = b * 8 + g8; const float w = PGT[(size_t)t * 128 + idx] * gelu_erf(sx[i] * d) * VSC[EL[i * 128 + idx]];
;             if (k8 == 0) WL[i * 128 + idx] = w; } }
	v_mov_b32_e32 v0, s41
	v_mov_b32_e32 v1, s42
	v_add_f32_e32 v0, s39, v0
	v_add_f32_e32 v1, s40, v1
	v_add_f32_e32 v0, v0, v1
	v_mov_b32_e32 v1, 0x358637bd
	v_fmac_f32_e32 v1, 0x39800000, v0
	s_mov_b32 s0, 0xf800000
	v_mul_f32_e32 v0, 0x4f800000, v1
	v_cmp_gt_f32_e32 vcc, s0, v1
	s_add_u32 s43, s68, 0x1200000
	s_addc_u32 s44, s69, 0
	v_cndmask_b32_e32 v0, v1, v0, vcc
	v_sqrt_f32_e32 v1, v0
	s_add_u32 s18, s68, 0xf000000
	s_addc_u32 s19, s69, 0
	v_add_u32_e32 v2, -1, v1
	v_fma_f32 v3, -v2, v1, v0
	v_cmp_ge_f32_e64 s[0:1], 0, v3
	v_add_u32_e32 v3, 1, v1
	s_add_u32 s2, s43, s2
	v_cndmask_b32_e64 v2, v1, v2, s[0:1]
	v_fma_f32 v1, -v3, v1, v0
	v_cmp_lt_f32_e64 s[0:1], 0, v1
	s_waitcnt lgkmcnt(0)
	s_addc_u32 s3, s44, s3
	v_ashrrev_i32_e32 v95, 31, v94
	v_cndmask_b32_e64 v1, v2, v3, s[0:1]
	v_mul_f32_e32 v2, 0x37800000, v1
	v_cndmask_b32_e32 v1, v1, v2, vcc
	v_mov_b32_e32 v2, 0x260
	v_cmp_class_f32_e32 vcc, v0, v2
	s_nop 1
	v_cndmask_b32_e32 v2, v1, v0, vcc
	v_div_scale_f32 v3, s[0:1], v2, v2, 1.0
	v_rcp_f32_e32 v4, v3
	v_lshl_add_u64 v[0:1], v[94:95], 2, s[2:3]
	ds_read_u16 v20, v93 offset:16384
	ds_read_u16 v21, v93 offset:16400
	ds_read_u16 v22, v93 offset:16416
	ds_read_u16 v23, v93 offset:16432
	ds_read_u16 v24, v93 offset:16448
	ds_read_u16 v25, v93 offset:16464
	ds_read_u16 v26, v93 offset:16480
	ds_read_u16 v27, v93 offset:16496
	s_waitcnt lgkmcnt(0)
	ds_read_u16 v28, v93 offset:16512
	ds_read_u16 v29, v93 offset:16528
	ds_read_u16 v30, v93 offset:16544
	ds_read_u16 v31, v93 offset:16560
	ds_read_u16 v32, v93 offset:16576
	ds_read_u16 v33, v93 offset:16592
	ds_read_u16 v34, v93 offset:16608
	ds_read_u16 v35, v93 offset:16624
	s_waitcnt lgkmcnt(0)
	v_lshlrev_b32_e32 v20, 2, v20
	v_lshlrev_b32_e32 v21, 2, v21
	v_lshlrev_b32_e32 v22, 2, v22
	v_lshlrev_b32_e32 v23, 2, v23
	v_lshlrev_b32_e32 v24, 2, v24
	v_lshlrev_b32_e32 v25, 2, v25
	v_lshlrev_b32_e32 v26, 2, v26
	v_lshlrev_b32_e32 v27, 2, v27
	v_lshlrev_b32_e32 v28, 2, v28
	v_lshlrev_b32_e32 v29, 2, v29
	v_lshlrev_b32_e32 v30, 2, v30
	v_lshlrev_b32_e32 v31, 2, v31
	v_lshlrev_b32_e32 v32, 2, v32
	v_lshlrev_b32_e32 v33, 2, v33
	v_lshlrev_b32_e32 v34, 2, v34
	v_lshlrev_b32_e32 v35, 2, v35
	global_load_dword v40, v[0:1], off offset:0
	global_load_dword v60, v20, s[18:19]
	global_load_dword v41, v[0:1], off offset:32
	global_load_dword v61, v21, s[18:19]
	global_load_dword v42, v[0:1], off offset:64
	global_load_dword v62, v22, s[18:19]
	global_load_dword v43, v[0:1], off offset:96
	global_load_dword v63, v23, s[18:19]
	global_load_dword v44, v[0:1], off offset:128
	global_load_dword v64, v24, s[18:19]
	global_load_dword v45, v[0:1], off offset:160
	global_load_dword v65, v25, s[18:19]
	global_load_dword v46, v[0:1], off offset:192
	global_load_dword v66, v26, s[18:19]
	global_load_dword v47, v[0:1], off offset:224
	global_load_dword v67, v27, s[18:19]
	global_load_dword v48, v[0:1], off offset:256
	global_load_dword v68, v28, s[18:19]
	global_load_dword v49, v[0:1], off offset:288
	global_load_dword v69, v29, s[18:19]
	global_load_dword v50, v[0:1], off offset:320
	global_load_dword v70, v30, s[18:19]
	global_load_dword v51, v[0:1], off offset:352
	global_load_dword v71, v31, s[18:19]
	global_load_dword v52, v[0:1], off offset:384
	global_load_dword v72, v32, s[18:19]
	global_load_dword v53, v[0:1], off offset:416
	global_load_dword v73, v33, s[18:19]
	global_load_dword v54, v[0:1], off offset:448
	global_load_dword v74, v34, s[18:19]
	global_load_dword v55, v[0:1], off offset:480
	global_load_dword v75, v35, s[18:19]
	s_waitcnt vmcnt(0)
	v_cmp_eq_u32_e64 s[0:1], 0, v164
	v_fma_f32 v5, -v3, v4, 1.0
	v_fmac_f32_e32 v4, v5, v4
	v_div_scale_f32 v5, vcc, 1.0, v2, 1.0
	v_mul_f32_e32 v6, v5, v4
	v_fma_f32 v7, -v3, v6, v5
	v_fmac_f32_e32 v6, v7, v4
	v_fma_f32 v3, -v3, v6, v5
	v_div_fmas_f32 v3, v3, v4, v6
	v_div_fixup_f32 v2, v3, v2, 1.0
	v_add_f32_dpp v5, v159, v159 quad_perm:[1,0,3,2] row_mask:0xf bank_mask:0xf bound_ctrl:1
	v_mul_f32_e32 v3, v163, v2
	v_mov_b32_e32 v6, 0
	v_add_f32_dpp v5, v5, v5 quad_perm:[2,3,0,1] row_mask:0xf bank_mask:0xf bound_ctrl:1
	v_mov_b32_e32 v4, 0
	v_lshl_add_u32 v2, v94, 2, s20
	v_mul_f32_e32 v3, 0x3c010204, v3
	v_mov_b32_dpp v6, v5 row_half_mirror row_mask:0xf bank_mask:0xf
	s_and_saveexec_b64 s[2:3], s[0:1]
	s_cbranch_execz .LBB0_3275
	v_add_f32_e32 v5, v5, v6
	v_mul_f32_e32 v5, v3, v5
	s_mov_b32 s39, 0x3e6d3388
	v_mul_f32_e32 v6, v5, v5
	s_waitcnt lgkmcnt(0)
	v_fma_f32 v7, |v5|, s39, 1.0
	v_rcp_f32_e32 v7, v7
	v_mov_b32_e32 v10, 0xbf3a00e3
	v_mul_f32_e32 v6, 0xbf38aa3b, v6
	v_exp_f32_e32 v6, v6
	v_fmac_f32_e32 v10, 0x3f07dc22, v7
	v_fmaak_f32 v10, v7, v10, 0x3f35f0e3
	v_fmaak_f32 v10, v7, v10, 0xbe11a98e
	v_fmaak_f32 v10, v7, v10, 0x3e027906
	v_mul_f32_e32 v7, v7, v10
	v_mul_f32_e32 v6, v6, v7
	v_mul_f32_e32 v7, v5, v6
	v_fma_f32 v6, -v5, v6, v5
	v_cmp_gt_f32_e32 vcc, 0, v5
	s_nop 1
	v_cndmask_b32_e32 v5, v6, v7, vcc
	s_waitcnt vmcnt(1)
	v_mul_f32_e32 v5, v5, v40
	s_waitcnt vmcnt(0)
	v_mul_f32_e32 v5, v5, v60
	ds_write_b32 v2, v5
